# non-temporal hint on the in-projection output stores, on the single-use gate loads of the merged GEMM and on the expert-combine norm loads (final norm loads/stores too); attention rebalance + static p
# speedup vs baseline: 1.0166x; 1.0166x over previous
.LBB0_42:
	s_ashr_i32 s43, s42, 31
	s_add_i32 s48, s42, 0x800
	s_lshl_b64 s[0:1], s[42:43], 11
	s_ashr_i32 s49, s48, 31
	s_add_i32 s46, s42, 0x1000
	v_lshl_add_u64 v[64:65], v[4:5], 0, s[0:1]
	s_lshl_b64 s[0:1], s[48:49], 11
	s_ashr_i32 s47, s46, 31
	s_add_i32 s44, s42, 0x1800
	v_lshl_add_u64 v[44:45], v[4:5], 0, s[0:1]
	s_lshl_b64 s[0:1], s[46:47], 11
	s_ashr_i32 s45, s44, 31
	v_lshl_add_u64 v[30:31], v[4:5], 0, s[0:1]
	s_lshl_b64 s[0:1], s[44:45], 11
	v_lshl_add_u64 v[8:9], v[4:5], 0, s[0:1]
	s_lshl_b64 s[0:1], s[42:43], 6
	v_lshl_add_u64 v[32:33], v[0:1], 0, s[0:1]
	s_lshl_b64 s[0:1], s[48:49], 6
	global_load_dwordx4 v[10:13], v[64:65], off nt
	global_load_dwordx4 v[14:17], v[64:65], off offset:1024 nt
	global_load_dwordx4 v[18:21], v[44:45], off nt
	global_load_dwordx4 v[22:25], v[44:45], off offset:1024 nt
	global_load_dwordx4 v[26:29], v[30:31], off nt
	global_load_dwordx4 v[82:85], v[30:31], off offset:1024 nt
	global_load_dwordx4 v[86:89], v[8:9], off nt
	global_load_dwordx4 v[90:93], v[8:9], off offset:1024 nt
	s_lshl_b64 s[4:5], s[46:47], 6
	global_load_dword v100, v[32:33], off nt
	v_lshl_add_u64 v[32:33], v[0:1], 0, s[0:1]
	s_lshl_b64 s[12:13], s[44:45], 6
	global_load_dword v101, v[32:33], off nt
	v_lshl_add_u64 v[32:33], v[0:1], 0, s[4:5]
	global_load_dword v102, v[32:33], off nt
	v_lshl_add_u64 v[32:33], v[0:1], 0, s[12:13]
	global_load_dword v103, v[32:33], off nt
	s_waitcnt vmcnt(11)
	v_lshlrev_b32_e32 v80, 16, v10
	v_and_b32_e32 v81, 0xffff0000, v10
	v_lshlrev_b32_e32 v78, 16, v11
	v_and_b32_e32 v79, 0xffff0000, v11
	v_lshlrev_b32_e32 v76, 16, v12
	v_and_b32_e32 v77, 0xffff0000, v12
	s_waitcnt vmcnt(3)
	v_cmp_lt_i32_e32 vcc, -1, v100
	s_and_b32 s10, vcc_lo, 0xffff
	v_lshlrev_b32_e32 v74, 16, v13
	s_waitcnt vmcnt(2)
	v_cmp_lt_i32_e32 vcc, -1, v101
	s_and_b32 s12, vcc_lo, 0xffff
	s_waitcnt vmcnt(1)
	v_cmp_lt_i32_e32 vcc, -1, v102
	s_and_b32 s13, vcc_lo, 0xffff
	s_waitcnt vmcnt(0)
	v_cmp_lt_i32_e32 vcc, -1, v103
	s_or_b32 s0, s12, s10
	s_and_b32 s14, vcc_lo, 0xffff
	s_or_b32 s0, s0, s13
	s_or_b32 s0, s0, s14
	v_and_b32_e32 v75, 0xffff0000, v13
	v_lshlrev_b32_e32 v72, 16, v14
	v_and_b32_e32 v73, 0xffff0000, v14
	v_lshlrev_b32_e32 v70, 16, v15
	v_and_b32_e32 v71, 0xffff0000, v15
	v_lshlrev_b32_e32 v68, 16, v16
	v_and_b32_e32 v69, 0xffff0000, v16
	v_lshlrev_b32_e32 v66, 16, v17
	v_and_b32_e32 v67, 0xffff0000, v17
	v_lshlrev_b32_e32 v62, 16, v18
	v_and_b32_e32 v63, 0xffff0000, v18
	v_lshlrev_b32_e32 v60, 16, v19
	v_and_b32_e32 v61, 0xffff0000, v19
	v_lshlrev_b32_e32 v58, 16, v20
	v_and_b32_e32 v59, 0xffff0000, v20
	v_lshlrev_b32_e32 v56, 16, v21
	v_and_b32_e32 v57, 0xffff0000, v21
	v_lshlrev_b32_e32 v54, 16, v22
	v_and_b32_e32 v55, 0xffff0000, v22
	v_lshlrev_b32_e32 v52, 16, v23
	v_and_b32_e32 v53, 0xffff0000, v23
	v_lshlrev_b32_e32 v50, 16, v24
	v_and_b32_e32 v51, 0xffff0000, v24
	v_lshlrev_b32_e32 v46, 16, v25
	v_and_b32_e32 v47, 0xffff0000, v25
	v_lshlrev_b32_e32 v42, 16, v26
	v_and_b32_e32 v43, 0xffff0000, v26
	v_lshlrev_b32_e32 v40, 16, v27
	v_and_b32_e32 v41, 0xffff0000, v27
	v_lshlrev_b32_e32 v38, 16, v28
	v_and_b32_e32 v39, 0xffff0000, v28
	v_lshlrev_b32_e32 v36, 16, v29
	v_and_b32_e32 v37, 0xffff0000, v29
	v_lshlrev_b32_e32 v32, 16, v82
	v_and_b32_e32 v33, 0xffff0000, v82
	v_lshlrev_b32_e32 v34, 16, v83
	v_and_b32_e32 v35, 0xffff0000, v83
	v_lshlrev_b32_e32 v28, 16, v84
	v_and_b32_e32 v29, 0xffff0000, v84
	v_lshlrev_b32_e32 v26, 16, v85
	v_and_b32_e32 v27, 0xffff0000, v85
	v_lshlrev_b32_e32 v24, 16, v86
	v_and_b32_e32 v25, 0xffff0000, v86
	v_lshlrev_b32_e32 v22, 16, v87
	v_and_b32_e32 v23, 0xffff0000, v87
	v_lshlrev_b32_e32 v20, 16, v88
	v_and_b32_e32 v21, 0xffff0000, v88
	v_lshlrev_b32_e32 v18, 16, v89
	v_and_b32_e32 v19, 0xffff0000, v89
	v_lshlrev_b32_e32 v16, 16, v90
	v_and_b32_e32 v17, 0xffff0000, v90
	v_lshlrev_b32_e32 v14, 16, v91
	v_and_b32_e32 v15, 0xffff0000, v91
	v_lshlrev_b32_e32 v12, 16, v92
	v_and_b32_e32 v13, 0xffff0000, v92
	v_lshlrev_b32_e32 v10, 16, v93
	s_cmp_eq_u32 s0, 0
	v_and_b32_e32 v11, 0xffff0000, v93
	s_cbranch_scc1 .LBB0_54
	s_ashr_i32 s16, s42, 11
	s_ashr_i32 s18, s48, 11
	s_ashr_i32 s19, s46, 11
	s_ashr_i32 s20, s44, 11
	s_branch .LBB0_45
.LBB0_44:
	s_add_i32 s5, s13, -1
	s_and_b32 s13, s5, s13
	s_add_i32 s5, s12, -1
	s_and_b32 s12, s5, s12
	s_add_i32 s5, s10, -1
	s_and_b32 s10, s5, s10
	s_lshl_b32 s1, s1, 5
	s_and_b64 s[30:31], exec, s[52:53]
	s_cselect_b32 s1, 0, s1
	s_add_i32 s30, s1, s20
	s_ashr_i32 s31, s30, 31
	s_lshl_b64 s[30:31], s[30:31], 18
	s_add_u32 s1, s8, s30
	s_addc_u32 s5, s9, s31
	s_add_u32 s30, s1, s50
	s_addc_u32 s31, s5, s51
	v_lshl_add_u64 v[104:105], s[30:31], 0, v[2:3]
	global_load_dwordx2 v[106:107], v[104:105], off nt
	s_nop 0
	global_load_dwordx2 v[104:105], v[104:105], off offset:512 nt
	s_waitcnt vmcnt(7)
	v_cvt_pk_f32_fp8_e32 v[108:109], v92
	v_cvt_pk_f32_fp8_sdwa v[110:111], v92 src0_sel:WORD_1
	v_cvt_pk_f32_fp8_e32 v[112:113], v93
	v_cvt_pk_f32_fp8_sdwa v[92:93], v93 src0_sel:WORD_1
	v_pk_fma_f32 v[80:81], s[36:37], v[108:109], v[80:81] op_sel_hi:[0,1,1]
	v_pk_fma_f32 v[78:79], s[36:37], v[110:111], v[78:79] op_sel_hi:[0,1,1]
	s_waitcnt vmcnt(6)
	v_cvt_pk_f32_fp8_sdwa v[108:109], v88 src0_sel:WORD_1
	v_pk_fma_f32 v[74:75], s[36:37], v[92:93], v[74:75] op_sel_hi:[0,1,1]
	v_cvt_pk_f32_fp8_e32 v[92:93], v88
	v_cvt_pk_f32_fp8_e32 v[110:111], v89
	v_cvt_pk_f32_fp8_sdwa v[88:89], v89 src0_sel:WORD_1
	v_pk_fma_f32 v[70:71], s[36:37], v[108:109], v[70:71] op_sel_hi:[0,1,1]
	v_pk_fma_f32 v[72:73], s[36:37], v[92:93], v[72:73] op_sel_hi:[0,1,1]
	s_waitcnt vmcnt(5)
	v_cvt_pk_f32_fp8_sdwa v[92:93], v90 src0_sel:WORD_1
	v_pk_fma_f32 v[66:67], s[36:37], v[88:89], v[66:67] op_sel_hi:[0,1,1]
	v_cvt_pk_f32_fp8_e32 v[88:89], v90
	v_cvt_pk_f32_fp8_e32 v[108:109], v91
	v_cvt_pk_f32_fp8_sdwa v[90:91], v91 src0_sel:WORD_1
	v_pk_fma_f32 v[60:61], s[22:23], v[92:93], v[60:61] op_sel_hi:[0,1,1]
	v_pk_fma_f32 v[62:63], s[22:23], v[88:89], v[62:63] op_sel_hi:[0,1,1]
	s_waitcnt vmcnt(4)
	v_cvt_pk_f32_fp8_e32 v[88:89], v84
	v_pk_fma_f32 v[56:57], s[22:23], v[90:91], v[56:57] op_sel_hi:[0,1,1]
	v_cvt_pk_f32_fp8_sdwa v[90:91], v84 src0_sel:WORD_1
	v_cvt_pk_f32_fp8_e32 v[92:93], v85
	v_cvt_pk_f32_fp8_sdwa v[84:85], v85 src0_sel:WORD_1
	v_pk_fma_f32 v[54:55], s[22:23], v[88:89], v[54:55] op_sel_hi:[0,1,1]
	v_pk_fma_f32 v[52:53], s[22:23], v[90:91], v[52:53] op_sel_hi:[0,1,1]
	s_waitcnt vmcnt(3)
	v_cvt_pk_f32_fp8_sdwa v[88:89], v86 src0_sel:WORD_1
	v_pk_fma_f32 v[46:47], s[22:23], v[84:85], v[46:47] op_sel_hi:[0,1,1]
	v_cvt_pk_f32_fp8_e32 v[84:85], v86
	v_cvt_pk_f32_fp8_e32 v[90:91], v87
	v_cvt_pk_f32_fp8_sdwa v[86:87], v87 src0_sel:WORD_1
	v_pk_fma_f32 v[40:41], s[4:5], v[88:89], v[40:41] op_sel_hi:[0,1,1]
	v_pk_fma_f32 v[42:43], s[4:5], v[84:85], v[42:43] op_sel_hi:[0,1,1]
	s_waitcnt vmcnt(2)
	v_cvt_pk_f32_fp8_e32 v[84:85], v82
	v_pk_fma_f32 v[36:37], s[4:5], v[86:87], v[36:37] op_sel_hi:[0,1,1]
	v_cvt_pk_f32_fp8_sdwa v[86:87], v82 src0_sel:WORD_1
	v_cvt_pk_f32_fp8_e32 v[88:89], v83
	v_cvt_pk_f32_fp8_sdwa v[82:83], v83 src0_sel:WORD_1
	v_pk_fma_f32 v[32:33], s[4:5], v[84:85], v[32:33] op_sel_hi:[0,1,1]
	v_pk_fma_f32 v[34:35], s[4:5], v[86:87], v[34:35] op_sel_hi:[0,1,1]
	v_pk_fma_f32 v[28:29], s[4:5], v[88:89], v[28:29] op_sel_hi:[0,1,1]
	v_pk_fma_f32 v[26:27], s[4:5], v[82:83], v[26:27] op_sel_hi:[0,1,1]
	s_add_i32 s1, s14, -1
	s_and_b32 s14, s1, s14
	v_pk_fma_f32 v[76:77], s[36:37], v[112:113], v[76:77] op_sel_hi:[0,1,1]
	v_pk_fma_f32 v[68:69], s[36:37], v[110:111], v[68:69] op_sel_hi:[0,1,1]
	v_pk_fma_f32 v[58:59], s[22:23], v[108:109], v[58:59] op_sel_hi:[0,1,1]
	v_pk_fma_f32 v[50:51], s[22:23], v[92:93], v[50:51] op_sel_hi:[0,1,1]
	v_pk_fma_f32 v[38:39], s[4:5], v[90:91], v[38:39] op_sel_hi:[0,1,1]
	s_waitcnt vmcnt(1)
	v_cvt_pk_f32_fp8_e32 v[82:83], v106
	v_cvt_pk_f32_fp8_sdwa v[84:85], v106 src0_sel:WORD_1
	v_cvt_pk_f32_fp8_e32 v[86:87], v107
	v_cvt_pk_f32_fp8_sdwa v[88:89], v107 src0_sel:WORD_1
	v_pk_fma_f32 v[24:25], s[0:1], v[82:83], v[24:25] op_sel_hi:[0,1,1]
	v_pk_fma_f32 v[22:23], s[0:1], v[84:85], v[22:23] op_sel_hi:[0,1,1]
	v_pk_fma_f32 v[20:21], s[0:1], v[86:87], v[20:21] op_sel_hi:[0,1,1]
	v_pk_fma_f32 v[18:19], s[0:1], v[88:89], v[18:19] op_sel_hi:[0,1,1]
	s_waitcnt vmcnt(0)
	v_cvt_pk_f32_fp8_e32 v[82:83], v104
	v_cvt_pk_f32_fp8_sdwa v[84:85], v104 src0_sel:WORD_1
	v_cvt_pk_f32_fp8_e32 v[86:87], v105
	v_cvt_pk_f32_fp8_sdwa v[88:89], v105 src0_sel:WORD_1
	v_pk_fma_f32 v[16:17], s[0:1], v[82:83], v[16:17] op_sel_hi:[0,1,1]
	v_pk_fma_f32 v[14:15], s[0:1], v[84:85], v[14:15] op_sel_hi:[0,1,1]
	v_pk_fma_f32 v[12:13], s[0:1], v[86:87], v[12:13] op_sel_hi:[0,1,1]
	v_pk_fma_f32 v[10:11], s[0:1], v[88:89], v[10:11] op_sel_hi:[0,1,1]
	s_or_b32 s0, s13, s14
	s_or_b32 s0, s0, s12
	s_or_b32 s0, s0, s10
	s_cmp_lg_u32 s0, 0
	s_cbranch_scc0 .LBB0_53

.LBB0_47:
	s_lshl_b32 s21, s21, 5
	s_and_b64 s[4:5], exec, s[4:5]
	s_cselect_b32 s4, 0, s21
	s_add_i32 s4, s4, s16
	s_ashr_i32 s5, s4, 31
	s_lshl_b64 s[4:5], s[4:5], 18
	s_add_u32 s4, s8, s4
	s_addc_u32 s5, s9, s5
	s_add_u32 s4, s4, s50
	s_addc_u32 s5, s5, s51
	v_lshl_add_u64 v[82:83], s[4:5], 0, v[2:3]
	global_load_dwordx2 v[92:93], v[82:83], off nt
	global_load_dwordx2 v[88:89], v[82:83], off offset:512 nt
	s_cmp_eq_u32 s12, 0
	s_cselect_b64 s[4:5], -1, 0
	s_ff1_i32_b32 s21, s12
	s_and_b64 vcc, exec, s[4:5]
	s_cbranch_vccnz .LBB0_49
	v_readlane_b32 s0, v101, s21
	s_ashr_i32 s1, s0, 31
	s_lshl_b64 s[0:1], s[0:1], 10
	s_brev_b32 s22, 60
.LBB0_49:
	s_lshl_b32 s21, s21, 5
	s_and_b64 s[4:5], exec, s[4:5]
	s_cselect_b32 s4, 0, s21
	s_add_i32 s4, s4, s18
	s_ashr_i32 s5, s4, 31
	s_lshl_b64 s[4:5], s[4:5], 18
	s_add_u32 s4, s8, s4
	s_addc_u32 s5, s9, s5
	s_add_u32 s0, s4, s0
	s_addc_u32 s1, s5, s1
	v_lshl_add_u64 v[82:83], s[0:1], 0, v[2:3]
	global_load_dwordx2 v[90:91], v[82:83], off nt
	global_load_dwordx2 v[84:85], v[82:83], off offset:512 nt
	s_cmp_eq_u32 s13, 0
	s_cselect_b64 s[52:53], -1, 0
	s_ff1_i32_b32 s1, s13
	s_mov_b64 s[50:51], 0
	s_mov_b32 s0, 0
	s_and_b64 vcc, exec, s[52:53]
	s_mov_b32 s4, 0
	s_mov_b64 s[54:55], 0
	s_cbranch_vccnz .LBB0_51
	v_readlane_b32 s4, v102, s1
	s_ashr_i32 s5, s4, 31
	s_lshl_b64 s[54:55], s[4:5], 10
	s_brev_b32 s4, 60
.LBB0_51:
	s_lshl_b32 s1, s1, 5
	s_and_b64 s[30:31], exec, s[52:53]
	s_cselect_b32 s1, 0, s1
	s_add_i32 s30, s1, s19
	s_ashr_i32 s31, s30, 31
	s_lshl_b64 s[30:31], s[30:31], 18
	s_add_u32 s1, s8, s30
	s_addc_u32 s5, s9, s31
	s_add_u32 s30, s1, s54
	s_addc_u32 s31, s5, s55
	v_lshl_add_u64 v[82:83], s[30:31], 0, v[2:3]
	global_load_dwordx2 v[86:87], v[82:83], off nt
	s_nop 0
	global_load_dwordx2 v[82:83], v[82:83], off offset:512 nt
	s_cmp_eq_u32 s14, 0
	s_cselect_b64 s[52:53], -1, 0
	s_ff1_i32_b32 s1, s14
	s_and_b64 vcc, exec, s[52:53]
	s_cbranch_vccnz .LBB0_44
	v_readlane_b32 s30, v103, s1
	s_ashr_i32 s31, s30, 31
	s_lshl_b64 s[50:51], s[30:31], 10
	s_brev_b32 s0, 60
	s_branch .LBB0_44

.LBB0_67:
	v_lshl_add_u64 v[0:1], s[42:43], 0, v[70:71]
	global_load_dwordx4 v[58:61], v[0:1], off offset:16 nt
	global_load_dwordx4 v[62:65], v[0:1], off nt
	global_load_dwordx4 v[50:53], v[0:1], off offset:2064 nt
	global_load_dwordx4 v[54:57], v[0:1], off offset:2048 nt
	v_lshl_add_u64 v[0:1], s[38:39], 0, v[70:71]
	global_load_dwordx4 v[40:43], v[0:1], off offset:16 nt
	global_load_dwordx4 v[44:47], v[0:1], off nt
	global_load_dwordx4 v[32:35], v[0:1], off offset:2064 nt
	global_load_dwordx4 v[36:39], v[0:1], off offset:2048 nt
	v_lshl_add_u64 v[0:1], s[46:47], 0, v[70:71]
	v_lshl_add_u64 v[4:5], s[44:45], 0, v[70:71]
	global_load_dwordx4 v[24:27], v[0:1], off offset:16 nt
	global_load_dwordx4 v[28:31], v[0:1], off nt
	global_load_dwordx4 v[16:19], v[0:1], off offset:2064 nt
	global_load_dwordx4 v[20:23], v[0:1], off offset:2048 nt
	global_load_dwordx4 v[8:11], v[4:5], off offset:16 nt
	global_load_dwordx4 v[12:15], v[4:5], off nt
	s_nop 0
	global_load_dwordx4 v[0:3], v[4:5], off offset:2064 nt
	s_nop 0
	global_load_dwordx4 v[4:7], v[4:5], off offset:2048 nt
	v_lshl_add_u64 v[94:95], s[40:41], 0, v[72:73]
	s_mov_b32 s0, 0x3fd00000
	v_add_co_u32_e32 v94, vcc, s0, v94
	s_mov_b32 s0, 0xf800000
	s_nop 0
	v_addc_co_u32_e32 v95, vcc, 0, v95, vcc
	s_waitcnt vmcnt(15)
	v_cvt_pk_bf16_f32 v92, v58, v59
	s_waitcnt vmcnt(14)
	v_mul_f32_e32 v89, v63, v63
	v_fmac_f32_e32 v89, v62, v62
	v_fmac_f32_e32 v89, v64, v64
	v_fmac_f32_e32 v89, v65, v65
	v_fmac_f32_e32 v89, v58, v58
	v_fmac_f32_e32 v89, v59, v59
	v_fmac_f32_e32 v89, v60, v60
	v_fmac_f32_e32 v89, v61, v61
	s_waitcnt vmcnt(12)
	v_fmac_f32_e32 v89, v54, v54
	v_fmac_f32_e32 v89, v55, v55
	v_fmac_f32_e32 v89, v56, v56
	v_fmac_f32_e32 v89, v57, v57
	v_fmac_f32_e32 v89, v50, v50
	v_fmac_f32_e32 v89, v51, v51
	v_cvt_pk_bf16_f32 v90, v62, v63
	v_cvt_pk_bf16_f32 v91, v64, v65
	v_cvt_pk_bf16_f32 v93, v60, v61
	v_fmac_f32_e32 v89, v52, v52
	global_store_dwordx4 v[94:95], v[90:93], off
	v_fmac_f32_e32 v89, v53, v53
	s_nop 0
	v_cvt_pk_bf16_f32 v90, v54, v55
	v_cvt_pk_bf16_f32 v91, v56, v57
	v_cvt_pk_bf16_f32 v92, v50, v51
	v_cvt_pk_bf16_f32 v93, v52, v53
	global_store_dwordx4 v[94:95], v[90:93], off offset:1024
	ds_bpermute_b32 v90, v48, v89
	s_waitcnt lgkmcnt(0)
	v_add_f32_e32 v89, v89, v90
	ds_bpermute_b32 v90, v84, v89
	s_waitcnt lgkmcnt(0)
	v_add_f32_e32 v89, v89, v90
	ds_bpermute_b32 v90, v85, v89
	s_waitcnt lgkmcnt(0)
	v_add_f32_e32 v89, v89, v90
	ds_bpermute_b32 v90, v86, v89
	s_waitcnt lgkmcnt(0)
	v_add_f32_e32 v89, v89, v90
	ds_bpermute_b32 v90, v87, v89
	s_waitcnt lgkmcnt(0)
	v_add_f32_e32 v89, v89, v90
	ds_bpermute_b32 v90, v88, v89
	s_waitcnt lgkmcnt(0)
	v_add_f32_e32 v89, v89, v90
	v_fmamk_f32 v89, v89, 0x3a800000, v229
	v_cmp_gt_f32_e32 vcc, s0, v89
	v_mul_f32_e32 v90, 0x4f800000, v89
	s_nop 0
	v_cndmask_b32_e32 v89, v89, v90, vcc
	v_sqrt_f32_e32 v90, v89
	s_nop 0
	v_add_u32_e32 v91, -1, v90
	v_fma_f32 v92, -v91, v90, v89
	v_cmp_ge_f32_e64 s[36:37], 0, v92
	v_add_u32_e32 v92, 1, v90
	s_nop 0
	v_cndmask_b32_e64 v91, v90, v91, s[36:37]
	v_fma_f32 v90, -v92, v90, v89
	v_cmp_lt_f32_e64 s[36:37], 0, v90
	s_nop 1
	v_cndmask_b32_e64 v90, v91, v92, s[36:37]
	v_mul_f32_e32 v91, 0x37800000, v90
	v_cndmask_b32_e32 v90, v90, v91, vcc
	v_cmp_class_f32_e32 vcc, v89, v230
	s_nop 1
	v_cndmask_b32_e32 v89, v90, v89, vcc
	v_div_scale_f32 v90, s[0:1], v89, v89, 1.0
	v_rcp_f32_e32 v91, v90
	s_nop 0
	v_fma_f32 v92, -v90, v91, 1.0
	v_fmac_f32_e32 v91, v92, v91
	v_div_scale_f32 v92, vcc, 1.0, v89, 1.0
	v_mul_f32_e32 v93, v92, v91
	v_fma_f32 v94, -v90, v93, v92
	v_fmac_f32_e32 v93, v94, v91
	v_fma_f32 v90, -v90, v93, v92
	v_div_fmas_f32 v90, v90, v91, v93
	v_div_fixup_f32 v89, v90, v89, 1.0
	s_and_saveexec_b64 s[0:1], s[34:35]
	s_cbranch_execz .LBB0_69
	s_add_u32 s18, s40, s12
	s_addc_u32 s19, s41, s13
	global_store_dword v49, v89, s[18:19]

.LBB0_144:
	s_add_i32 s0, s6, -15
	v_lshl_or_b32 v48, s0, 7, v184
	v_lshlrev_b64 v[0:1], 2, v[48:49]
	v_lshl_add_u64 v[4:5], s[48:49], 0, v[0:1]
	v_lshl_add_u64 v[12:13], s[58:59], 0, v[0:1]
	global_load_dwordx4 v[0:3], v[4:5], off offset:16
	global_load_dwordx4 v[8:11], v[4:5], off
	s_nop 0
	global_load_dwordx4 v[4:7], v[12:13], off offset:16
	s_nop 0
	global_load_dwordx4 v[12:15], v[12:13], off
	s_and_b32 s1, s0, 1
	s_lshl_b32 s0, s0, 2
	s_and_b32 s0, s0, 0xffffff8
	s_add_i32 s0, s8, s0
	s_lshl_b32 s4, s68, 9
	s_lshl_b32 s0, s0, 4
	s_add_i32 s0, s0, s4
	s_or_b32 s70, s0, s1
	s_ashr_i32 s71, s70, 31
	s_lshl_b64 s[0:1], s[70:71], 10
	s_waitcnt vmcnt(0)
	v_fmamk_f32 v16, v158, 0x3a800000, v8
	v_med3_f32 v16, v16, s15, v233
	v_mul_f32_e32 v16, 0xbfb8aa3b, v16
	v_exp_f32_e32 v18, v16
	v_fmamk_f32 v17, v150, 0x3a800000, v12
	v_med3_f32 v17, v17, s15, v233
	v_mul_f32_e32 v16, 0xbfb8aa3b, v17
	v_add_f32_e32 v17, 1.0, v18
	v_rcp_f32_e32 v18, v17
	v_fmamk_f32 v17, v159, 0x3a800000, v9
	v_med3_f32 v17, v17, s15, v233
	v_mul_f32_e32 v17, 0xbfb8aa3b, v17
	v_exp_f32_e32 v20, v17
	v_fmamk_f32 v19, v151, 0x3a800000, v13
	v_med3_f32 v19, v19, s15, v233
	v_mul_f32_e32 v17, 0xbfb8aa3b, v19
	v_exp_f32_e32 v16, v16
	v_exp_f32_e32 v17, v17
	v_add_f32_e32 v19, 1.0, v20
	v_rcp_f32_e32 v19, v19
	v_fmamk_f32 v21, v153, 0x3a800000, v15
	v_pk_add_f32 v[16:17], v[16:17], 1.0 op_sel_hi:[1,0]
	v_med3_f32 v21, v21, s15, v233
	v_rcp_f32_e32 v22, v16
	v_rcp_f32_e32 v23, v17
	v_pk_mul_f32 v[16:17], v[16:17], v[18:19]
	v_fmamk_f32 v18, v160, 0x3a800000, v10
	v_med3_f32 v18, v18, s15, v233
	v_mul_f32_e32 v18, 0xbfb8aa3b, v18
	v_exp_f32_e32 v20, v18
	v_fmamk_f32 v19, v152, 0x3a800000, v14
	v_med3_f32 v19, v19, s15, v233
	v_mul_f32_e32 v18, 0xbfb8aa3b, v19
	v_add_f32_e32 v19, 1.0, v20
	v_rcp_f32_e32 v20, v19
	v_fmamk_f32 v19, v161, 0x3a800000, v11
	v_med3_f32 v19, v19, s15, v233
	v_mul_f32_e32 v19, 0xbfb8aa3b, v19
	v_exp_f32_e32 v24, v19
	v_mul_f32_e32 v19, 0xbfb8aa3b, v21
	v_exp_f32_e32 v18, v18
	v_exp_f32_e32 v19, v19
	v_add_f32_e32 v21, 1.0, v24
	v_rcp_f32_e32 v21, v21
	v_fmamk_f32 v25, v147, 0x3a800000, v5
	v_pk_add_f32 v[18:19], v[18:19], 1.0 op_sel_hi:[1,0]
	v_med3_f32 v25, v25, s15, v233
	v_rcp_f32_e32 v28, v18
	v_rcp_f32_e32 v29, v19
	v_pk_mul_f32 v[18:19], v[18:19], v[20:21]
	v_fmamk_f32 v20, v154, 0x3a800000, v0
	v_med3_f32 v20, v20, s15, v233
	v_mul_f32_e32 v20, 0xbfb8aa3b, v20
	v_exp_f32_e32 v24, v20
	v_fmamk_f32 v21, v146, 0x3a800000, v4
	v_med3_f32 v21, v21, s15, v233
	v_mul_f32_e32 v20, 0xbfb8aa3b, v21
	v_add_f32_e32 v21, 1.0, v24
	v_rcp_f32_e32 v24, v21
	v_fmamk_f32 v21, v155, 0x3a800000, v1
	v_med3_f32 v21, v21, s15, v233
	v_mul_f32_e32 v21, 0xbfb8aa3b, v21
	v_exp_f32_e32 v26, v21
	v_mul_f32_e32 v21, 0xbfb8aa3b, v25
	v_exp_f32_e32 v20, v20
	v_exp_f32_e32 v21, v21
	v_add_f32_e32 v25, 1.0, v26
	v_rcp_f32_e32 v25, v25
	v_fmamk_f32 v27, v149, 0x3a800000, v7
	v_pk_add_f32 v[20:21], v[20:21], 1.0 op_sel_hi:[1,0]
	v_med3_f32 v27, v27, s15, v233
	v_rcp_f32_e32 v30, v20
	v_rcp_f32_e32 v31, v21
	v_pk_mul_f32 v[20:21], v[20:21], v[24:25]
	v_fmamk_f32 v24, v156, 0x3a800000, v2
	v_med3_f32 v24, v24, s15, v233
	v_mul_f32_e32 v24, 0xbfb8aa3b, v24
	v_exp_f32_e32 v26, v24
	v_fmamk_f32 v25, v148, 0x3a800000, v6
	v_med3_f32 v25, v25, s15, v233
	v_mul_f32_e32 v24, 0xbfb8aa3b, v25
	v_add_f32_e32 v25, 1.0, v26
	v_rcp_f32_e32 v26, v25
	v_fmamk_f32 v25, v157, 0x3a800000, v3
	v_med3_f32 v25, v25, s15, v233
	v_mul_f32_e32 v25, 0xbfb8aa3b, v25
	v_exp_f32_e32 v48, v25
	v_mul_f32_e32 v25, 0xbfb8aa3b, v27
	v_exp_f32_e32 v24, v24
	v_exp_f32_e32 v25, v25
	v_add_f32_e32 v27, 1.0, v48
	v_rcp_f32_e32 v27, v27
	v_cvt_pk_bf16_f32 v16, v16, v17
	v_pk_add_f32 v[24:25], v[24:25], 1.0 op_sel_hi:[1,0]
	v_cvt_pk_bf16_f32 v17, v18, v19
	v_rcp_f32_e32 v48, v24
	v_rcp_f32_e32 v174, v25
	v_pk_mul_f32 v[26:27], v[24:25], v[26:27]
	v_cvt_pk_bf16_f32 v18, v20, v21
	v_or_b32_e32 v20, s0, v187
	v_mov_b32_e32 v21, s1
	v_cvt_pk_bf16_f32 v19, v26, v27
	v_lshl_add_u64 v[24:25], s[44:45], 0, v[20:21]
	global_store_dwordx4 v[24:25], v[16:19], off nt
	v_lshl_add_u64 v[20:21], s[46:47], 0, v[20:21]
	v_fmamk_f32 v25, v133, 0x3a800000, v7
	v_cvt_pk_bf16_f32 v16, v22, v23
	v_cvt_pk_bf16_f32 v17, v28, v29
	v_cvt_pk_bf16_f32 v18, v30, v31
	v_cvt_pk_bf16_f32 v19, v48, v174
	global_store_dwordx4 v[20:21], v[16:19], off nt
	v_fmamk_f32 v21, v137, 0x3a800000, v15
	v_med3_f32 v21, v21, s15, v233
	v_fmamk_f32 v16, v142, 0x3a800000, v8
	v_med3_f32 v16, v16, s15, v233
	v_mul_f32_e32 v16, 0xbfb8aa3b, v16
	v_exp_f32_e32 v18, v16
	v_fmamk_f32 v17, v134, 0x3a800000, v12
	v_med3_f32 v17, v17, s15, v233
	v_mul_f32_e32 v16, 0xbfb8aa3b, v17
	v_add_f32_e32 v17, 1.0, v18
	v_rcp_f32_e32 v18, v17
	v_fmamk_f32 v17, v143, 0x3a800000, v9
	v_med3_f32 v17, v17, s15, v233
	v_mul_f32_e32 v17, 0xbfb8aa3b, v17
	v_exp_f32_e32 v20, v17
	v_fmamk_f32 v19, v135, 0x3a800000, v13
	v_med3_f32 v19, v19, s15, v233
	v_mul_f32_e32 v17, 0xbfb8aa3b, v19
	v_exp_f32_e32 v16, v16
	v_exp_f32_e32 v17, v17
	v_add_f32_e32 v19, 1.0, v20
	v_rcp_f32_e32 v19, v19
	v_fmamk_f32 v23, v131, 0x3a800000, v5
	v_pk_add_f32 v[16:17], v[16:17], 1.0 op_sel_hi:[1,0]
	v_med3_f32 v23, v23, s15, v233
	v_rcp_f32_e32 v26, v16
	v_pk_mul_f32 v[18:19], v[16:17], v[18:19]
	v_fmamk_f32 v16, v144, 0x3a800000, v10
	v_med3_f32 v16, v16, s15, v233
	v_mul_f32_e32 v16, 0xbfb8aa3b, v16
	v_exp_f32_e32 v20, v16
	v_rcp_f32_e32 v27, v17
	v_fmamk_f32 v17, v136, 0x3a800000, v14
	v_med3_f32 v17, v17, s15, v233
	v_mul_f32_e32 v16, 0xbfb8aa3b, v17
	v_add_f32_e32 v17, 1.0, v20
	v_rcp_f32_e32 v20, v17
	v_fmamk_f32 v17, v145, 0x3a800000, v11
	v_med3_f32 v17, v17, s15, v233
	v_mul_f32_e32 v17, 0xbfb8aa3b, v17
	v_exp_f32_e32 v22, v17
	v_mul_f32_e32 v17, 0xbfb8aa3b, v21
	v_exp_f32_e32 v16, v16
	v_exp_f32_e32 v17, v17
	v_add_f32_e32 v21, 1.0, v22
	v_rcp_f32_e32 v21, v21
	v_med3_f32 v25, v25, s15, v233
	v_pk_add_f32 v[16:17], v[16:17], 1.0 op_sel_hi:[1,0]
	s_or_b32 s0, s70, 2
	v_rcp_f32_e32 v28, v16
	v_pk_mul_f32 v[20:21], v[16:17], v[20:21]
	v_fmamk_f32 v16, v138, 0x3a800000, v0
	v_med3_f32 v16, v16, s15, v233
	v_mul_f32_e32 v16, 0xbfb8aa3b, v16
	v_exp_f32_e32 v22, v16
	v_rcp_f32_e32 v29, v17
	v_fmamk_f32 v17, v130, 0x3a800000, v4
	v_med3_f32 v17, v17, s15, v233
	v_mul_f32_e32 v16, 0xbfb8aa3b, v17
	v_add_f32_e32 v17, 1.0, v22
	v_rcp_f32_e32 v22, v17
	v_fmamk_f32 v17, v139, 0x3a800000, v1
	v_med3_f32 v17, v17, s15, v233
	v_mul_f32_e32 v17, 0xbfb8aa3b, v17
	v_exp_f32_e32 v24, v17
	v_mul_f32_e32 v17, 0xbfb8aa3b, v23
	v_exp_f32_e32 v16, v16
	v_exp_f32_e32 v17, v17
	v_add_f32_e32 v23, 1.0, v24
	v_rcp_f32_e32 v23, v23
	s_ashr_i32 s1, s0, 31
	v_pk_add_f32 v[16:17], v[16:17], 1.0 op_sel_hi:[1,0]
	s_lshl_b64 s[0:1], s[0:1], 10
	v_rcp_f32_e32 v30, v16
	v_pk_mul_f32 v[22:23], v[16:17], v[22:23]
	v_fmamk_f32 v16, v140, 0x3a800000, v2
	v_med3_f32 v16, v16, s15, v233
	v_mul_f32_e32 v16, 0xbfb8aa3b, v16
	v_exp_f32_e32 v24, v16
	v_rcp_f32_e32 v31, v17
	v_fmamk_f32 v17, v132, 0x3a800000, v6
	v_med3_f32 v17, v17, s15, v233
	v_mul_f32_e32 v16, 0xbfb8aa3b, v17
	v_add_f32_e32 v17, 1.0, v24
	v_rcp_f32_e32 v24, v17
	v_fmamk_f32 v17, v141, 0x3a800000, v3
	v_med3_f32 v17, v17, s15, v233
	v_mul_f32_e32 v17, 0xbfb8aa3b, v17
	v_exp_f32_e32 v48, v17
	v_mul_f32_e32 v17, 0xbfb8aa3b, v25
	v_exp_f32_e32 v16, v16
	v_exp_f32_e32 v17, v17
	v_add_f32_e32 v25, 1.0, v48
	v_rcp_f32_e32 v25, v25
	v_pk_add_f32 v[16:17], v[16:17], 1.0 op_sel_hi:[1,0]
	s_nop 0
	v_rcp_f32_e32 v48, v16
	v_rcp_f32_e32 v174, v17
	v_pk_mul_f32 v[24:25], v[16:17], v[24:25]
	v_cvt_pk_bf16_f32 v17, v20, v21
	v_or_b32_e32 v20, s0, v187
	v_mov_b32_e32 v21, s1
	v_cvt_pk_bf16_f32 v16, v18, v19
	v_cvt_pk_bf16_f32 v18, v22, v23
	v_cvt_pk_bf16_f32 v19, v24, v25
	v_lshl_add_u64 v[22:23], s[44:45], 0, v[20:21]
	global_store_dwordx4 v[22:23], v[16:19], off nt
	v_lshl_add_u64 v[20:21], s[46:47], 0, v[20:21]
	v_fmamk_f32 v23, v115, 0x3a800000, v5
	v_cvt_pk_bf16_f32 v16, v26, v27
	v_cvt_pk_bf16_f32 v17, v28, v29
	v_cvt_pk_bf16_f32 v18, v30, v31
	v_cvt_pk_bf16_f32 v19, v48, v174
	global_store_dwordx4 v[20:21], v[16:19], off nt
	v_fmamk_f32 v21, v121, 0x3a800000, v15
	v_med3_f32 v21, v21, s15, v233
	v_fmamk_f32 v16, v126, 0x3a800000, v8
	v_med3_f32 v16, v16, s15, v233
	v_mul_f32_e32 v16, 0xbfb8aa3b, v16
	v_exp_f32_e32 v18, v16
	v_fmamk_f32 v17, v118, 0x3a800000, v12
	v_med3_f32 v17, v17, s15, v233
	v_mul_f32_e32 v16, 0xbfb8aa3b, v17
	v_add_f32_e32 v17, 1.0, v18
	v_rcp_f32_e32 v18, v17
	v_fmamk_f32 v17, v127, 0x3a800000, v9
	v_med3_f32 v17, v17, s15, v233
	v_mul_f32_e32 v17, 0xbfb8aa3b, v17
	v_exp_f32_e32 v20, v17
	v_fmamk_f32 v19, v119, 0x3a800000, v13
	v_med3_f32 v19, v19, s15, v233
	v_mul_f32_e32 v17, 0xbfb8aa3b, v19
	v_exp_f32_e32 v16, v16
	v_exp_f32_e32 v17, v17
	v_add_f32_e32 v19, 1.0, v20
	v_rcp_f32_e32 v19, v19
	v_med3_f32 v23, v23, s15, v233
	v_pk_add_f32 v[16:17], v[16:17], 1.0 op_sel_hi:[1,0]
	v_fmamk_f32 v25, v117, 0x3a800000, v7
	v_rcp_f32_e32 v26, v16
	v_pk_mul_f32 v[18:19], v[16:17], v[18:19]
	v_fmamk_f32 v16, v128, 0x3a800000, v10
	v_med3_f32 v16, v16, s15, v233
	v_mul_f32_e32 v16, 0xbfb8aa3b, v16
	v_exp_f32_e32 v20, v16
	v_rcp_f32_e32 v27, v17
	v_fmamk_f32 v17, v120, 0x3a800000, v14
	v_med3_f32 v17, v17, s15, v233
	v_mul_f32_e32 v16, 0xbfb8aa3b, v17
	v_add_f32_e32 v17, 1.0, v20
	v_rcp_f32_e32 v20, v17
	v_fmamk_f32 v17, v129, 0x3a800000, v11
	v_med3_f32 v17, v17, s15, v233
	v_mul_f32_e32 v17, 0xbfb8aa3b, v17
	v_exp_f32_e32 v22, v17
	v_mul_f32_e32 v17, 0xbfb8aa3b, v21
	v_exp_f32_e32 v16, v16
	v_exp_f32_e32 v17, v17
	v_add_f32_e32 v21, 1.0, v22
	v_rcp_f32_e32 v21, v21
	v_med3_f32 v25, v25, s15, v233
	v_pk_add_f32 v[16:17], v[16:17], 1.0 op_sel_hi:[1,0]
	s_or_b32 s0, s70, 4
	v_rcp_f32_e32 v28, v16
	v_pk_mul_f32 v[20:21], v[16:17], v[20:21]
	v_fmamk_f32 v16, v122, 0x3a800000, v0
	v_med3_f32 v16, v16, s15, v233
	v_mul_f32_e32 v16, 0xbfb8aa3b, v16
	v_exp_f32_e32 v22, v16
	v_rcp_f32_e32 v29, v17
	v_fmamk_f32 v17, v114, 0x3a800000, v4
	v_med3_f32 v17, v17, s15, v233
	v_mul_f32_e32 v16, 0xbfb8aa3b, v17
	v_add_f32_e32 v17, 1.0, v22
	v_rcp_f32_e32 v22, v17
	v_fmamk_f32 v17, v123, 0x3a800000, v1
	v_med3_f32 v17, v17, s15, v233
	v_mul_f32_e32 v17, 0xbfb8aa3b, v17
	v_exp_f32_e32 v24, v17
	v_mul_f32_e32 v17, 0xbfb8aa3b, v23
	v_exp_f32_e32 v16, v16
	v_exp_f32_e32 v17, v17
	v_add_f32_e32 v23, 1.0, v24
	v_rcp_f32_e32 v23, v23
	s_ashr_i32 s1, s0, 31
	v_pk_add_f32 v[16:17], v[16:17], 1.0 op_sel_hi:[1,0]
	s_lshl_b64 s[0:1], s[0:1], 10
	v_rcp_f32_e32 v30, v16
	v_pk_mul_f32 v[22:23], v[16:17], v[22:23]
	v_fmamk_f32 v16, v124, 0x3a800000, v2
	v_med3_f32 v16, v16, s15, v233
	v_mul_f32_e32 v16, 0xbfb8aa3b, v16
	v_exp_f32_e32 v24, v16
	v_rcp_f32_e32 v31, v17
	v_fmamk_f32 v17, v116, 0x3a800000, v6
	v_med3_f32 v17, v17, s15, v233
	v_mul_f32_e32 v16, 0xbfb8aa3b, v17
	v_add_f32_e32 v17, 1.0, v24
	v_rcp_f32_e32 v24, v17
	v_fmamk_f32 v17, v125, 0x3a800000, v3
	v_med3_f32 v17, v17, s15, v233
	v_mul_f32_e32 v17, 0xbfb8aa3b, v17
	v_exp_f32_e32 v48, v17
	v_mul_f32_e32 v17, 0xbfb8aa3b, v25
	v_exp_f32_e32 v16, v16
	v_exp_f32_e32 v17, v17
	v_add_f32_e32 v25, 1.0, v48
	v_rcp_f32_e32 v25, v25
	v_pk_add_f32 v[16:17], v[16:17], 1.0 op_sel_hi:[1,0]
	s_nop 0
	v_rcp_f32_e32 v48, v16
	v_rcp_f32_e32 v174, v17
	v_pk_mul_f32 v[24:25], v[16:17], v[24:25]
	v_cvt_pk_bf16_f32 v17, v20, v21
	v_or_b32_e32 v20, s0, v187
	v_mov_b32_e32 v21, s1
	v_cvt_pk_bf16_f32 v16, v18, v19
	v_cvt_pk_bf16_f32 v18, v22, v23
	v_cvt_pk_bf16_f32 v19, v24, v25
	v_lshl_add_u64 v[22:23], s[44:45], 0, v[20:21]
	global_store_dwordx4 v[22:23], v[16:19], off nt
	v_lshl_add_u64 v[20:21], s[46:47], 0, v[20:21]
	v_fmamk_f32 v23, v99, 0x3a800000, v5
	v_cvt_pk_bf16_f32 v16, v26, v27
	v_cvt_pk_bf16_f32 v17, v28, v29
	v_cvt_pk_bf16_f32 v18, v30, v31
	v_cvt_pk_bf16_f32 v19, v48, v174
	global_store_dwordx4 v[20:21], v[16:19], off nt
	v_fmamk_f32 v21, v105, 0x3a800000, v15
	v_med3_f32 v21, v21, s15, v233
	v_fmamk_f32 v16, v110, 0x3a800000, v8
	v_med3_f32 v16, v16, s15, v233
	v_mul_f32_e32 v16, 0xbfb8aa3b, v16
	v_exp_f32_e32 v18, v16
	v_fmamk_f32 v17, v102, 0x3a800000, v12
	v_med3_f32 v17, v17, s15, v233
	v_mul_f32_e32 v16, 0xbfb8aa3b, v17
	v_add_f32_e32 v17, 1.0, v18
	v_rcp_f32_e32 v18, v17
	v_fmamk_f32 v17, v111, 0x3a800000, v9
	v_med3_f32 v17, v17, s15, v233
	v_mul_f32_e32 v17, 0xbfb8aa3b, v17
	v_exp_f32_e32 v20, v17
	v_fmamk_f32 v19, v103, 0x3a800000, v13
	v_med3_f32 v19, v19, s15, v233
	v_mul_f32_e32 v17, 0xbfb8aa3b, v19
	v_exp_f32_e32 v16, v16
	v_exp_f32_e32 v17, v17
	v_add_f32_e32 v19, 1.0, v20
	v_rcp_f32_e32 v19, v19
	v_med3_f32 v23, v23, s15, v233
	v_pk_add_f32 v[16:17], v[16:17], 1.0 op_sel_hi:[1,0]
	v_fmamk_f32 v25, v101, 0x3a800000, v7
	v_rcp_f32_e32 v26, v16
	v_pk_mul_f32 v[18:19], v[16:17], v[18:19]
	v_fmamk_f32 v16, v112, 0x3a800000, v10
	v_med3_f32 v16, v16, s15, v233
	v_mul_f32_e32 v16, 0xbfb8aa3b, v16
	v_exp_f32_e32 v20, v16
	v_rcp_f32_e32 v27, v17
	v_fmamk_f32 v17, v104, 0x3a800000, v14
	v_med3_f32 v17, v17, s15, v233
	v_mul_f32_e32 v16, 0xbfb8aa3b, v17
	v_add_f32_e32 v17, 1.0, v20
	v_rcp_f32_e32 v20, v17
	v_fmamk_f32 v17, v113, 0x3a800000, v11
	v_med3_f32 v17, v17, s15, v233
	v_mul_f32_e32 v17, 0xbfb8aa3b, v17
	v_exp_f32_e32 v22, v17
	v_mul_f32_e32 v17, 0xbfb8aa3b, v21
	v_exp_f32_e32 v16, v16
	v_exp_f32_e32 v17, v17
	v_add_f32_e32 v21, 1.0, v22
	v_rcp_f32_e32 v21, v21
	v_med3_f32 v25, v25, s15, v233
	v_pk_add_f32 v[16:17], v[16:17], 1.0 op_sel_hi:[1,0]
	s_or_b32 s0, s70, 6
	v_rcp_f32_e32 v28, v16
	v_pk_mul_f32 v[20:21], v[16:17], v[20:21]
	v_fmamk_f32 v16, v106, 0x3a800000, v0
	v_med3_f32 v16, v16, s15, v233
	v_mul_f32_e32 v16, 0xbfb8aa3b, v16
	v_exp_f32_e32 v22, v16
	v_rcp_f32_e32 v29, v17
	v_fmamk_f32 v17, v98, 0x3a800000, v4
	v_med3_f32 v17, v17, s15, v233
	v_mul_f32_e32 v16, 0xbfb8aa3b, v17
	v_add_f32_e32 v17, 1.0, v22
	v_rcp_f32_e32 v22, v17
	v_fmamk_f32 v17, v107, 0x3a800000, v1
	v_med3_f32 v17, v17, s15, v233
	v_mul_f32_e32 v17, 0xbfb8aa3b, v17
	v_exp_f32_e32 v24, v17
	v_mul_f32_e32 v17, 0xbfb8aa3b, v23
	v_exp_f32_e32 v16, v16
	v_exp_f32_e32 v17, v17
	v_add_f32_e32 v23, 1.0, v24
	v_rcp_f32_e32 v23, v23
	s_ashr_i32 s1, s0, 31
	v_pk_add_f32 v[16:17], v[16:17], 1.0 op_sel_hi:[1,0]
	s_lshl_b64 s[0:1], s[0:1], 10
	v_rcp_f32_e32 v30, v16
	v_pk_mul_f32 v[22:23], v[16:17], v[22:23]
	v_fmamk_f32 v16, v108, 0x3a800000, v2
	v_med3_f32 v16, v16, s15, v233
	v_mul_f32_e32 v16, 0xbfb8aa3b, v16
	v_exp_f32_e32 v24, v16
	v_rcp_f32_e32 v31, v17
	v_fmamk_f32 v17, v100, 0x3a800000, v6
	v_med3_f32 v17, v17, s15, v233
	v_mul_f32_e32 v16, 0xbfb8aa3b, v17
	v_add_f32_e32 v17, 1.0, v24
	v_rcp_f32_e32 v24, v17
	v_fmamk_f32 v17, v109, 0x3a800000, v3
	v_med3_f32 v17, v17, s15, v233
	v_mul_f32_e32 v17, 0xbfb8aa3b, v17
	v_exp_f32_e32 v48, v17
	v_mul_f32_e32 v17, 0xbfb8aa3b, v25
	v_exp_f32_e32 v16, v16
	v_exp_f32_e32 v17, v17
	v_add_f32_e32 v25, 1.0, v48
	v_rcp_f32_e32 v25, v25
	v_pk_add_f32 v[16:17], v[16:17], 1.0 op_sel_hi:[1,0]
	s_nop 0
	v_rcp_f32_e32 v48, v16
	v_rcp_f32_e32 v174, v17
	v_pk_mul_f32 v[24:25], v[16:17], v[24:25]
	v_cvt_pk_bf16_f32 v17, v20, v21
	v_or_b32_e32 v20, s0, v187
	v_mov_b32_e32 v21, s1
	v_cvt_pk_bf16_f32 v16, v18, v19
	v_cvt_pk_bf16_f32 v18, v22, v23
	v_cvt_pk_bf16_f32 v19, v24, v25
	v_lshl_add_u64 v[22:23], s[44:45], 0, v[20:21]
	global_store_dwordx4 v[22:23], v[16:19], off nt
	v_lshl_add_u64 v[20:21], s[46:47], 0, v[20:21]
	v_fmamk_f32 v23, v83, 0x3a800000, v5
	v_cvt_pk_bf16_f32 v16, v26, v27
	v_cvt_pk_bf16_f32 v17, v28, v29
	v_cvt_pk_bf16_f32 v18, v30, v31
	v_cvt_pk_bf16_f32 v19, v48, v174
	global_store_dwordx4 v[20:21], v[16:19], off nt
	v_fmamk_f32 v21, v89, 0x3a800000, v15
	v_med3_f32 v21, v21, s15, v233
	v_fmamk_f32 v16, v94, 0x3a800000, v8
	v_med3_f32 v16, v16, s15, v233
	v_mul_f32_e32 v16, 0xbfb8aa3b, v16
	v_exp_f32_e32 v18, v16
	v_fmamk_f32 v17, v86, 0x3a800000, v12
	v_med3_f32 v17, v17, s15, v233
	v_mul_f32_e32 v16, 0xbfb8aa3b, v17
	v_add_f32_e32 v17, 1.0, v18
	v_rcp_f32_e32 v18, v17
	v_fmamk_f32 v17, v95, 0x3a800000, v9
	v_med3_f32 v17, v17, s15, v233
	v_mul_f32_e32 v17, 0xbfb8aa3b, v17
	v_exp_f32_e32 v20, v17
	v_fmamk_f32 v19, v87, 0x3a800000, v13
	v_med3_f32 v19, v19, s15, v233
	v_mul_f32_e32 v17, 0xbfb8aa3b, v19
	v_exp_f32_e32 v16, v16
	v_exp_f32_e32 v17, v17
	v_add_f32_e32 v19, 1.0, v20
	v_rcp_f32_e32 v19, v19
	v_med3_f32 v23, v23, s15, v233
	v_pk_add_f32 v[16:17], v[16:17], 1.0 op_sel_hi:[1,0]
	v_fmamk_f32 v25, v85, 0x3a800000, v7
	v_rcp_f32_e32 v26, v16
	v_pk_mul_f32 v[18:19], v[16:17], v[18:19]
	v_fmamk_f32 v16, v96, 0x3a800000, v10
	v_med3_f32 v16, v16, s15, v233
	v_mul_f32_e32 v16, 0xbfb8aa3b, v16
	v_exp_f32_e32 v20, v16
	v_rcp_f32_e32 v27, v17
	v_fmamk_f32 v17, v88, 0x3a800000, v14
	v_med3_f32 v17, v17, s15, v233
	v_mul_f32_e32 v16, 0xbfb8aa3b, v17
	v_add_f32_e32 v17, 1.0, v20
	v_rcp_f32_e32 v20, v17
	v_fmamk_f32 v17, v97, 0x3a800000, v11
	v_med3_f32 v17, v17, s15, v233
	v_mul_f32_e32 v17, 0xbfb8aa3b, v17
	v_exp_f32_e32 v22, v17
	v_mul_f32_e32 v17, 0xbfb8aa3b, v21
	v_exp_f32_e32 v16, v16
	v_exp_f32_e32 v17, v17
	v_add_f32_e32 v21, 1.0, v22
	v_rcp_f32_e32 v21, v21
	v_med3_f32 v25, v25, s15, v233
	v_pk_add_f32 v[16:17], v[16:17], 1.0 op_sel_hi:[1,0]
	s_or_b32 s0, s70, 8
	v_rcp_f32_e32 v28, v16
	v_pk_mul_f32 v[20:21], v[16:17], v[20:21]
	v_fmamk_f32 v16, v90, 0x3a800000, v0
	v_med3_f32 v16, v16, s15, v233
	v_mul_f32_e32 v16, 0xbfb8aa3b, v16
	v_exp_f32_e32 v22, v16
	v_rcp_f32_e32 v29, v17
	v_fmamk_f32 v17, v82, 0x3a800000, v4
	v_med3_f32 v17, v17, s15, v233
	v_mul_f32_e32 v16, 0xbfb8aa3b, v17
	v_add_f32_e32 v17, 1.0, v22
	v_rcp_f32_e32 v22, v17
	v_fmamk_f32 v17, v91, 0x3a800000, v1
	v_med3_f32 v17, v17, s15, v233
	v_mul_f32_e32 v17, 0xbfb8aa3b, v17
	v_exp_f32_e32 v24, v17
	v_mul_f32_e32 v17, 0xbfb8aa3b, v23
	v_exp_f32_e32 v16, v16
	v_exp_f32_e32 v17, v17
	v_add_f32_e32 v23, 1.0, v24
	v_rcp_f32_e32 v23, v23
	s_ashr_i32 s1, s0, 31
	v_pk_add_f32 v[16:17], v[16:17], 1.0 op_sel_hi:[1,0]
	s_lshl_b64 s[0:1], s[0:1], 10
	v_rcp_f32_e32 v30, v16
	v_pk_mul_f32 v[22:23], v[16:17], v[22:23]
	v_fmamk_f32 v16, v92, 0x3a800000, v2
	v_med3_f32 v16, v16, s15, v233
	v_mul_f32_e32 v16, 0xbfb8aa3b, v16
	v_exp_f32_e32 v24, v16
	v_rcp_f32_e32 v31, v17
	v_fmamk_f32 v17, v84, 0x3a800000, v6
	v_med3_f32 v17, v17, s15, v233
	v_mul_f32_e32 v16, 0xbfb8aa3b, v17
	v_add_f32_e32 v17, 1.0, v24
	v_rcp_f32_e32 v24, v17
	v_fmamk_f32 v17, v93, 0x3a800000, v3
	v_med3_f32 v17, v17, s15, v233
	v_mul_f32_e32 v17, 0xbfb8aa3b, v17
	v_exp_f32_e32 v48, v17
	v_mul_f32_e32 v17, 0xbfb8aa3b, v25
	v_exp_f32_e32 v16, v16
	v_exp_f32_e32 v17, v17
	v_add_f32_e32 v25, 1.0, v48
	v_rcp_f32_e32 v25, v25
	v_pk_add_f32 v[16:17], v[16:17], 1.0 op_sel_hi:[1,0]
	s_nop 0
	v_rcp_f32_e32 v48, v16
	v_rcp_f32_e32 v174, v17
	v_pk_mul_f32 v[24:25], v[16:17], v[24:25]
	v_cvt_pk_bf16_f32 v17, v20, v21
	v_or_b32_e32 v20, s0, v187
	v_mov_b32_e32 v21, s1
	v_cvt_pk_bf16_f32 v16, v18, v19
	v_cvt_pk_bf16_f32 v18, v22, v23
	v_cvt_pk_bf16_f32 v19, v24, v25
	v_lshl_add_u64 v[22:23], s[44:45], 0, v[20:21]
	global_store_dwordx4 v[22:23], v[16:19], off nt
	v_lshl_add_u64 v[20:21], s[46:47], 0, v[20:21]
	v_fmamk_f32 v23, v51, 0x3a800000, v5
	v_cvt_pk_bf16_f32 v16, v26, v27
	v_cvt_pk_bf16_f32 v17, v28, v29
	v_cvt_pk_bf16_f32 v18, v30, v31
	v_cvt_pk_bf16_f32 v19, v48, v174
	global_store_dwordx4 v[20:21], v[16:19], off nt
	v_fmamk_f32 v21, v65, 0x3a800000, v15
	v_med3_f32 v21, v21, s15, v233
	v_fmamk_f32 v16, v70, 0x3a800000, v8
	v_med3_f32 v16, v16, s15, v233
	v_mul_f32_e32 v16, 0xbfb8aa3b, v16
	v_exp_f32_e32 v18, v16
	v_fmamk_f32 v17, v62, 0x3a800000, v12
	v_med3_f32 v17, v17, s15, v233
	v_mul_f32_e32 v16, 0xbfb8aa3b, v17
	v_add_f32_e32 v17, 1.0, v18
	v_rcp_f32_e32 v18, v17
	v_fmamk_f32 v17, v71, 0x3a800000, v9
	v_med3_f32 v17, v17, s15, v233
	v_mul_f32_e32 v17, 0xbfb8aa3b, v17
	v_exp_f32_e32 v20, v17
	v_fmamk_f32 v19, v63, 0x3a800000, v13
	v_med3_f32 v19, v19, s15, v233
	v_mul_f32_e32 v17, 0xbfb8aa3b, v19
	v_exp_f32_e32 v16, v16
	v_exp_f32_e32 v17, v17
	v_add_f32_e32 v19, 1.0, v20
	v_rcp_f32_e32 v19, v19
	v_med3_f32 v23, v23, s15, v233
	v_pk_add_f32 v[16:17], v[16:17], 1.0 op_sel_hi:[1,0]
	v_fmamk_f32 v25, v53, 0x3a800000, v7
	v_rcp_f32_e32 v26, v16
	v_pk_mul_f32 v[18:19], v[16:17], v[18:19]
	v_fmamk_f32 v16, v72, 0x3a800000, v10
	v_med3_f32 v16, v16, s15, v233
	v_mul_f32_e32 v16, 0xbfb8aa3b, v16
	v_exp_f32_e32 v20, v16
	v_rcp_f32_e32 v27, v17
	v_fmamk_f32 v17, v64, 0x3a800000, v14
	v_med3_f32 v17, v17, s15, v233
	v_mul_f32_e32 v16, 0xbfb8aa3b, v17
	v_add_f32_e32 v17, 1.0, v20
	v_rcp_f32_e32 v20, v17
	v_fmamk_f32 v17, v73, 0x3a800000, v11
	v_med3_f32 v17, v17, s15, v233
	v_mul_f32_e32 v17, 0xbfb8aa3b, v17
	v_exp_f32_e32 v22, v17
	v_mul_f32_e32 v17, 0xbfb8aa3b, v21
	v_exp_f32_e32 v16, v16
	v_exp_f32_e32 v17, v17
	v_add_f32_e32 v21, 1.0, v22
	v_rcp_f32_e32 v21, v21
	v_med3_f32 v25, v25, s15, v233
	v_pk_add_f32 v[16:17], v[16:17], 1.0 op_sel_hi:[1,0]
	s_or_b32 s0, s70, 10
	v_rcp_f32_e32 v28, v16
	v_pk_mul_f32 v[20:21], v[16:17], v[20:21]
	v_fmamk_f32 v16, v66, 0x3a800000, v0
	v_med3_f32 v16, v16, s15, v233
	v_mul_f32_e32 v16, 0xbfb8aa3b, v16
	v_exp_f32_e32 v22, v16
	v_rcp_f32_e32 v29, v17
	v_fmamk_f32 v17, v50, 0x3a800000, v4
	v_med3_f32 v17, v17, s15, v233
	v_mul_f32_e32 v16, 0xbfb8aa3b, v17
	v_add_f32_e32 v17, 1.0, v22
	v_rcp_f32_e32 v22, v17
	v_fmamk_f32 v17, v67, 0x3a800000, v1
	v_med3_f32 v17, v17, s15, v233
	v_mul_f32_e32 v17, 0xbfb8aa3b, v17
	v_exp_f32_e32 v24, v17
	v_mul_f32_e32 v17, 0xbfb8aa3b, v23
	v_exp_f32_e32 v16, v16
	v_exp_f32_e32 v17, v17
	v_add_f32_e32 v23, 1.0, v24
	v_rcp_f32_e32 v23, v23
	s_ashr_i32 s1, s0, 31
	v_pk_add_f32 v[16:17], v[16:17], 1.0 op_sel_hi:[1,0]
	s_lshl_b64 s[0:1], s[0:1], 10
	v_rcp_f32_e32 v30, v16
	v_pk_mul_f32 v[22:23], v[16:17], v[22:23]
	v_fmamk_f32 v16, v68, 0x3a800000, v2
	v_med3_f32 v16, v16, s15, v233
	v_mul_f32_e32 v16, 0xbfb8aa3b, v16
	v_exp_f32_e32 v24, v16
	v_rcp_f32_e32 v31, v17
	v_fmamk_f32 v17, v52, 0x3a800000, v6
	v_med3_f32 v17, v17, s15, v233
	v_mul_f32_e32 v16, 0xbfb8aa3b, v17
	v_add_f32_e32 v17, 1.0, v24
	v_rcp_f32_e32 v24, v17
	v_fmamk_f32 v17, v69, 0x3a800000, v3
	v_med3_f32 v17, v17, s15, v233
	v_mul_f32_e32 v17, 0xbfb8aa3b, v17
	v_exp_f32_e32 v48, v17
	v_mul_f32_e32 v17, 0xbfb8aa3b, v25
	v_exp_f32_e32 v16, v16
	v_exp_f32_e32 v17, v17
	v_add_f32_e32 v25, 1.0, v48
	v_rcp_f32_e32 v25, v25
	v_pk_add_f32 v[16:17], v[16:17], 1.0 op_sel_hi:[1,0]
	s_nop 0
	v_rcp_f32_e32 v48, v16
	v_rcp_f32_e32 v174, v17
	v_pk_mul_f32 v[24:25], v[16:17], v[24:25]
	v_cvt_pk_bf16_f32 v17, v20, v21
	v_or_b32_e32 v20, s0, v187
	v_mov_b32_e32 v21, s1
	v_cvt_pk_bf16_f32 v16, v18, v19
	v_cvt_pk_bf16_f32 v18, v22, v23
	v_cvt_pk_bf16_f32 v19, v24, v25
	v_lshl_add_u64 v[22:23], s[44:45], 0, v[20:21]
	global_store_dwordx4 v[22:23], v[16:19], off nt
	v_lshl_add_u64 v[20:21], s[46:47], 0, v[20:21]
	v_fmamk_f32 v23, v75, 0x3a800000, v5
	v_cvt_pk_bf16_f32 v16, v26, v27
	v_cvt_pk_bf16_f32 v17, v28, v29
	v_cvt_pk_bf16_f32 v18, v30, v31
	v_cvt_pk_bf16_f32 v19, v48, v174
	global_store_dwordx4 v[20:21], v[16:19], off nt
	v_fmamk_f32 v21, v81, 0x3a800000, v15
	v_med3_f32 v21, v21, s15, v233
	v_fmamk_f32 v16, v44, 0x3a800000, v8
	v_med3_f32 v16, v16, s15, v233
	v_mul_f32_e32 v16, 0xbfb8aa3b, v16
	v_exp_f32_e32 v18, v16
	v_fmamk_f32 v17, v78, 0x3a800000, v12
	v_med3_f32 v17, v17, s15, v233
	v_mul_f32_e32 v16, 0xbfb8aa3b, v17
	v_add_f32_e32 v17, 1.0, v18
	v_rcp_f32_e32 v18, v17
	v_fmamk_f32 v17, v45, 0x3a800000, v9
	v_med3_f32 v17, v17, s15, v233
	v_mul_f32_e32 v17, 0xbfb8aa3b, v17
	v_exp_f32_e32 v20, v17
	v_fmamk_f32 v19, v79, 0x3a800000, v13
	v_med3_f32 v19, v19, s15, v233
	v_mul_f32_e32 v17, 0xbfb8aa3b, v19
	v_exp_f32_e32 v16, v16
	v_exp_f32_e32 v17, v17
	v_add_f32_e32 v19, 1.0, v20
	v_rcp_f32_e32 v19, v19
	v_med3_f32 v23, v23, s15, v233
	v_pk_add_f32 v[16:17], v[16:17], 1.0 op_sel_hi:[1,0]
	v_fmamk_f32 v25, v77, 0x3a800000, v7
	v_rcp_f32_e32 v26, v16
	v_pk_mul_f32 v[18:19], v[16:17], v[18:19]
	v_fmamk_f32 v16, v46, 0x3a800000, v10
	v_med3_f32 v16, v16, s15, v233
	v_mul_f32_e32 v16, 0xbfb8aa3b, v16
	v_exp_f32_e32 v20, v16
	v_rcp_f32_e32 v27, v17
	v_fmamk_f32 v17, v80, 0x3a800000, v14
	v_med3_f32 v17, v17, s15, v233
	v_mul_f32_e32 v16, 0xbfb8aa3b, v17
	v_add_f32_e32 v17, 1.0, v20
	v_rcp_f32_e32 v20, v17
	v_fmamk_f32 v17, v47, 0x3a800000, v11
	v_med3_f32 v17, v17, s15, v233
	v_mul_f32_e32 v17, 0xbfb8aa3b, v17
	v_exp_f32_e32 v22, v17
	v_mul_f32_e32 v17, 0xbfb8aa3b, v21
	v_exp_f32_e32 v16, v16
	v_exp_f32_e32 v17, v17
	v_add_f32_e32 v21, 1.0, v22
	v_rcp_f32_e32 v21, v21
	v_med3_f32 v25, v25, s15, v233
	v_pk_add_f32 v[16:17], v[16:17], 1.0 op_sel_hi:[1,0]
	s_or_b32 s0, s70, 12
	v_rcp_f32_e32 v28, v16
	v_pk_mul_f32 v[20:21], v[16:17], v[20:21]
	v_fmamk_f32 v16, v40, 0x3a800000, v0
	v_med3_f32 v16, v16, s15, v233
	v_mul_f32_e32 v16, 0xbfb8aa3b, v16
	v_exp_f32_e32 v22, v16
	v_rcp_f32_e32 v29, v17
	v_fmamk_f32 v17, v74, 0x3a800000, v4
	v_med3_f32 v17, v17, s15, v233
	v_mul_f32_e32 v16, 0xbfb8aa3b, v17
	v_add_f32_e32 v17, 1.0, v22
	v_rcp_f32_e32 v22, v17
	v_fmamk_f32 v17, v41, 0x3a800000, v1
	v_med3_f32 v17, v17, s15, v233
	v_mul_f32_e32 v17, 0xbfb8aa3b, v17
	v_exp_f32_e32 v24, v17
	v_mul_f32_e32 v17, 0xbfb8aa3b, v23
	v_exp_f32_e32 v16, v16
	v_exp_f32_e32 v17, v17
	v_add_f32_e32 v23, 1.0, v24
	v_rcp_f32_e32 v23, v23
	s_ashr_i32 s1, s0, 31
	v_pk_add_f32 v[16:17], v[16:17], 1.0 op_sel_hi:[1,0]
	s_lshl_b64 s[0:1], s[0:1], 10
	v_rcp_f32_e32 v30, v16
	v_pk_mul_f32 v[22:23], v[16:17], v[22:23]
	v_fmamk_f32 v16, v42, 0x3a800000, v2
	v_med3_f32 v16, v16, s15, v233
	v_mul_f32_e32 v16, 0xbfb8aa3b, v16
	v_exp_f32_e32 v24, v16
	v_rcp_f32_e32 v31, v17
	v_fmamk_f32 v17, v76, 0x3a800000, v6
	v_med3_f32 v17, v17, s15, v233
	v_mul_f32_e32 v16, 0xbfb8aa3b, v17
	v_add_f32_e32 v17, 1.0, v24
	v_rcp_f32_e32 v24, v17
	v_fmamk_f32 v17, v43, 0x3a800000, v3
	v_med3_f32 v17, v17, s15, v233
	v_mul_f32_e32 v17, 0xbfb8aa3b, v17
	v_exp_f32_e32 v48, v17
	v_mul_f32_e32 v17, 0xbfb8aa3b, v25
	v_exp_f32_e32 v16, v16
	v_exp_f32_e32 v17, v17
	v_add_f32_e32 v25, 1.0, v48
	v_rcp_f32_e32 v25, v25
	v_fmamk_f32 v8, v36, 0x3a800000, v8
	v_pk_add_f32 v[16:17], v[16:17], 1.0 op_sel_hi:[1,0]
	v_med3_f32 v8, v8, s15, v233
	v_rcp_f32_e32 v48, v16
	v_rcp_f32_e32 v174, v17
	v_pk_mul_f32 v[24:25], v[16:17], v[24:25]
	v_cvt_pk_bf16_f32 v17, v20, v21
	v_or_b32_e32 v20, s0, v187
	v_mov_b32_e32 v21, s1
	v_cvt_pk_bf16_f32 v16, v18, v19
	v_cvt_pk_bf16_f32 v18, v22, v23
	v_cvt_pk_bf16_f32 v19, v24, v25
	v_lshl_add_u64 v[22:23], s[44:45], 0, v[20:21]
	global_store_dwordx4 v[22:23], v[16:19], off nt
	v_lshl_add_u64 v[20:21], s[46:47], 0, v[20:21]
	v_mul_f32_e32 v8, 0xbfb8aa3b, v8
	v_cvt_pk_bf16_f32 v16, v26, v27
	v_cvt_pk_bf16_f32 v17, v28, v29
	v_cvt_pk_bf16_f32 v18, v30, v31
	v_cvt_pk_bf16_f32 v19, v48, v174
	global_store_dwordx4 v[20:21], v[16:19], off nt
	v_fmamk_f32 v9, v37, 0x3a800000, v9
	v_fmamk_f32 v12, v58, 0x3a800000, v12
	v_exp_f32_e32 v16, v8
	v_med3_f32 v9, v9, s15, v233
	v_med3_f32 v12, v12, s15, v233
	v_mul_f32_e32 v9, 0xbfb8aa3b, v9
	v_mul_f32_e32 v8, 0xbfb8aa3b, v12
	v_add_f32_e32 v12, 1.0, v16
	v_exp_f32_e32 v16, v9
	v_fmamk_f32 v13, v59, 0x3a800000, v13
	v_med3_f32 v13, v13, s15, v233
	v_mul_f32_e32 v9, 0xbfb8aa3b, v13
	v_exp_f32_e32 v8, v8
	v_exp_f32_e32 v9, v9
	v_add_f32_e32 v13, 1.0, v16
	v_rcp_f32_e32 v12, v12
	v_rcp_f32_e32 v13, v13
	v_pk_add_f32 v[8:9], v[8:9], 1.0 op_sel_hi:[1,0]
	v_fmac_f32_e32 v11, 0x3a800000, v39
	v_rcp_f32_e32 v16, v8
	v_pk_mul_f32 v[12:13], v[8:9], v[12:13]
	v_fmamk_f32 v8, v38, 0x3a800000, v10
	v_med3_f32 v8, v8, s15, v233
	v_mul_f32_e32 v8, 0xbfb8aa3b, v8
	v_exp_f32_e32 v10, v8
	v_rcp_f32_e32 v17, v9
	v_fmamk_f32 v9, v60, 0x3a800000, v14
	v_med3_f32 v9, v9, s15, v233
	v_mul_f32_e32 v8, 0xbfb8aa3b, v9
	v_add_f32_e32 v9, 1.0, v10
	v_rcp_f32_e32 v10, v9
	v_med3_f32 v9, v11, s15, v233
	v_mul_f32_e32 v9, 0xbfb8aa3b, v9
	v_exp_f32_e32 v14, v9
	v_fmac_f32_e32 v15, 0x3a800000, v61
	v_med3_f32 v11, v15, s15, v233
	v_mul_f32_e32 v9, 0xbfb8aa3b, v11
	v_exp_f32_e32 v8, v8
	v_exp_f32_e32 v9, v9
	v_add_f32_e32 v11, 1.0, v14
	v_rcp_f32_e32 v11, v11
	v_fmamk_f32 v0, v32, 0x3a800000, v0
	v_med3_f32 v0, v0, s15, v233
	v_pk_add_f32 v[8:9], v[8:9], 1.0 op_sel_hi:[1,0]
	v_mul_f32_e32 v0, 0xbfb8aa3b, v0
	v_rcp_f32_e32 v14, v8
	v_pk_mul_f32 v[10:11], v[8:9], v[10:11]
	v_rcp_f32_e32 v8, v9
	v_exp_f32_e32 v9, v0
	v_fmamk_f32 v1, v33, 0x3a800000, v1
	v_fmamk_f32 v4, v54, 0x3a800000, v4
	v_med3_f32 v1, v1, s15, v233
	v_med3_f32 v4, v4, s15, v233
	v_mul_f32_e32 v1, 0xbfb8aa3b, v1
	v_mul_f32_e32 v0, 0xbfb8aa3b, v4
	v_add_f32_e32 v4, 1.0, v9
	v_exp_f32_e32 v9, v1
	v_fmamk_f32 v5, v55, 0x3a800000, v5
	v_med3_f32 v5, v5, s15, v233
	v_mul_f32_e32 v1, 0xbfb8aa3b, v5
	v_exp_f32_e32 v0, v0
	v_exp_f32_e32 v1, v1
	v_add_f32_e32 v5, 1.0, v9
	v_rcp_f32_e32 v4, v4
	v_rcp_f32_e32 v5, v5
	v_pk_add_f32 v[0:1], v[0:1], 1.0 op_sel_hi:[1,0]
	v_fmac_f32_e32 v3, 0x3a800000, v35
	v_rcp_f32_e32 v9, v0
	v_pk_mul_f32 v[4:5], v[0:1], v[4:5]
	v_fmamk_f32 v0, v34, 0x3a800000, v2
	v_med3_f32 v0, v0, s15, v233
	v_mul_f32_e32 v0, 0xbfb8aa3b, v0
	v_exp_f32_e32 v2, v0
	v_rcp_f32_e32 v15, v1
	v_fmamk_f32 v1, v56, 0x3a800000, v6
	v_med3_f32 v1, v1, s15, v233
	v_mul_f32_e32 v0, 0xbfb8aa3b, v1
	v_add_f32_e32 v1, 1.0, v2
	v_rcp_f32_e32 v2, v1
	v_med3_f32 v1, v3, s15, v233
	v_fmac_f32_e32 v7, 0x3a800000, v57
	v_mul_f32_e32 v1, 0xbfb8aa3b, v1
	v_med3_f32 v3, v7, s15, v233
	v_exp_f32_e32 v6, v1
	v_mul_f32_e32 v1, 0xbfb8aa3b, v3
	v_exp_f32_e32 v0, v0
	v_exp_f32_e32 v1, v1
	v_add_f32_e32 v3, 1.0, v6
	v_rcp_f32_e32 v3, v3
	s_or_b32 s0, s70, 14
	v_pk_add_f32 v[0:1], v[0:1], 1.0 op_sel_hi:[1,0]
	s_ashr_i32 s1, s0, 31
	v_rcp_f32_e32 v18, v0
	v_rcp_f32_e32 v19, v1
	s_lshl_b64 s[0:1], s[0:1], 10
	v_pk_mul_f32 v[6:7], v[0:1], v[2:3]
	v_cvt_pk_bf16_f32 v2, v4, v5
	v_or_b32_e32 v4, s0, v187
	v_mov_b32_e32 v5, s1
	v_cvt_pk_bf16_f32 v0, v12, v13
	v_cvt_pk_bf16_f32 v1, v10, v11
	v_cvt_pk_bf16_f32 v3, v6, v7
	v_lshl_add_u64 v[6:7], s[44:45], 0, v[4:5]
	global_store_dwordx4 v[6:7], v[0:3], off nt
	v_lshl_add_u64 v[4:5], s[46:47], 0, v[4:5]
	s_nop 0
	v_cvt_pk_bf16_f32 v0, v16, v17
	v_cvt_pk_bf16_f32 v1, v14, v8
	v_cvt_pk_bf16_f32 v2, v9, v15
	v_cvt_pk_bf16_f32 v3, v18, v19
	global_store_dwordx4 v[4:5], v[0:3], off nt
	s_cbranch_execnz .LBB0_143

.LBB0_159:
	v_lshl_or_b32 v0, s6, 8, v185
	v_lshl_add_u32 v12, s68, 8, v183
	v_ashrrev_i32_e32 v1, 31, v0
	v_ashrrev_i32_e32 v2, 31, v12
	v_lshl_add_u64 v[0:1], v[0:1], 1, s[4:5]
	v_mul_lo_u32 v4, s0, v2
	v_mul_lo_u32 v5, s1, v12
	v_mad_u64_u32 v[2:3], s[4:5], s0, v12, 0
	v_add3_u32 v3, v3, v4, v5
	v_lshl_add_u64 v[10:11], v[2:3], 1, v[0:1]
	v_pk_mul_f32 v[2:3], v[160:161], s[70:71] op_sel_hi:[1,0]
	v_pk_mul_f32 v[4:5], v[158:159], s[70:71] op_sel_hi:[1,0]
	v_pk_mul_f32 v[6:7], v[156:157], s[70:71] op_sel_hi:[1,0]
	v_pk_mul_f32 v[8:9], v[154:155], s[70:71] op_sel_hi:[1,0]
	v_cvt_pk_bf16_f32 v13, v4, v5
	v_cvt_pk_bf16_f32 v14, v2, v3
	v_cvt_pk_bf16_f32 v15, v8, v9
	v_cvt_pk_bf16_f32 v16, v6, v7
	v_pk_mul_f32 v[2:3], v[152:153], s[70:71] op_sel_hi:[1,0]
	v_pk_mul_f32 v[4:5], v[150:151], s[70:71] op_sel_hi:[1,0]
	v_pk_mul_f32 v[6:7], v[148:149], s[70:71] op_sel_hi:[1,0]
	v_pk_mul_f32 v[8:9], v[146:147], s[70:71] op_sel_hi:[1,0]
	v_cvt_pk_bf16_f32 v17, v4, v5
	v_cvt_pk_bf16_f32 v18, v2, v3
	v_cvt_pk_bf16_f32 v8, v8, v9
	v_cvt_pk_bf16_f32 v6, v6, v7
	v_cndmask_b32_e64 v2, v16, v6, s[36:37]
	v_cndmask_b32_e64 v3, v14, v18, s[36:37]
	v_cndmask_b32_e64 v4, v15, v8, s[36:37]
	v_cndmask_b32_e64 v5, v13, v17, s[36:37]
	v_mov_b32_dpp v7, v3 quad_perm:[1,0,3,2] row_mask:0xf bank_mask:0xf bound_ctrl:1
	v_mov_b32_dpp v20, v4 quad_perm:[1,0,3,2] row_mask:0xf bank_mask:0xf bound_ctrl:1
	v_mov_b32_dpp v19, v5 quad_perm:[1,0,3,2] row_mask:0xf bank_mask:0xf bound_ctrl:1
	v_mov_b32_dpp v9, v2 quad_perm:[1,0,3,2] row_mask:0xf bank_mask:0xf bound_ctrl:1
	v_cndmask_b32_e64 v5, v9, v16, s[36:37]
	v_cndmask_b32_e64 v3, v7, v14, s[36:37]
	v_cndmask_b32_e64 v4, v20, v15, s[36:37]
	v_cndmask_b32_e64 v2, v19, v13, s[36:37]
	s_lshl_b64 s[68:69], s[0:1], 1
	v_cndmask_b32_e64 v9, v6, v9, s[36:37]
	v_cndmask_b32_e64 v7, v18, v7, s[36:37]
	v_cndmask_b32_e64 v8, v8, v20, s[36:37]
	v_cndmask_b32_e64 v6, v17, v19, s[36:37]
	global_store_dwordx4 v[10:11], v[2:5], off nt
	s_nop 1
	v_lshl_add_u64 v[2:3], v[10:11], 0, s[68:69]
	global_store_dwordx4 v[2:3], v[6:9], off nt
	v_add_u32_e32 v2, 16, v12
	v_ashrrev_i32_e32 v3, 31, v2
	v_mul_lo_u32 v4, s0, v3
	v_mul_lo_u32 v5, s1, v2
	v_mad_u64_u32 v[2:3], s[4:5], s0, v2, 0
	v_add3_u32 v3, v3, v4, v5
	v_lshl_add_u64 v[10:11], v[2:3], 1, v[0:1]
	v_pk_mul_f32 v[2:3], v[144:145], s[70:71] op_sel_hi:[1,0]
	v_pk_mul_f32 v[4:5], v[142:143], s[70:71] op_sel_hi:[1,0]
	v_pk_mul_f32 v[6:7], v[140:141], s[70:71] op_sel_hi:[1,0]
	v_pk_mul_f32 v[8:9], v[138:139], s[70:71] op_sel_hi:[1,0]
	v_cvt_pk_bf16_f32 v13, v4, v5
	v_cvt_pk_bf16_f32 v14, v2, v3
	v_cvt_pk_bf16_f32 v15, v8, v9
	v_cvt_pk_bf16_f32 v16, v6, v7
	v_pk_mul_f32 v[2:3], v[136:137], s[70:71] op_sel_hi:[1,0]
	v_pk_mul_f32 v[4:5], v[134:135], s[70:71] op_sel_hi:[1,0]
	v_pk_mul_f32 v[6:7], v[132:133], s[70:71] op_sel_hi:[1,0]
	v_pk_mul_f32 v[8:9], v[130:131], s[70:71] op_sel_hi:[1,0]
	v_cvt_pk_bf16_f32 v17, v4, v5
	v_cvt_pk_bf16_f32 v18, v2, v3
	v_cvt_pk_bf16_f32 v8, v8, v9
	v_cvt_pk_bf16_f32 v6, v6, v7
	v_cndmask_b32_e64 v2, v16, v6, s[36:37]
	v_cndmask_b32_e64 v3, v14, v18, s[36:37]
	v_cndmask_b32_e64 v4, v15, v8, s[36:37]
	v_cndmask_b32_e64 v5, v13, v17, s[36:37]
	v_mov_b32_dpp v7, v3 quad_perm:[1,0,3,2] row_mask:0xf bank_mask:0xf bound_ctrl:1
	v_mov_b32_dpp v20, v4 quad_perm:[1,0,3,2] row_mask:0xf bank_mask:0xf bound_ctrl:1
	v_mov_b32_dpp v19, v5 quad_perm:[1,0,3,2] row_mask:0xf bank_mask:0xf bound_ctrl:1
	v_mov_b32_dpp v9, v2 quad_perm:[1,0,3,2] row_mask:0xf bank_mask:0xf bound_ctrl:1
	v_cndmask_b32_e64 v5, v9, v16, s[36:37]
	v_cndmask_b32_e64 v3, v7, v14, s[36:37]
	v_cndmask_b32_e64 v4, v20, v15, s[36:37]
	v_cndmask_b32_e64 v2, v19, v13, s[36:37]
	v_cndmask_b32_e64 v9, v6, v9, s[36:37]
	v_cndmask_b32_e64 v7, v18, v7, s[36:37]
	v_cndmask_b32_e64 v8, v8, v20, s[36:37]
	v_cndmask_b32_e64 v6, v17, v19, s[36:37]
	global_store_dwordx4 v[10:11], v[2:5], off nt
	s_nop 1
	v_lshl_add_u64 v[2:3], v[10:11], 0, s[68:69]
	global_store_dwordx4 v[2:3], v[6:9], off nt
	v_add_u32_e32 v2, 32, v12
	v_ashrrev_i32_e32 v3, 31, v2
	v_mul_lo_u32 v4, s0, v3
	v_mul_lo_u32 v5, s1, v2
	v_mad_u64_u32 v[2:3], s[4:5], s0, v2, 0
	v_add3_u32 v3, v3, v4, v5
	v_lshl_add_u64 v[10:11], v[2:3], 1, v[0:1]
	v_pk_mul_f32 v[2:3], v[128:129], s[70:71] op_sel_hi:[1,0]
	v_pk_mul_f32 v[4:5], v[126:127], s[70:71] op_sel_hi:[1,0]
	v_pk_mul_f32 v[6:7], v[124:125], s[70:71] op_sel_hi:[1,0]
	v_pk_mul_f32 v[8:9], v[122:123], s[70:71] op_sel_hi:[1,0]
	v_cvt_pk_bf16_f32 v13, v4, v5
	v_cvt_pk_bf16_f32 v14, v2, v3
	v_cvt_pk_bf16_f32 v15, v8, v9
	v_cvt_pk_bf16_f32 v16, v6, v7
	v_pk_mul_f32 v[2:3], v[120:121], s[70:71] op_sel_hi:[1,0]
	v_pk_mul_f32 v[4:5], v[118:119], s[70:71] op_sel_hi:[1,0]
	v_pk_mul_f32 v[6:7], v[116:117], s[70:71] op_sel_hi:[1,0]
	v_pk_mul_f32 v[8:9], v[114:115], s[70:71] op_sel_hi:[1,0]
	v_cvt_pk_bf16_f32 v17, v4, v5
	v_cvt_pk_bf16_f32 v18, v2, v3
	v_cvt_pk_bf16_f32 v8, v8, v9
	v_cvt_pk_bf16_f32 v6, v6, v7
	v_cndmask_b32_e64 v2, v16, v6, s[36:37]
	v_cndmask_b32_e64 v3, v14, v18, s[36:37]
	v_cndmask_b32_e64 v4, v15, v8, s[36:37]
	v_cndmask_b32_e64 v5, v13, v17, s[36:37]
	v_mov_b32_dpp v7, v3 quad_perm:[1,0,3,2] row_mask:0xf bank_mask:0xf bound_ctrl:1
	v_mov_b32_dpp v20, v4 quad_perm:[1,0,3,2] row_mask:0xf bank_mask:0xf bound_ctrl:1
	v_mov_b32_dpp v19, v5 quad_perm:[1,0,3,2] row_mask:0xf bank_mask:0xf bound_ctrl:1
	v_mov_b32_dpp v9, v2 quad_perm:[1,0,3,2] row_mask:0xf bank_mask:0xf bound_ctrl:1
	v_cndmask_b32_e64 v5, v9, v16, s[36:37]
	v_cndmask_b32_e64 v3, v7, v14, s[36:37]
	v_cndmask_b32_e64 v4, v20, v15, s[36:37]
	v_cndmask_b32_e64 v2, v19, v13, s[36:37]
	v_cndmask_b32_e64 v9, v6, v9, s[36:37]
	v_cndmask_b32_e64 v7, v18, v7, s[36:37]
	v_cndmask_b32_e64 v8, v8, v20, s[36:37]
	v_cndmask_b32_e64 v6, v17, v19, s[36:37]
	global_store_dwordx4 v[10:11], v[2:5], off nt
	s_nop 1
	v_lshl_add_u64 v[2:3], v[10:11], 0, s[68:69]
	global_store_dwordx4 v[2:3], v[6:9], off nt
	v_add_u32_e32 v2, 48, v12
	v_ashrrev_i32_e32 v3, 31, v2
	v_mul_lo_u32 v4, s0, v3
	v_mul_lo_u32 v5, s1, v2
	v_mad_u64_u32 v[2:3], s[4:5], s0, v2, 0
	v_add3_u32 v3, v3, v4, v5
	v_lshl_add_u64 v[10:11], v[2:3], 1, v[0:1]
	v_pk_mul_f32 v[2:3], v[112:113], s[70:71] op_sel_hi:[1,0]
	v_pk_mul_f32 v[4:5], v[110:111], s[70:71] op_sel_hi:[1,0]
	v_pk_mul_f32 v[6:7], v[108:109], s[70:71] op_sel_hi:[1,0]
	v_pk_mul_f32 v[8:9], v[106:107], s[70:71] op_sel_hi:[1,0]
	v_cvt_pk_bf16_f32 v13, v4, v5
	v_cvt_pk_bf16_f32 v14, v2, v3
	v_cvt_pk_bf16_f32 v15, v8, v9
	v_cvt_pk_bf16_f32 v16, v6, v7
	v_pk_mul_f32 v[2:3], v[104:105], s[70:71] op_sel_hi:[1,0]
	v_pk_mul_f32 v[4:5], v[102:103], s[70:71] op_sel_hi:[1,0]
	v_pk_mul_f32 v[6:7], v[100:101], s[70:71] op_sel_hi:[1,0]
	v_pk_mul_f32 v[8:9], v[98:99], s[70:71] op_sel_hi:[1,0]
	v_cvt_pk_bf16_f32 v17, v4, v5
	v_cvt_pk_bf16_f32 v18, v2, v3
	v_cvt_pk_bf16_f32 v8, v8, v9
	v_cvt_pk_bf16_f32 v6, v6, v7
	v_cndmask_b32_e64 v2, v16, v6, s[36:37]
	v_cndmask_b32_e64 v3, v14, v18, s[36:37]
	v_cndmask_b32_e64 v4, v15, v8, s[36:37]
	v_cndmask_b32_e64 v5, v13, v17, s[36:37]
	v_mov_b32_dpp v7, v3 quad_perm:[1,0,3,2] row_mask:0xf bank_mask:0xf bound_ctrl:1
	v_mov_b32_dpp v20, v4 quad_perm:[1,0,3,2] row_mask:0xf bank_mask:0xf bound_ctrl:1
	v_mov_b32_dpp v19, v5 quad_perm:[1,0,3,2] row_mask:0xf bank_mask:0xf bound_ctrl:1
	v_mov_b32_dpp v9, v2 quad_perm:[1,0,3,2] row_mask:0xf bank_mask:0xf bound_ctrl:1
	v_cndmask_b32_e64 v5, v9, v16, s[36:37]
	v_cndmask_b32_e64 v3, v7, v14, s[36:37]
	v_cndmask_b32_e64 v4, v20, v15, s[36:37]
	v_cndmask_b32_e64 v2, v19, v13, s[36:37]
	v_cndmask_b32_e64 v9, v6, v9, s[36:37]
	v_cndmask_b32_e64 v7, v18, v7, s[36:37]
	v_cndmask_b32_e64 v8, v8, v20, s[36:37]
	v_cndmask_b32_e64 v6, v17, v19, s[36:37]
	global_store_dwordx4 v[10:11], v[2:5], off nt
	s_nop 1
	v_lshl_add_u64 v[2:3], v[10:11], 0, s[68:69]
	global_store_dwordx4 v[2:3], v[6:9], off nt
	v_add_u32_e32 v2, 0x80, v12
	v_ashrrev_i32_e32 v3, 31, v2
	v_mul_lo_u32 v4, s0, v3
	v_mul_lo_u32 v5, s1, v2
	v_mad_u64_u32 v[2:3], s[4:5], s0, v2, 0
	v_add3_u32 v3, v3, v4, v5
	v_lshl_add_u64 v[10:11], v[2:3], 1, v[0:1]
	v_pk_mul_f32 v[2:3], v[96:97], s[70:71] op_sel_hi:[1,0]
	v_pk_mul_f32 v[4:5], v[94:95], s[70:71] op_sel_hi:[1,0]
	v_pk_mul_f32 v[6:7], v[92:93], s[70:71] op_sel_hi:[1,0]
	v_pk_mul_f32 v[8:9], v[90:91], s[70:71] op_sel_hi:[1,0]
	v_cvt_pk_bf16_f32 v13, v4, v5
	v_cvt_pk_bf16_f32 v14, v2, v3
	v_cvt_pk_bf16_f32 v15, v8, v9
	v_cvt_pk_bf16_f32 v16, v6, v7
	v_pk_mul_f32 v[2:3], v[88:89], s[70:71] op_sel_hi:[1,0]
	v_pk_mul_f32 v[4:5], v[86:87], s[70:71] op_sel_hi:[1,0]
	v_pk_mul_f32 v[6:7], v[84:85], s[70:71] op_sel_hi:[1,0]
	v_pk_mul_f32 v[8:9], v[82:83], s[70:71] op_sel_hi:[1,0]
	v_cvt_pk_bf16_f32 v17, v4, v5
	v_cvt_pk_bf16_f32 v18, v2, v3
	v_cvt_pk_bf16_f32 v8, v8, v9
	v_cvt_pk_bf16_f32 v6, v6, v7
	v_cndmask_b32_e64 v2, v16, v6, s[36:37]
	v_cndmask_b32_e64 v3, v14, v18, s[36:37]
	v_cndmask_b32_e64 v4, v15, v8, s[36:37]
	v_cndmask_b32_e64 v5, v13, v17, s[36:37]
	v_mov_b32_dpp v7, v3 quad_perm:[1,0,3,2] row_mask:0xf bank_mask:0xf bound_ctrl:1
	v_mov_b32_dpp v20, v4 quad_perm:[1,0,3,2] row_mask:0xf bank_mask:0xf bound_ctrl:1
	v_mov_b32_dpp v19, v5 quad_perm:[1,0,3,2] row_mask:0xf bank_mask:0xf bound_ctrl:1
	v_mov_b32_dpp v9, v2 quad_perm:[1,0,3,2] row_mask:0xf bank_mask:0xf bound_ctrl:1
	v_cndmask_b32_e64 v5, v9, v16, s[36:37]
	v_cndmask_b32_e64 v3, v7, v14, s[36:37]
	v_cndmask_b32_e64 v4, v20, v15, s[36:37]
	v_cndmask_b32_e64 v2, v19, v13, s[36:37]
	v_cndmask_b32_e64 v9, v6, v9, s[36:37]
	v_cndmask_b32_e64 v7, v18, v7, s[36:37]
	v_cndmask_b32_e64 v8, v8, v20, s[36:37]
	v_cndmask_b32_e64 v6, v17, v19, s[36:37]
	global_store_dwordx4 v[10:11], v[2:5], off nt
	s_nop 1
	v_lshl_add_u64 v[2:3], v[10:11], 0, s[68:69]
	global_store_dwordx4 v[2:3], v[6:9], off nt
	v_add_u32_e32 v2, 0x90, v12
	v_ashrrev_i32_e32 v3, 31, v2
	v_mul_lo_u32 v4, s0, v3
	v_mul_lo_u32 v5, s1, v2
	v_mad_u64_u32 v[2:3], s[4:5], s0, v2, 0
	v_add3_u32 v3, v3, v4, v5
	v_lshl_add_u64 v[10:11], v[2:3], 1, v[0:1]
	v_pk_mul_f32 v[2:3], v[72:73], s[70:71] op_sel_hi:[1,0]
	v_pk_mul_f32 v[4:5], v[70:71], s[70:71] op_sel_hi:[1,0]
	v_pk_mul_f32 v[6:7], v[68:69], s[70:71] op_sel_hi:[1,0]
	v_pk_mul_f32 v[8:9], v[66:67], s[70:71] op_sel_hi:[1,0]
	v_cvt_pk_bf16_f32 v13, v4, v5
	v_cvt_pk_bf16_f32 v14, v2, v3
	v_cvt_pk_bf16_f32 v15, v8, v9
	v_cvt_pk_bf16_f32 v16, v6, v7
	v_pk_mul_f32 v[2:3], v[64:65], s[70:71] op_sel_hi:[1,0]
	v_pk_mul_f32 v[4:5], v[62:63], s[70:71] op_sel_hi:[1,0]
	v_pk_mul_f32 v[6:7], v[52:53], s[70:71] op_sel_hi:[1,0]
	v_pk_mul_f32 v[8:9], v[50:51], s[70:71] op_sel_hi:[1,0]
	v_cvt_pk_bf16_f32 v17, v4, v5
	v_cvt_pk_bf16_f32 v18, v2, v3
	v_cvt_pk_bf16_f32 v8, v8, v9
	v_cvt_pk_bf16_f32 v6, v6, v7
	v_cndmask_b32_e64 v2, v16, v6, s[36:37]
	v_cndmask_b32_e64 v3, v14, v18, s[36:37]
	v_cndmask_b32_e64 v4, v15, v8, s[36:37]
	v_cndmask_b32_e64 v5, v13, v17, s[36:37]
	v_mov_b32_dpp v7, v3 quad_perm:[1,0,3,2] row_mask:0xf bank_mask:0xf bound_ctrl:1
	v_mov_b32_dpp v20, v4 quad_perm:[1,0,3,2] row_mask:0xf bank_mask:0xf bound_ctrl:1
	v_mov_b32_dpp v19, v5 quad_perm:[1,0,3,2] row_mask:0xf bank_mask:0xf bound_ctrl:1
	v_mov_b32_dpp v9, v2 quad_perm:[1,0,3,2] row_mask:0xf bank_mask:0xf bound_ctrl:1
	v_cndmask_b32_e64 v5, v9, v16, s[36:37]
	v_cndmask_b32_e64 v3, v7, v14, s[36:37]
	v_cndmask_b32_e64 v4, v20, v15, s[36:37]
	v_cndmask_b32_e64 v2, v19, v13, s[36:37]
	v_cndmask_b32_e64 v9, v6, v9, s[36:37]
	v_cndmask_b32_e64 v7, v18, v7, s[36:37]
	v_cndmask_b32_e64 v8, v8, v20, s[36:37]
	v_cndmask_b32_e64 v6, v17, v19, s[36:37]
	global_store_dwordx4 v[10:11], v[2:5], off nt
	s_nop 1
	v_lshl_add_u64 v[2:3], v[10:11], 0, s[68:69]
	global_store_dwordx4 v[2:3], v[6:9], off nt
	v_add_u32_e32 v2, 0xa0, v12
	v_ashrrev_i32_e32 v3, 31, v2
	v_mul_lo_u32 v4, s0, v3
	v_mul_lo_u32 v5, s1, v2
	v_mad_u64_u32 v[2:3], s[4:5], s0, v2, 0
	v_add3_u32 v3, v3, v4, v5
	v_lshl_add_u64 v[10:11], v[2:3], 1, v[0:1]
	v_pk_mul_f32 v[2:3], v[46:47], s[70:71] op_sel_hi:[1,0]
	v_pk_mul_f32 v[4:5], v[44:45], s[70:71] op_sel_hi:[1,0]
	v_pk_mul_f32 v[6:7], v[42:43], s[70:71] op_sel_hi:[1,0]
	v_pk_mul_f32 v[8:9], v[40:41], s[70:71] op_sel_hi:[1,0]
	v_cvt_pk_bf16_f32 v13, v4, v5
	v_cvt_pk_bf16_f32 v14, v2, v3
	v_cvt_pk_bf16_f32 v15, v8, v9
	v_cvt_pk_bf16_f32 v16, v6, v7
	v_pk_mul_f32 v[2:3], v[80:81], s[70:71] op_sel_hi:[1,0]
	v_pk_mul_f32 v[4:5], v[78:79], s[70:71] op_sel_hi:[1,0]
	v_pk_mul_f32 v[6:7], v[76:77], s[70:71] op_sel_hi:[1,0]
	v_pk_mul_f32 v[8:9], v[74:75], s[70:71] op_sel_hi:[1,0]
	v_cvt_pk_bf16_f32 v17, v4, v5
	v_cvt_pk_bf16_f32 v18, v2, v3
	v_cvt_pk_bf16_f32 v8, v8, v9
	v_cvt_pk_bf16_f32 v6, v6, v7
	v_cndmask_b32_e64 v2, v16, v6, s[36:37]
	v_cndmask_b32_e64 v3, v14, v18, s[36:37]
	v_cndmask_b32_e64 v4, v15, v8, s[36:37]
	v_cndmask_b32_e64 v5, v13, v17, s[36:37]
	v_mov_b32_dpp v7, v3 quad_perm:[1,0,3,2] row_mask:0xf bank_mask:0xf bound_ctrl:1
	v_mov_b32_dpp v20, v4 quad_perm:[1,0,3,2] row_mask:0xf bank_mask:0xf bound_ctrl:1
	v_mov_b32_dpp v19, v5 quad_perm:[1,0,3,2] row_mask:0xf bank_mask:0xf bound_ctrl:1
	v_mov_b32_dpp v9, v2 quad_perm:[1,0,3,2] row_mask:0xf bank_mask:0xf bound_ctrl:1
	v_cndmask_b32_e64 v5, v9, v16, s[36:37]
	v_cndmask_b32_e64 v3, v7, v14, s[36:37]
	v_cndmask_b32_e64 v4, v20, v15, s[36:37]
	v_cndmask_b32_e64 v2, v19, v13, s[36:37]
	v_cndmask_b32_e64 v9, v6, v9, s[36:37]
	v_cndmask_b32_e64 v7, v18, v7, s[36:37]
	v_cndmask_b32_e64 v8, v8, v20, s[36:37]
	v_cndmask_b32_e64 v6, v17, v19, s[36:37]
	global_store_dwordx4 v[10:11], v[2:5], off nt
	s_nop 1
	v_lshl_add_u64 v[2:3], v[10:11], 0, s[68:69]
	global_store_dwordx4 v[2:3], v[6:9], off nt
	v_add_u32_e32 v2, 0xb0, v12
	v_ashrrev_i32_e32 v3, 31, v2
	v_mul_lo_u32 v4, s0, v3
	v_mul_lo_u32 v5, s1, v2
	v_mad_u64_u32 v[2:3], s[0:1], s0, v2, 0
	v_add3_u32 v3, v3, v4, v5
	v_lshl_add_u64 v[8:9], v[2:3], 1, v[0:1]
	v_pk_mul_f32 v[0:1], v[38:39], s[70:71] op_sel_hi:[1,0]
	v_pk_mul_f32 v[2:3], v[36:37], s[70:71] op_sel_hi:[1,0]
	v_pk_mul_f32 v[4:5], v[34:35], s[70:71] op_sel_hi:[1,0]
	v_pk_mul_f32 v[6:7], v[32:33], s[70:71] op_sel_hi:[1,0]
	v_cvt_pk_bf16_f32 v10, v2, v3
	v_cvt_pk_bf16_f32 v11, v0, v1
	v_cvt_pk_bf16_f32 v12, v6, v7
	v_cvt_pk_bf16_f32 v13, v4, v5
	v_pk_mul_f32 v[0:1], v[60:61], s[70:71] op_sel_hi:[1,0]
	v_pk_mul_f32 v[2:3], v[58:59], s[70:71] op_sel_hi:[1,0]
	v_pk_mul_f32 v[4:5], v[56:57], s[70:71] op_sel_hi:[1,0]
	v_pk_mul_f32 v[6:7], v[54:55], s[70:71] op_sel_hi:[1,0]
	v_cvt_pk_bf16_f32 v14, v2, v3
	v_cvt_pk_bf16_f32 v15, v0, v1
	v_cvt_pk_bf16_f32 v6, v6, v7
	v_cvt_pk_bf16_f32 v4, v4, v5
	v_cndmask_b32_e64 v0, v13, v4, s[36:37]
	v_cndmask_b32_e64 v1, v11, v15, s[36:37]
	v_cndmask_b32_e64 v2, v12, v6, s[36:37]
	v_cndmask_b32_e64 v3, v10, v14, s[36:37]
	v_mov_b32_dpp v5, v1 quad_perm:[1,0,3,2] row_mask:0xf bank_mask:0xf bound_ctrl:1
	v_mov_b32_dpp v17, v2 quad_perm:[1,0,3,2] row_mask:0xf bank_mask:0xf bound_ctrl:1
	v_mov_b32_dpp v16, v3 quad_perm:[1,0,3,2] row_mask:0xf bank_mask:0xf bound_ctrl:1
	v_mov_b32_dpp v7, v0 quad_perm:[1,0,3,2] row_mask:0xf bank_mask:0xf bound_ctrl:1
	v_cndmask_b32_e64 v3, v7, v13, s[36:37]
	v_cndmask_b32_e64 v1, v5, v11, s[36:37]
	v_cndmask_b32_e64 v2, v17, v12, s[36:37]
	v_cndmask_b32_e64 v0, v16, v10, s[36:37]
	v_cndmask_b32_e64 v7, v4, v7, s[36:37]
	v_cndmask_b32_e64 v5, v15, v5, s[36:37]
	v_cndmask_b32_e64 v6, v6, v17, s[36:37]
	v_cndmask_b32_e64 v4, v14, v16, s[36:37]
	global_store_dwordx4 v[8:9], v[0:3], off nt
	s_nop 1
	v_lshl_add_u64 v[0:1], v[8:9], 0, s[68:69]
	global_store_dwordx4 v[0:1], v[4:7], off nt
	s_andn2_b64 vcc, exec, s[38:39]
	s_mov_b64 s[0:1], -1
	s_cbranch_vccnz .LBB0_134

.LBB0_445:
	v_lshl_add_u64 v[50:51], v[218:219], 0, s[58:59]
	global_load_dwordx4 v[188:191], v[50:51], off nt
	v_lshl_add_u64 v[50:51], v[218:219], 0, s[60:61]
	global_load_dwordx4 v[202:205], v[50:51], off nt
	v_lshl_add_u64 v[50:51], v[218:219], 0, s[62:63]
	global_load_dwordx4 v[184:187], v[50:51], off nt
	v_lshl_add_u64 v[50:51], v[218:219], 0, s[70:71]
	global_load_dwordx4 v[180:183], v[50:51], off nt
	v_lshl_add_u64 v[50:51], v[218:219], 0, s[78:79]
	global_load_dwordx4 v[176:179], v[50:51], off nt
	v_lshl_add_u64 v[50:51], v[218:219], 0, s[76:77]
	global_load_dwordx4 v[172:175], v[50:51], off nt
	v_lshl_add_u64 v[50:51], v[218:219], 0, s[74:75]
	global_load_dwordx4 v[168:171], v[50:51], off nt
	v_lshl_add_u64 v[50:51], v[218:219], 0, s[72:73]
	global_load_dwordx4 v[164:167], v[50:51], off nt
	v_lshl_add_u64 v[50:51], v[218:219], 0, s[68:69]
	s_or_b32 s0, s4, s7
	global_load_dwordx4 v[160:163], v[50:51], off nt
	v_lshl_add_u64 v[50:51], v[218:219], 0, s[66:67]
	s_ashr_i32 s1, s0, 31
	global_load_dwordx4 v[156:159], v[50:51], off nt
	v_lshl_add_u64 v[50:51], v[218:219], 0, s[64:65]
	s_lshl_b64 s[0:1], s[0:1], 10
	global_load_dwordx4 v[148:151], v[50:51], off nt
	v_lshl_add_u64 v[50:51], v[218:219], 0, s[0:1]
	s_or_b32 s0, s5, s40
	s_ashr_i32 s1, s0, 31
	s_lshl_b64 s[0:1], s[0:1], 10
	global_load_dwordx4 v[152:155], v[50:51], off nt
	v_lshl_add_u64 v[50:51], v[218:219], 0, s[0:1]
	s_or_b32 s0, s4, s40
	s_ashr_i32 s1, s0, 31
	s_lshl_b64 s[0:1], s[0:1], 10
	global_load_dwordx4 v[140:143], v[50:51], off nt
	v_lshl_add_u64 v[50:51], v[218:219], 0, s[0:1]
	s_or_b32 s0, s5, s41
	s_ashr_i32 s1, s0, 31
	s_lshl_b64 s[0:1], s[0:1], 10
	global_load_dwordx4 v[144:147], v[50:51], off nt
	v_lshl_add_u64 v[50:51], v[218:219], 0, s[0:1]
	s_or_b32 s0, s4, s41
	s_ashr_i32 s1, s0, 31
	s_lshl_b64 s[0:1], s[0:1], 10
	global_load_dwordx4 v[132:135], v[50:51], off nt
	v_lshl_add_u64 v[50:51], v[218:219], 0, s[0:1]
	global_load_dwordx4 v[136:139], v[50:51], off nt
	v_lshl_add_u32 v222, s36, 8, v199
	v_ashrrev_i32_e32 v223, 31, v222
	s_lshl_b32 vcc_lo, s20, 8
	s_ashr_i32 vcc_hi, vcc_lo, 31
	s_mov_b64 s[0:1], 0x20000
	s_waitcnt vmcnt(0)
	v_lshlrev_b32_e32 v224, 16, v188
	v_and_b32_e32 v225, 0xffff0000, v188
	v_lshlrev_b32_e32 v188, 16, v189
	v_and_b32_e32 v189, 0xffff0000, v189
	v_lshlrev_b32_e32 v194, 16, v202
	v_and_b32_e32 v195, 0xffff0000, v202
	v_lshlrev_b32_e32 v192, 16, v203
	v_and_b32_e32 v193, 0xffff0000, v203
	v_pk_mul_f32 v[202:203], v[128:129], v[224:225]
	v_pk_mul_f32 v[188:189], v[130:131], v[188:189]
	v_pk_mul_f32 v[202:203], v[202:203], s[26:27] op_sel_hi:[1,0]
	v_pk_mul_f32 v[188:189], v[188:189], s[26:27] op_sel_hi:[1,0]
	v_med3_f32 v48, v202, s11, v232
	v_med3_f32 v202, v203, s11, v232
	v_med3_f32 v203, v188, s11, v232
	v_mov_b32_e32 v188, v49
	v_cvt_pk_fp8_f32 v188, v48, v202
	v_lshlrev_b32_e32 v226, 16, v190
	v_and_b32_e32 v227, 0xffff0000, v190
	v_med3_f32 v189, v189, s11, v232
	v_cvt_pk_fp8_f32 v188, v203, v189 op_sel:[0,0,1]
	v_pk_mul_f32 v[202:203], v[120:121], v[226:227]
	v_pk_mul_f32 v[194:195], v[64:65], v[194:195]
	v_pk_mul_f32 v[202:203], v[202:203], s[26:27] op_sel_hi:[1,0]
	v_pk_mul_f32 v[192:193], v[66:67], v[192:193]
	v_med3_f32 v48, v202, s11, v232
	v_med3_f32 v202, v203, s11, v232
	v_mov_b32_e32 v189, v49
	v_pk_mul_f32 v[192:193], v[192:193], s[26:27] op_sel_hi:[1,0]
	v_pk_mul_f32 v[194:195], v[194:195], s[26:27] op_sel_hi:[1,0]
	v_cvt_pk_fp8_f32 v189, v48, v202
	v_med3_f32 v48, v194, s11, v232
	v_med3_f32 v194, v195, s11, v232
	v_med3_f32 v195, v192, s11, v232
	v_mov_b32_e32 v192, v49
	v_cvt_pk_fp8_f32 v192, v48, v194
	v_lshlrev_b32_e32 v234, 16, v191
	v_and_b32_e32 v235, 0xffff0000, v191
	v_lshlrev_b32_e32 v190, 16, v204
	v_and_b32_e32 v191, 0xffff0000, v204
	v_pk_mul_f32 v[190:191], v[60:61], v[190:191]
	v_med3_f32 v193, v193, s11, v232
	v_pk_mul_f32 v[190:191], v[190:191], s[26:27] op_sel_hi:[1,0]
	v_cvt_pk_fp8_f32 v192, v195, v193 op_sel:[0,0,1]
	v_med3_f32 v48, v190, s11, v232
	v_med3_f32 v190, v191, s11, v232
	v_mov_b32_e32 v193, v49
	v_lshlrev_b32_e32 v50, 16, v205
	v_and_b32_e32 v51, 0xffff0000, v205
	v_cvt_pk_fp8_f32 v193, v48, v190
	v_pk_mul_f32 v[50:51], v[62:63], v[50:51]
	v_mov_b32_e32 v190, v49
	v_pk_mul_f32 v[50:51], v[50:51], s[26:27] op_sel_hi:[1,0]
	v_lshlrev_b32_e32 v194, 16, v186
	v_med3_f32 v50, v50, s11, v232
	v_med3_f32 v51, v51, s11, v232
	v_cvt_pk_fp8_f32 v193, v50, v51 op_sel:[0,0,1]
	v_lshlrev_b32_e32 v50, 16, v184
	v_and_b32_e32 v51, 0xffff0000, v184
	v_pk_mul_f32 v[50:51], v[112:113], v[50:51]
	v_lshlrev_b32_e32 v184, 16, v185
	v_pk_mul_f32 v[50:51], v[50:51], s[26:27] op_sel_hi:[1,0]
	v_and_b32_e32 v185, 0xffff0000, v185
	v_med3_f32 v48, v50, s11, v232
	v_med3_f32 v50, v51, s11, v232
	v_cvt_pk_fp8_f32 v190, v48, v50
	v_pk_mul_f32 v[184:185], v[114:115], v[184:185]
	v_and_b32_e32 v195, 0xffff0000, v186
	v_pk_mul_f32 v[184:185], v[184:185], s[26:27] op_sel_hi:[1,0]
	v_mov_b32_e32 v191, v49
	v_med3_f32 v51, v184, s11, v232
	v_med3_f32 v184, v185, s11, v232
	v_cvt_pk_fp8_f32 v190, v51, v184 op_sel:[0,0,1]
	v_pk_mul_f32 v[50:51], v[104:105], v[194:195]
	v_pk_mul_f32 v[204:205], v[122:123], v[234:235]
	v_pk_mul_f32 v[50:51], v[50:51], s[26:27] op_sel_hi:[1,0]
	v_lshlrev_b32_e32 v186, 16, v187
	v_med3_f32 v48, v50, s11, v232
	v_med3_f32 v50, v51, s11, v232
	v_and_b32_e32 v187, 0xffff0000, v187
	v_cvt_pk_fp8_f32 v191, v48, v50
	v_pk_mul_f32 v[204:205], v[204:205], s[26:27] op_sel_hi:[1,0]
	v_pk_mul_f32 v[184:185], v[106:107], v[186:187]
	v_med3_f32 v203, v204, s11, v232
	v_med3_f32 v204, v205, s11, v232
	v_pk_mul_f32 v[184:185], v[184:185], s[26:27] op_sel_hi:[1,0]
	v_cvt_pk_fp8_f32 v189, v203, v204 op_sel:[0,0,1]
	v_lshlrev_b32_e32 v202, 16, v180
	v_and_b32_e32 v203, 0xffff0000, v180
	v_med3_f32 v51, v184, s11, v232
	v_med3_f32 v184, v185, s11, v232
	v_cvt_pk_fp8_f32 v191, v51, v184 op_sel:[0,0,1]
	v_pk_mul_f32 v[50:51], v[56:57], v[202:203]
	v_mov_b32_e32 v194, v49
	v_pk_mul_f32 v[50:51], v[50:51], s[26:27] op_sel_hi:[1,0]
	v_lshlrev_b32_e32 v180, 16, v181
	v_med3_f32 v48, v50, s11, v232
	v_med3_f32 v50, v51, s11, v232
	v_and_b32_e32 v181, 0xffff0000, v181
	v_cvt_pk_fp8_f32 v194, v48, v50
	v_pk_mul_f32 v[180:181], v[58:59], v[180:181]
	v_lshlrev_b32_e32 v204, 16, v182
	v_pk_mul_f32 v[180:181], v[180:181], s[26:27] op_sel_hi:[1,0]
	v_and_b32_e32 v205, 0xffff0000, v182
	v_med3_f32 v51, v180, s11, v232
	v_med3_f32 v180, v181, s11, v232
	v_cvt_pk_fp8_f32 v194, v51, v180 op_sel:[0,0,1]
	v_pk_mul_f32 v[50:51], v[52:53], v[204:205]
	v_mov_b32_e32 v195, v49
	v_pk_mul_f32 v[50:51], v[50:51], s[26:27] op_sel_hi:[1,0]
	v_lshlrev_b32_e32 v182, 16, v183
	v_med3_f32 v48, v50, s11, v232
	v_med3_f32 v50, v51, s11, v232
	v_and_b32_e32 v183, 0xffff0000, v183
	v_cvt_pk_fp8_f32 v195, v48, v50
	v_pk_mul_f32 v[180:181], v[54:55], v[182:183]
	v_lshlrev_b32_e32 v184, 16, v172
	v_pk_mul_f32 v[180:181], v[180:181], s[26:27] op_sel_hi:[1,0]
	v_and_b32_e32 v185, 0xffff0000, v172
	v_med3_f32 v51, v180, s11, v232
	v_med3_f32 v180, v181, s11, v232
	v_cvt_pk_fp8_f32 v195, v51, v180 op_sel:[0,0,1]
	v_lshlrev_b32_e32 v180, 16, v176
	v_and_b32_e32 v181, 0xffff0000, v176
	v_lshlrev_b32_e32 v186, 16, v173
	v_and_b32_e32 v187, 0xffff0000, v173
	v_pk_mul_f32 v[172:173], v[96:97], v[180:181]
	v_lshlrev_b32_e32 v176, 16, v177
	v_pk_mul_f32 v[172:173], v[172:173], s[26:27] op_sel_hi:[1,0]
	v_and_b32_e32 v177, 0xffff0000, v177
	v_med3_f32 v48, v172, s11, v232
	v_med3_f32 v173, v173, s11, v232
	v_mov_b32_e32 v172, v49
	v_cvt_pk_fp8_f32 v172, v48, v173
	v_pk_mul_f32 v[176:177], v[98:99], v[176:177]
	v_lshlrev_b32_e32 v182, 16, v178
	v_pk_mul_f32 v[176:177], v[176:177], s[26:27] op_sel_hi:[1,0]
	v_and_b32_e32 v183, 0xffff0000, v178
	v_med3_f32 v176, v176, s11, v232
	v_med3_f32 v177, v177, s11, v232
	v_cvt_pk_fp8_f32 v172, v176, v177 op_sel:[0,0,1]
	v_pk_mul_f32 v[176:177], v[88:89], v[182:183]
	v_mov_b32_e32 v173, v49
	v_pk_mul_f32 v[176:177], v[176:177], s[26:27] op_sel_hi:[1,0]
	v_lshlrev_b32_e32 v178, 16, v179
	v_med3_f32 v48, v176, s11, v232
	v_med3_f32 v176, v177, s11, v232
	v_and_b32_e32 v179, 0xffff0000, v179
	v_cvt_pk_fp8_f32 v173, v48, v176
	v_pk_mul_f32 v[178:179], v[90:91], v[178:179]
	v_lshlrev_b64 v[50:51], 10, v[222:223]
	v_pk_mul_f32 v[178:179], v[178:179], s[26:27] op_sel_hi:[1,0]
	v_lshl_add_u64 v[50:51], s[42:43], 0, v[50:51]
	v_med3_f32 v177, v178, s11, v232
	v_med3_f32 v178, v179, s11, v232
	v_cvt_pk_fp8_f32 v173, v177, v178 op_sel:[0,0,1]
	v_pk_mul_f32 v[176:177], v[44:45], v[184:185]
	v_lshl_add_u64 v[50:51], v[50:51], 0, vcc
	v_pk_mul_f32 v[176:177], v[176:177], s[26:27] op_sel_hi:[1,0]
	v_lshl_add_u64 v[50:51], v[50:51], 0, s[22:23]
	v_med3_f32 v48, v176, s11, v232
	v_med3_f32 v177, v177, s11, v232
	v_mov_b32_e32 v176, v49
	v_cvt_pk_fp8_f32 v176, v48, v177
	v_pk_mul_f32 v[178:179], v[46:47], v[186:187]
	v_lshl_add_u64 v[50:51], v[50:51], 0, v[216:217]
	v_permlane16_swap_b32_e32 v188, v190
	v_permlane16_swap_b32_e32 v189, v191
	v_pk_mul_f32 v[178:179], v[178:179], s[26:27] op_sel_hi:[1,0]
	global_store_dwordx4 v[50:51], v[188:191], off
	v_med3_f32 v178, v178, s11, v232
	v_med3_f32 v179, v179, s11, v232
	v_lshlrev_b32_e32 v188, 16, v174
	v_and_b32_e32 v189, 0xffff0000, v174
	v_cvt_pk_fp8_f32 v176, v178, v179 op_sel:[0,0,1]
	v_pk_mul_f32 v[178:179], v[40:41], v[188:189]
	v_mov_b32_e32 v177, v49
	v_pk_mul_f32 v[178:179], v[178:179], s[26:27] op_sel_hi:[1,0]
	v_lshlrev_b32_e32 v174, 16, v175
	v_med3_f32 v48, v178, s11, v232
	v_med3_f32 v178, v179, s11, v232
	v_and_b32_e32 v175, 0xffff0000, v175
	v_cvt_pk_fp8_f32 v177, v48, v178
	v_pk_mul_f32 v[174:175], v[42:43], v[174:175]
	v_lshlrev_b32_e32 v178, 16, v170
	v_pk_mul_f32 v[174:175], v[174:175], s[26:27] op_sel_hi:[1,0]
	v_and_b32_e32 v179, 0xffff0000, v170
	v_med3_f32 v174, v174, s11, v232
	v_med3_f32 v175, v175, s11, v232
	v_cvt_pk_fp8_f32 v177, v174, v175 op_sel:[0,0,1]
	v_lshlrev_b32_e32 v174, 16, v168
	v_and_b32_e32 v175, 0xffff0000, v168
	v_pk_mul_f32 v[174:175], v[80:81], v[174:175]
	v_lshlrev_b32_e32 v168, 16, v169
	v_pk_mul_f32 v[174:175], v[174:175], s[26:27] op_sel_hi:[1,0]
	v_and_b32_e32 v169, 0xffff0000, v169
	v_med3_f32 v48, v174, s11, v232
	v_med3_f32 v175, v175, s11, v232
	v_mov_b32_e32 v174, v49
	v_cvt_pk_fp8_f32 v174, v48, v175
	v_pk_mul_f32 v[168:169], v[82:83], v[168:169]
	v_mov_b32_e32 v175, v49
	v_pk_mul_f32 v[168:169], v[168:169], s[26:27] op_sel_hi:[1,0]
	v_lshlrev_b32_e32 v170, 16, v171
	v_med3_f32 v168, v168, s11, v232
	v_med3_f32 v169, v169, s11, v232
	v_cvt_pk_fp8_f32 v174, v168, v169 op_sel:[0,0,1]
	v_pk_mul_f32 v[168:169], v[72:73], v[178:179]
	v_and_b32_e32 v171, 0xffff0000, v171
	v_pk_mul_f32 v[168:169], v[168:169], s[26:27] op_sel_hi:[1,0]
	v_pk_mul_f32 v[170:171], v[74:75], v[170:171]
	v_med3_f32 v48, v168, s11, v232
	v_med3_f32 v168, v169, s11, v232
	v_cvt_pk_fp8_f32 v175, v48, v168
	v_pk_mul_f32 v[170:171], v[170:171], s[26:27] op_sel_hi:[1,0]
	v_lshlrev_b32_e32 v180, 16, v164
	v_and_b32_e32 v181, 0xffff0000, v164
	v_med3_f32 v169, v170, s11, v232
	v_med3_f32 v170, v171, s11, v232
	v_cvt_pk_fp8_f32 v175, v169, v170 op_sel:[0,0,1]
	v_pk_mul_f32 v[168:169], v[36:37], v[180:181]
	v_mov_b32_e32 v178, v49
	v_pk_mul_f32 v[168:169], v[168:169], s[26:27] op_sel_hi:[1,0]
	v_lshlrev_b32_e32 v164, 16, v165
	v_med3_f32 v48, v168, s11, v232
	v_med3_f32 v168, v169, s11, v232
	v_and_b32_e32 v165, 0xffff0000, v165
	v_cvt_pk_fp8_f32 v178, v48, v168
	v_pk_mul_f32 v[164:165], v[38:39], v[164:165]
	v_lshlrev_b32_e32 v182, 16, v166
	v_pk_mul_f32 v[164:165], v[164:165], s[26:27] op_sel_hi:[1,0]
	v_and_b32_e32 v183, 0xffff0000, v166
	v_med3_f32 v164, v164, s11, v232
	v_med3_f32 v165, v165, s11, v232
	v_cvt_pk_fp8_f32 v178, v164, v165 op_sel:[0,0,1]
	v_pk_mul_f32 v[164:165], v[32:33], v[182:183]
	v_mov_b32_e32 v179, v49
	v_pk_mul_f32 v[164:165], v[164:165], s[26:27] op_sel_hi:[1,0]
	v_lshlrev_b32_e32 v166, 16, v167
	v_med3_f32 v48, v164, s11, v232
	v_med3_f32 v164, v165, s11, v232
	v_and_b32_e32 v167, 0xffff0000, v167
	v_cvt_pk_fp8_f32 v179, v48, v164
	v_pk_mul_f32 v[166:167], v[34:35], v[166:167]
	v_or_b32_e32 v164, 32, v222
	v_pk_mul_f32 v[166:167], v[166:167], s[26:27] op_sel_hi:[1,0]
	v_permlane16_swap_b32_e32 v172, v174
	v_med3_f32 v165, v166, s11, v232
	v_med3_f32 v166, v167, s11, v232
	v_cvt_pk_fp8_f32 v179, v165, v166 op_sel:[0,0,1]
	v_ashrrev_i32_e32 v165, 31, v164
	v_lshlrev_b64 v[164:165], 10, v[164:165]
	v_lshl_add_u64 v[164:165], s[42:43], 0, v[164:165]
	v_lshl_add_u64 v[164:165], v[164:165], 0, vcc
	v_lshl_add_u64 v[164:165], v[164:165], 0, s[22:23]
	v_lshl_add_u64 v[164:165], v[164:165], 0, v[216:217]
	v_permlane16_swap_b32_e32 v173, v175
	v_permlane16_swap_b32_e32 v176, v178
	v_permlane16_swap_b32_e32 v177, v179
	global_store_dwordx4 v[164:165], v[172:175], off
	global_store_dwordx4 v[164:165], v[176:179], off offset:32
	v_lshlrev_b32_e32 v164, 16, v160
	v_and_b32_e32 v165, 0xffff0000, v160
	v_lshlrev_b32_e32 v168, 16, v156
	v_and_b32_e32 v169, 0xffff0000, v156
	v_lshlrev_b32_e32 v170, 16, v157
	v_and_b32_e32 v171, 0xffff0000, v157
	v_pk_mul_f32 v[156:157], v[28:29], v[164:165]
	v_lshlrev_b32_e32 v160, 16, v161
	v_pk_mul_f32 v[156:157], v[156:157], s[26:27] op_sel_hi:[1,0]
	v_and_b32_e32 v161, 0xffff0000, v161
	v_med3_f32 v48, v156, s11, v232
	v_med3_f32 v157, v157, s11, v232
	v_mov_b32_e32 v156, v49
	v_cvt_pk_fp8_f32 v156, v48, v157
	v_pk_mul_f32 v[160:161], v[30:31], v[160:161]
	v_lshlrev_b32_e32 v166, 16, v162
	v_pk_mul_f32 v[160:161], v[160:161], s[26:27] op_sel_hi:[1,0]
	v_and_b32_e32 v167, 0xffff0000, v162
	v_med3_f32 v160, v160, s11, v232
	v_med3_f32 v161, v161, s11, v232
	v_cvt_pk_fp8_f32 v156, v160, v161 op_sel:[0,0,1]
	v_pk_mul_f32 v[160:161], v[24:25], v[166:167]
	v_mov_b32_e32 v157, v49
	v_pk_mul_f32 v[160:161], v[160:161], s[26:27] op_sel_hi:[1,0]
	v_lshlrev_b32_e32 v162, 16, v163
	v_med3_f32 v48, v160, s11, v232
	v_med3_f32 v160, v161, s11, v232
	v_and_b32_e32 v163, 0xffff0000, v163
	v_cvt_pk_fp8_f32 v157, v48, v160
	v_pk_mul_f32 v[162:163], v[26:27], v[162:163]
	v_lshlrev_b32_e32 v172, 16, v158
	v_pk_mul_f32 v[162:163], v[162:163], s[26:27] op_sel_hi:[1,0]
	v_and_b32_e32 v173, 0xffff0000, v158
	v_med3_f32 v161, v162, s11, v232
	v_med3_f32 v162, v163, s11, v232
	v_cvt_pk_fp8_f32 v157, v161, v162 op_sel:[0,0,1]
	v_pk_mul_f32 v[160:161], v[68:69], v[168:169]
	v_pk_mul_f32 v[162:163], v[70:71], v[170:171]
	v_pk_mul_f32 v[160:161], v[160:161], s[26:27] op_sel_hi:[1,0]
	v_pk_mul_f32 v[162:163], v[162:163], s[26:27] op_sel_hi:[1,0]
	v_med3_f32 v48, v160, s11, v232
	v_med3_f32 v161, v161, s11, v232
	v_mov_b32_e32 v160, v49
	v_cvt_pk_fp8_f32 v160, v48, v161
	v_med3_f32 v162, v162, s11, v232
	v_med3_f32 v163, v163, s11, v232
	v_mov_b32_e32 v161, v49
	v_cvt_pk_fp8_f32 v160, v162, v163 op_sel:[0,0,1]
	v_pk_mul_f32 v[162:163], v[76:77], v[172:173]
	v_lshlrev_b32_e32 v158, 16, v159
	v_pk_mul_f32 v[162:163], v[162:163], s[26:27] op_sel_hi:[1,0]
	v_and_b32_e32 v159, 0xffff0000, v159
	v_med3_f32 v48, v162, s11, v232
	v_med3_f32 v162, v163, s11, v232
	v_cvt_pk_fp8_f32 v161, v48, v162
	v_pk_mul_f32 v[158:159], v[78:79], v[158:159]
	v_lshlrev_b32_e32 v162, 16, v150
	v_pk_mul_f32 v[158:159], v[158:159], s[26:27] op_sel_hi:[1,0]
	v_and_b32_e32 v163, 0xffff0000, v150
	v_med3_f32 v158, v158, s11, v232
	v_med3_f32 v159, v159, s11, v232
	v_cvt_pk_fp8_f32 v161, v158, v159 op_sel:[0,0,1]
	v_lshlrev_b32_e32 v158, 16, v148
	v_and_b32_e32 v159, 0xffff0000, v148
	v_pk_mul_f32 v[158:159], v[20:21], v[158:159]
	v_lshlrev_b32_e32 v148, 16, v149
	v_pk_mul_f32 v[158:159], v[158:159], s[26:27] op_sel_hi:[1,0]
	v_and_b32_e32 v149, 0xffff0000, v149
	v_med3_f32 v48, v158, s11, v232
	v_med3_f32 v159, v159, s11, v232
	v_mov_b32_e32 v158, v49
	v_cvt_pk_fp8_f32 v158, v48, v159
	v_pk_mul_f32 v[148:149], v[22:23], v[148:149]
	v_mov_b32_e32 v159, v49
	v_pk_mul_f32 v[148:149], v[148:149], s[26:27] op_sel_hi:[1,0]
	v_lshlrev_b32_e32 v150, 16, v151
	v_med3_f32 v148, v148, s11, v232
	v_med3_f32 v149, v149, s11, v232
	v_cvt_pk_fp8_f32 v158, v148, v149 op_sel:[0,0,1]
	v_pk_mul_f32 v[148:149], v[16:17], v[162:163]
	v_and_b32_e32 v151, 0xffff0000, v151
	v_pk_mul_f32 v[148:149], v[148:149], s[26:27] op_sel_hi:[1,0]
	v_pk_mul_f32 v[150:151], v[18:19], v[150:151]
	v_med3_f32 v48, v148, s11, v232
	v_med3_f32 v148, v149, s11, v232
	v_cvt_pk_fp8_f32 v159, v48, v148
	v_pk_mul_f32 v[150:151], v[150:151], s[26:27] op_sel_hi:[1,0]
	v_lshlrev_b32_e32 v164, 16, v152
	v_and_b32_e32 v165, 0xffff0000, v152
	v_med3_f32 v149, v150, s11, v232
	v_med3_f32 v150, v151, s11, v232
	v_cvt_pk_fp8_f32 v159, v149, v150 op_sel:[0,0,1]
	v_pk_mul_f32 v[148:149], v[84:85], v[164:165]
	v_mov_b32_e32 v162, v49
	v_pk_mul_f32 v[148:149], v[148:149], s[26:27] op_sel_hi:[1,0]
	v_lshlrev_b32_e32 v152, 16, v153
	v_med3_f32 v48, v148, s11, v232
	v_med3_f32 v148, v149, s11, v232
	v_and_b32_e32 v153, 0xffff0000, v153
	v_cvt_pk_fp8_f32 v162, v48, v148
	v_pk_mul_f32 v[150:151], v[86:87], v[152:153]
	v_lshlrev_b32_e32 v166, 16, v154
	v_pk_mul_f32 v[150:151], v[150:151], s[26:27] op_sel_hi:[1,0]
	v_and_b32_e32 v167, 0xffff0000, v154
	v_med3_f32 v149, v150, s11, v232
	v_med3_f32 v150, v151, s11, v232
	v_cvt_pk_fp8_f32 v162, v149, v150 op_sel:[0,0,1]
	v_pk_mul_f32 v[148:149], v[92:93], v[166:167]
	v_mov_b32_e32 v163, v49
	v_pk_mul_f32 v[148:149], v[148:149], s[26:27] op_sel_hi:[1,0]
	v_lshlrev_b32_e32 v154, 16, v155
	v_med3_f32 v48, v148, s11, v232
	v_med3_f32 v148, v149, s11, v232
	v_and_b32_e32 v155, 0xffff0000, v155
	v_cvt_pk_fp8_f32 v163, v48, v148
	v_pk_mul_f32 v[150:151], v[94:95], v[154:155]
	v_permlane16_swap_b32_e32 v160, v162
	v_pk_mul_f32 v[150:151], v[150:151], s[26:27] op_sel_hi:[1,0]
	v_permlane16_swap_b32_e32 v156, v158
	v_med3_f32 v149, v150, s11, v232
	v_med3_f32 v150, v151, s11, v232
	v_cvt_pk_fp8_f32 v163, v149, v150 op_sel:[0,0,1]
	v_lshl_add_u64 v[148:149], v[50:51], 0, s[0:1]
	s_mov_b32 s0, 0x20000
	v_add_co_u32_e32 v150, vcc, s0, v50
	v_permlane16_swap_b32_e32 v161, v163
	global_store_dwordx4 v[148:149], v[160:163], off offset:32
	v_lshlrev_b32_e32 v148, 16, v140
	v_and_b32_e32 v149, 0xffff0000, v140
	v_lshlrev_b32_e32 v140, 16, v141
	v_and_b32_e32 v141, 0xffff0000, v141
	v_pk_mul_f32 v[148:149], v[12:13], v[148:149]
	v_pk_mul_f32 v[140:141], v[14:15], v[140:141]
	v_pk_mul_f32 v[148:149], v[148:149], s[26:27] op_sel_hi:[1,0]
	v_pk_mul_f32 v[140:141], v[140:141], s[26:27] op_sel_hi:[1,0]
	v_med3_f32 v48, v148, s11, v232
	v_med3_f32 v148, v149, s11, v232
	v_med3_f32 v149, v140, s11, v232
	v_mov_b32_e32 v140, v49
	v_cvt_pk_fp8_f32 v140, v48, v148
	v_permlane16_swap_b32_e32 v157, v159
	v_addc_co_u32_e32 v151, vcc, 0, v51, vcc
	global_store_dwordx4 v[150:151], v[156:159], off
	v_lshlrev_b32_e32 v150, 16, v142
	v_and_b32_e32 v151, 0xffff0000, v142
	v_med3_f32 v141, v141, s11, v232
	v_cvt_pk_fp8_f32 v140, v149, v141 op_sel:[0,0,1]
	v_pk_mul_f32 v[148:149], v[8:9], v[150:151]
	v_mov_b32_e32 v141, v49
	v_pk_mul_f32 v[148:149], v[148:149], s[26:27] op_sel_hi:[1,0]
	v_lshlrev_b32_e32 v142, 16, v143
	v_med3_f32 v48, v148, s11, v232
	v_med3_f32 v148, v149, s11, v232
	v_and_b32_e32 v143, 0xffff0000, v143
	v_cvt_pk_fp8_f32 v141, v48, v148
	v_pk_mul_f32 v[142:143], v[10:11], v[142:143]
	v_lshlrev_b32_e32 v152, 16, v144
	v_pk_mul_f32 v[142:143], v[142:143], s[26:27] op_sel_hi:[1,0]
	v_and_b32_e32 v153, 0xffff0000, v144
	v_lshlrev_b32_e32 v144, 16, v145
	v_and_b32_e32 v145, 0xffff0000, v145
	v_med3_f32 v142, v142, s11, v232
	v_med3_f32 v143, v143, s11, v232
	v_cvt_pk_fp8_f32 v141, v142, v143 op_sel:[0,0,1]
	v_pk_mul_f32 v[142:143], v[100:101], v[152:153]
	v_pk_mul_f32 v[144:145], v[102:103], v[144:145]
	v_pk_mul_f32 v[142:143], v[142:143], s[26:27] op_sel_hi:[1,0]
	v_pk_mul_f32 v[144:145], v[144:145], s[26:27] op_sel_hi:[1,0]
	v_med3_f32 v48, v142, s11, v232
	v_med3_f32 v142, v143, s11, v232
	v_med3_f32 v143, v144, s11, v232
	v_mov_b32_e32 v144, v49
	v_cvt_pk_fp8_f32 v144, v48, v142
	v_lshlrev_b32_e32 v154, 16, v146
	v_and_b32_e32 v155, 0xffff0000, v146
	v_med3_f32 v145, v145, s11, v232
	v_cvt_pk_fp8_f32 v144, v143, v145 op_sel:[0,0,1]
	v_pk_mul_f32 v[142:143], v[108:109], v[154:155]
	v_mov_b32_e32 v145, v49
	v_pk_mul_f32 v[142:143], v[142:143], s[26:27] op_sel_hi:[1,0]
	v_lshlrev_b32_e32 v146, 16, v147
	v_med3_f32 v48, v142, s11, v232
	v_med3_f32 v142, v143, s11, v232
	v_and_b32_e32 v147, 0xffff0000, v147
	v_cvt_pk_fp8_f32 v145, v48, v142
	v_pk_mul_f32 v[146:147], v[110:111], v[146:147]
	v_lshlrev_b32_e32 v142, 16, v132
	v_pk_mul_f32 v[146:147], v[146:147], s[26:27] op_sel_hi:[1,0]
	v_lshlrev_b32_e32 v148, 16, v136
	v_med3_f32 v143, v146, s11, v232
	v_med3_f32 v146, v147, s11, v232
	v_cvt_pk_fp8_f32 v145, v143, v146 op_sel:[0,0,1]
	v_and_b32_e32 v143, 0xffff0000, v132
	v_pk_mul_f32 v[142:143], v[4:5], v[142:143]
	v_lshlrev_b32_e32 v132, 16, v133
	v_pk_mul_f32 v[142:143], v[142:143], s[26:27] op_sel_hi:[1,0]
	v_and_b32_e32 v133, 0xffff0000, v133
	v_med3_f32 v48, v142, s11, v232
	v_med3_f32 v143, v143, s11, v232
	v_mov_b32_e32 v142, v49
	v_cvt_pk_fp8_f32 v142, v48, v143
	v_pk_mul_f32 v[132:133], v[6:7], v[132:133]
	v_lshlrev_b32_e32 v146, 16, v134
	v_pk_mul_f32 v[132:133], v[132:133], s[26:27] op_sel_hi:[1,0]
	v_and_b32_e32 v147, 0xffff0000, v134
	v_med3_f32 v132, v132, s11, v232
	v_med3_f32 v133, v133, s11, v232
	v_cvt_pk_fp8_f32 v142, v132, v133 op_sel:[0,0,1]
	v_pk_mul_f32 v[132:133], v[0:1], v[146:147]
	v_mov_b32_e32 v143, v49
	v_pk_mul_f32 v[132:133], v[132:133], s[26:27] op_sel_hi:[1,0]
	v_lshlrev_b32_e32 v134, 16, v135
	v_med3_f32 v48, v132, s11, v232
	v_med3_f32 v132, v133, s11, v232
	v_and_b32_e32 v135, 0xffff0000, v135
	v_cvt_pk_fp8_f32 v143, v48, v132
	v_pk_mul_f32 v[134:135], v[2:3], v[134:135]
	v_and_b32_e32 v149, 0xffff0000, v136
	v_pk_mul_f32 v[134:135], v[134:135], s[26:27] op_sel_hi:[1,0]
	v_mov_b32_e32 v146, v49
	v_med3_f32 v133, v134, s11, v232
	v_med3_f32 v134, v135, s11, v232
	v_cvt_pk_fp8_f32 v143, v133, v134 op_sel:[0,0,1]
	v_pk_mul_f32 v[132:133], v[116:117], v[148:149]
	v_lshlrev_b32_e32 v136, 16, v137
	v_pk_mul_f32 v[132:133], v[132:133], s[26:27] op_sel_hi:[1,0]
	v_and_b32_e32 v137, 0xffff0000, v137
	v_med3_f32 v48, v132, s11, v232
	v_med3_f32 v132, v133, s11, v232
	v_cvt_pk_fp8_f32 v146, v48, v132
	v_pk_mul_f32 v[134:135], v[118:119], v[136:137]
	v_lshlrev_b32_e32 v150, 16, v138
	v_pk_mul_f32 v[134:135], v[134:135], s[26:27] op_sel_hi:[1,0]
	v_and_b32_e32 v151, 0xffff0000, v138
	v_med3_f32 v133, v134, s11, v232
	v_med3_f32 v134, v135, s11, v232
	v_cvt_pk_fp8_f32 v146, v133, v134 op_sel:[0,0,1]
	v_pk_mul_f32 v[132:133], v[124:125], v[150:151]
	v_mov_b32_e32 v147, v49
	v_pk_mul_f32 v[132:133], v[132:133], s[26:27] op_sel_hi:[1,0]
	v_lshlrev_b32_e32 v138, 16, v139
	v_med3_f32 v48, v132, s11, v232
	v_med3_f32 v132, v133, s11, v232
	v_and_b32_e32 v139, 0xffff0000, v139
	v_cvt_pk_fp8_f32 v147, v48, v132
	v_pk_mul_f32 v[134:135], v[126:127], v[138:139]
	v_permlane16_swap_b32_e32 v192, v194
	v_pk_mul_f32 v[134:135], v[134:135], s[26:27] op_sel_hi:[1,0]
	v_permlane16_swap_b32_e32 v193, v195
	v_med3_f32 v133, v134, s11, v232
	v_med3_f32 v134, v135, s11, v232
	v_cvt_pk_fp8_f32 v147, v133, v134 op_sel:[0,0,1]
	s_mov_b64 s[0:1], 0x28000
	global_store_dwordx4 v[50:51], v[192:195], off offset:32
	v_lshl_add_u64 v[132:133], v[50:51], 0, s[0:1]
	v_add_co_u32_e32 v50, vcc, 0x28000, v50
	v_permlane16_swap_b32_e32 v140, v142
	v_permlane16_swap_b32_e32 v141, v143
	v_addc_co_u32_e32 v51, vcc, 0, v51, vcc
	v_permlane16_swap_b32_e32 v144, v146
	v_permlane16_swap_b32_e32 v145, v147
	global_store_dwordx4 v[50:51], v[140:143], off
	global_store_dwordx4 v[132:133], v[144:147], off offset:32
	s_cbranch_execnz .LBB0_444
.LBB0_446:
	v_lshl_add_u64 v[50:51], v[220:221], 0, s[58:59]
	global_load_dwordx4 v[192:195], v[50:51], off nt
	v_lshl_add_u64 v[50:51], v[220:221], 0, s[60:61]
	global_load_dwordx4 v[188:191], v[50:51], off nt
	v_lshl_add_u64 v[50:51], v[220:221], 0, s[62:63]
	global_load_dwordx4 v[184:187], v[50:51], off nt
	v_lshl_add_u64 v[50:51], v[220:221], 0, s[70:71]
	global_load_dwordx4 v[180:183], v[50:51], off nt
	v_lshl_add_u64 v[50:51], v[220:221], 0, s[78:79]
	global_load_dwordx4 v[176:179], v[50:51], off nt
	v_lshl_add_u64 v[50:51], v[220:221], 0, s[76:77]
	global_load_dwordx4 v[172:175], v[50:51], off nt
	v_lshl_add_u64 v[50:51], v[220:221], 0, s[74:75]
	global_load_dwordx4 v[168:171], v[50:51], off nt
	v_lshl_add_u64 v[50:51], v[220:221], 0, s[72:73]
	global_load_dwordx4 v[164:167], v[50:51], off nt
	v_lshl_add_u64 v[50:51], v[220:221], 0, s[68:69]
	s_or_b32 s0, s4, s7
	global_load_dwordx4 v[160:163], v[50:51], off nt
	v_lshl_add_u64 v[50:51], v[220:221], 0, s[66:67]
	s_ashr_i32 s1, s0, 31
	global_load_dwordx4 v[156:159], v[50:51], off nt
	v_lshl_add_u64 v[50:51], v[220:221], 0, s[64:65]
	s_lshl_b64 s[0:1], s[0:1], 10
	global_load_dwordx4 v[148:151], v[50:51], off nt
	v_lshl_add_u64 v[50:51], v[220:221], 0, s[0:1]
	s_or_b32 s0, s5, s40
	s_ashr_i32 s1, s0, 31
	s_lshl_b64 s[0:1], s[0:1], 10
	global_load_dwordx4 v[144:147], v[50:51], off nt
	v_lshl_add_u64 v[50:51], v[220:221], 0, s[0:1]
	s_or_b32 s0, s4, s40
	s_ashr_i32 s1, s0, 31
	s_lshl_b64 s[0:1], s[0:1], 10
	global_load_dwordx4 v[140:143], v[50:51], off nt
	v_lshl_add_u64 v[50:51], v[220:221], 0, s[0:1]
	s_or_b32 s0, s5, s41
	s_ashr_i32 s1, s0, 31
	s_lshl_b64 s[0:1], s[0:1], 10
	global_load_dwordx4 v[136:139], v[50:51], off nt
	v_lshl_add_u64 v[50:51], v[220:221], 0, s[0:1]
	s_or_b32 s0, s4, s41
	s_ashr_i32 s1, s0, 31
	s_lshl_b64 s[0:1], s[0:1], 10
	global_load_dwordx4 v[132:135], v[50:51], off nt
	v_lshl_add_u64 v[50:51], v[220:221], 0, s[0:1]
	global_load_dwordx4 v[152:155], v[50:51], off nt
	s_waitcnt vmcnt(0)
	v_lshlrev_b32_e32 v50, 16, v192
	v_and_b32_e32 v51, 0xffff0000, v192
	v_pk_mul_f32 v[128:129], v[128:129], v[50:51]
	v_lshlrev_b32_e32 v50, 16, v188
	v_and_b32_e32 v51, 0xffff0000, v188
	v_pk_mul_f32 v[64:65], v[64:65], v[50:51]
	v_lshlrev_b32_e32 v50, 16, v184
	v_and_b32_e32 v51, 0xffff0000, v184
	v_pk_mul_f32 v[112:113], v[112:113], v[50:51]
	v_lshlrev_b32_e32 v50, 16, v180
	v_and_b32_e32 v51, 0xffff0000, v180
	v_pk_mul_f32 v[56:57], v[56:57], v[50:51]
	v_lshlrev_b32_e32 v50, 16, v176
	v_and_b32_e32 v51, 0xffff0000, v176
	v_pk_mul_f32 v[96:97], v[96:97], v[50:51]
	v_lshlrev_b32_e32 v50, 16, v172
	v_and_b32_e32 v51, 0xffff0000, v172
	v_pk_mul_f32 v[44:45], v[44:45], v[50:51]
	v_lshlrev_b32_e32 v50, 16, v168
	v_and_b32_e32 v51, 0xffff0000, v168
	v_pk_mul_f32 v[80:81], v[80:81], v[50:51]
	v_lshlrev_b32_e32 v50, 16, v164
	v_and_b32_e32 v51, 0xffff0000, v164
	v_pk_mul_f32 v[36:37], v[36:37], v[50:51]
	v_lshlrev_b32_e32 v50, 16, v160
	v_and_b32_e32 v51, 0xffff0000, v160
	v_pk_mul_f32 v[28:29], v[28:29], v[50:51]
	v_lshlrev_b32_e32 v50, 16, v156
	v_and_b32_e32 v51, 0xffff0000, v156
	v_pk_mul_f32 v[68:69], v[68:69], v[50:51]
	v_lshlrev_b32_e32 v50, 16, v148
	v_and_b32_e32 v51, 0xffff0000, v148
	v_pk_mul_f32 v[20:21], v[20:21], v[50:51]
	v_lshlrev_b32_e32 v50, 16, v144
	v_and_b32_e32 v51, 0xffff0000, v144
	v_pk_mul_f32 v[84:85], v[84:85], v[50:51]
	v_lshlrev_b32_e32 v50, 16, v140
	v_and_b32_e32 v51, 0xffff0000, v140
	v_pk_mul_f32 v[12:13], v[12:13], v[50:51]
	v_lshlrev_b32_e32 v50, 16, v136
	v_and_b32_e32 v51, 0xffff0000, v136
	v_lshlrev_b32_e32 v136, 16, v137
	v_and_b32_e32 v137, 0xffff0000, v137
	v_lshlrev_b32_e32 v192, 16, v193
	v_and_b32_e32 v193, 0xffff0000, v193
	v_lshlrev_b32_e32 v188, 16, v189
	v_and_b32_e32 v189, 0xffff0000, v189
	v_lshlrev_b32_e32 v184, 16, v185
	v_and_b32_e32 v185, 0xffff0000, v185
	v_lshlrev_b32_e32 v180, 16, v181
	v_and_b32_e32 v181, 0xffff0000, v181
	v_lshlrev_b32_e32 v176, 16, v177
	v_and_b32_e32 v177, 0xffff0000, v177
	v_lshlrev_b32_e32 v172, 16, v173
	v_and_b32_e32 v173, 0xffff0000, v173
	v_lshlrev_b32_e32 v168, 16, v169
	v_and_b32_e32 v169, 0xffff0000, v169
	v_lshlrev_b32_e32 v164, 16, v165
	v_and_b32_e32 v165, 0xffff0000, v165
	v_lshlrev_b32_e32 v160, 16, v161
	v_and_b32_e32 v161, 0xffff0000, v161
	v_lshlrev_b32_e32 v156, 16, v157
	v_and_b32_e32 v157, 0xffff0000, v157
	v_lshlrev_b32_e32 v148, 16, v149
	v_and_b32_e32 v149, 0xffff0000, v149
	v_lshlrev_b32_e32 v144, 16, v145
	v_and_b32_e32 v145, 0xffff0000, v145
	v_lshlrev_b32_e32 v140, 16, v141
	v_and_b32_e32 v141, 0xffff0000, v141
	v_pk_mul_f32 v[102:103], v[102:103], v[136:137]
	v_pk_mul_f32 v[100:101], v[100:101], v[50:51]
	v_lshlrev_b32_e32 v50, 16, v132
	v_and_b32_e32 v51, 0xffff0000, v132
	v_lshlrev_b32_e32 v132, 16, v133
	v_and_b32_e32 v133, 0xffff0000, v133
	v_lshlrev_b32_e32 v136, 16, v134
	v_and_b32_e32 v137, 0xffff0000, v134
	v_lshlrev_b32_e32 v134, 16, v135
	v_and_b32_e32 v135, 0xffff0000, v135
	v_lshlrev_b32_e32 v202, 16, v194
	v_and_b32_e32 v203, 0xffff0000, v194
	v_lshlrev_b32_e32 v194, 16, v195
	v_and_b32_e32 v195, 0xffff0000, v195
	v_pk_mul_f32 v[130:131], v[130:131], v[192:193]
	v_lshlrev_b32_e32 v192, 16, v190
	v_and_b32_e32 v193, 0xffff0000, v190
	v_lshlrev_b32_e32 v190, 16, v191
	v_and_b32_e32 v191, 0xffff0000, v191
	v_pk_mul_f32 v[66:67], v[66:67], v[188:189]
	v_lshlrev_b32_e32 v188, 16, v186
	v_and_b32_e32 v189, 0xffff0000, v186
	v_lshlrev_b32_e32 v186, 16, v187
	v_and_b32_e32 v187, 0xffff0000, v187
	v_pk_mul_f32 v[114:115], v[114:115], v[184:185]
	v_lshlrev_b32_e32 v184, 16, v182
	v_and_b32_e32 v185, 0xffff0000, v182
	v_lshlrev_b32_e32 v182, 16, v183
	v_and_b32_e32 v183, 0xffff0000, v183
	v_pk_mul_f32 v[58:59], v[58:59], v[180:181]
	v_lshlrev_b32_e32 v180, 16, v178
	v_and_b32_e32 v181, 0xffff0000, v178
	v_lshlrev_b32_e32 v178, 16, v179
	v_and_b32_e32 v179, 0xffff0000, v179
	v_pk_mul_f32 v[98:99], v[98:99], v[176:177]
	v_lshlrev_b32_e32 v176, 16, v174
	v_and_b32_e32 v177, 0xffff0000, v174
	v_lshlrev_b32_e32 v174, 16, v175
	v_and_b32_e32 v175, 0xffff0000, v175
	v_pk_mul_f32 v[46:47], v[46:47], v[172:173]
	v_lshlrev_b32_e32 v172, 16, v170
	v_and_b32_e32 v173, 0xffff0000, v170
	v_lshlrev_b32_e32 v170, 16, v171
	v_and_b32_e32 v171, 0xffff0000, v171
	v_pk_mul_f32 v[82:83], v[82:83], v[168:169]
	v_lshlrev_b32_e32 v168, 16, v166
	v_and_b32_e32 v169, 0xffff0000, v166
	v_lshlrev_b32_e32 v166, 16, v167
	v_and_b32_e32 v167, 0xffff0000, v167
	v_pk_mul_f32 v[38:39], v[38:39], v[164:165]
	v_lshlrev_b32_e32 v164, 16, v162
	v_and_b32_e32 v165, 0xffff0000, v162
	v_lshlrev_b32_e32 v162, 16, v163
	v_and_b32_e32 v163, 0xffff0000, v163
	v_pk_mul_f32 v[30:31], v[30:31], v[160:161]
	v_lshlrev_b32_e32 v160, 16, v158
	v_and_b32_e32 v161, 0xffff0000, v158
	v_lshlrev_b32_e32 v158, 16, v159
	v_and_b32_e32 v159, 0xffff0000, v159
	v_pk_mul_f32 v[70:71], v[70:71], v[156:157]
	v_lshlrev_b32_e32 v156, 16, v150
	v_and_b32_e32 v157, 0xffff0000, v150
	v_lshlrev_b32_e32 v150, 16, v151
	v_and_b32_e32 v151, 0xffff0000, v151
	v_pk_mul_f32 v[22:23], v[22:23], v[148:149]
	v_lshlrev_b32_e32 v148, 16, v146
	v_and_b32_e32 v149, 0xffff0000, v146
	v_lshlrev_b32_e32 v146, 16, v147
	v_and_b32_e32 v147, 0xffff0000, v147
	v_pk_mul_f32 v[86:87], v[86:87], v[144:145]
	v_lshlrev_b32_e32 v144, 16, v142
	v_and_b32_e32 v145, 0xffff0000, v142
	v_lshlrev_b32_e32 v142, 16, v143
	v_and_b32_e32 v143, 0xffff0000, v143
	v_pk_mul_f32 v[14:15], v[14:15], v[140:141]
	v_lshlrev_b32_e32 v140, 16, v138
	v_and_b32_e32 v141, 0xffff0000, v138
	v_lshlrev_b32_e32 v138, 16, v139
	v_and_b32_e32 v139, 0xffff0000, v139
	v_pk_mul_f32 v[6:7], v[6:7], v[132:133]
	v_pk_mul_f32 v[4:5], v[4:5], v[50:51]
	v_pk_mul_f32 v[2:3], v[2:3], v[134:135]
	v_pk_mul_f32 v[0:1], v[0:1], v[136:137]
	v_lshlrev_b32_e32 v50, 16, v152
	v_and_b32_e32 v51, 0xffff0000, v152
	v_lshlrev_b32_e32 v132, 16, v153
	v_and_b32_e32 v133, 0xffff0000, v153
	v_lshlrev_b32_e32 v134, 16, v154
	v_and_b32_e32 v135, 0xffff0000, v154
	v_lshlrev_b32_e32 v136, 16, v155
	v_and_b32_e32 v137, 0xffff0000, v155
	v_pk_mul_f32 v[122:123], v[122:123], v[194:195]
	v_pk_mul_f32 v[120:121], v[120:121], v[202:203]
	v_pk_mul_f32 v[62:63], v[62:63], v[190:191]
	v_pk_mul_f32 v[60:61], v[60:61], v[192:193]
	v_pk_mul_f32 v[106:107], v[106:107], v[186:187]
	v_pk_mul_f32 v[104:105], v[104:105], v[188:189]
	v_pk_mul_f32 v[54:55], v[54:55], v[182:183]
	v_pk_mul_f32 v[52:53], v[52:53], v[184:185]
	v_pk_mul_f32 v[90:91], v[90:91], v[178:179]
	v_pk_mul_f32 v[88:89], v[88:89], v[180:181]
	v_pk_mul_f32 v[42:43], v[42:43], v[174:175]
	v_pk_mul_f32 v[40:41], v[40:41], v[176:177]
	v_pk_mul_f32 v[74:75], v[74:75], v[170:171]
	v_pk_mul_f32 v[72:73], v[72:73], v[172:173]
	v_pk_mul_f32 v[34:35], v[34:35], v[166:167]
	v_pk_mul_f32 v[32:33], v[32:33], v[168:169]
	v_pk_mul_f32 v[26:27], v[26:27], v[162:163]
	v_pk_mul_f32 v[24:25], v[24:25], v[164:165]
	v_pk_mul_f32 v[78:79], v[78:79], v[158:159]
	v_pk_mul_f32 v[76:77], v[76:77], v[160:161]
	v_pk_mul_f32 v[18:19], v[18:19], v[150:151]
	v_pk_mul_f32 v[16:17], v[16:17], v[156:157]
	v_pk_mul_f32 v[94:95], v[94:95], v[146:147]
	v_pk_mul_f32 v[92:93], v[92:93], v[148:149]
	v_pk_mul_f32 v[10:11], v[10:11], v[142:143]
	v_pk_mul_f32 v[8:9], v[8:9], v[144:145]
	v_pk_mul_f32 v[110:111], v[110:111], v[138:139]
	v_pk_mul_f32 v[108:109], v[108:109], v[140:141]
	v_pk_mul_f32 v[118:119], v[118:119], v[132:133]
	v_pk_mul_f32 v[116:117], v[116:117], v[50:51]
	v_pk_mul_f32 v[126:127], v[126:127], v[136:137]
	v_pk_mul_f32 v[124:125], v[124:125], v[134:135]
	s_andn2_b64 vcc, exec, s[56:57]
	s_mov_b64 s[0:1], -1
	s_cbranch_vccnz .LBB0_430

.LBB0_1046:
	v_mov_b32_e32 v0, 0
	s_add_i32 s0, 0, 0x24100
	v_mbcnt_lo_u32_b32 v0, -1, v0
	v_mbcnt_hi_u32_b32 v20, -1, v0
	v_mov_b32_e32 v0, s0
	ds_read_b64 v[0:1], v0 offset:120
	v_mov_b32_e32 v4, s0
	s_lshl_b32 s0, s91, 3
	s_add_i32 s2, s0, s92
	v_mov_b32_e32 v2, v4
	s_waitcnt lgkmcnt(0)
	v_readfirstlane_b32 s0, v0
	v_mov_b32_e32 v0, v4
	v_readfirstlane_b32 s1, v1
	ds_read_b64 v[0:1], v0 offset:104
	ds_read_b64 v[2:3], v2 offset:112
	ds_read_b64 v[4:5], v4 offset:120
	v_mov_b32_e32 v19, 0
	s_waitcnt lgkmcnt(2)
	v_readfirstlane_b32 s9, v1
	v_readfirstlane_b32 s8, v0
	s_waitcnt lgkmcnt(1)
	v_readfirstlane_b32 s5, v3
	v_readfirstlane_b32 s4, v2
	s_waitcnt lgkmcnt(0)
	v_readfirstlane_b32 s7, v5
	s_cmp_gt_i32 s2, 0xffff
	v_readfirstlane_b32 s6, v4
	s_cbranch_scc1 .LBB0_1060
	v_lshlrev_b32_e32 v16, 3, v20
	v_ashrrev_i32_e32 v17, 31, v16
	v_lshlrev_b64 v[22:23], 2, v[16:17]
	v_lshl_add_u64 v[24:25], s[8:9], 0, v[22:23]
	global_load_dwordx4 v[0:3], v[24:25], off offset:16 nt
	global_load_dwordx4 v[4:7], v[24:25], off nt
	global_load_dwordx4 v[8:11], v[24:25], off offset:2064 nt
	global_load_dwordx4 v[12:15], v[24:25], off offset:2048 nt
	v_and_b32_e32 v18, 15, v20
	s_add_u32 s13, s6, 0x2f100000
	v_lshlrev_b32_e32 v18, 2, v18
	v_lshlrev_b32_e32 v20, 2, v20
	s_addc_u32 s22, s7, 0
	v_lshl_add_u64 v[18:19], s[6:7], 0, v[18:19]
	s_mov_b64 s[6:7], 0x3f500000
	v_xor_b32_e32 v100, 4, v20
	v_xor_b32_e32 v101, 8, v20
	v_xor_b32_e32 v102, 16, v20
	v_xor_b32_e32 v103, 32, v20
	v_xor_b32_e32 v104, 64, v20
	v_xor_b32_e32 v105, 0x80, v20
	v_lshl_add_u64 v[20:21], v[16:17], 1, s[0:1]
	s_mov_b64 s[0:1], 0x3fd00000
	v_lshl_add_u64 v[18:19], v[18:19], 0, s[6:7]
	v_lshl_add_u64 v[20:21], v[20:21], 0, s[0:1]
	v_lshl_add_u64 v[22:23], s[4:5], 0, v[22:23]
	v_mov_b32_e32 v106, 0x358637bd
	s_mov_b32 s23, 0xf800000
	v_mov_b32_e32 v107, 0x260
	s_branch .LBB0_1049
.LBB0_1048:
	v_pk_mul_f32 v[88:89], v[84:85], v[84:85]
	v_pk_mul_f32 v[90:91], v[86:87], v[86:87]
	v_add_f32_e32 v88, v89, v88
	v_add_f32_e32 v88, v90, v88
	v_pk_mul_f32 v[92:93], v[82:83], v[82:83]
	v_add_f32_e32 v88, v91, v88
	v_add_f32_e32 v88, v92, v88
	v_pk_mul_f32 v[94:95], v[80:81], v[80:81]
	v_add_f32_e32 v88, v93, v88
	v_add_f32_e32 v88, v94, v88
	v_pk_mul_f32 v[96:97], v[76:77], v[76:77]
	v_add_f32_e32 v88, v95, v88
	v_add_f32_e32 v88, v96, v88
	v_pk_mul_f32 v[98:99], v[78:79], v[78:79]
	v_add_f32_e32 v88, v97, v88
	v_add_f32_e32 v88, v98, v88
	v_pk_mul_f32 v[108:109], v[72:73], v[72:73]
	v_add_f32_e32 v88, v99, v88
	v_add_f32_e32 v88, v108, v88
	v_pk_mul_f32 v[110:111], v[74:75], v[74:75]
	v_add_f32_e32 v88, v109, v88
	v_add_f32_e32 v88, v110, v88
	v_add_f32_e32 v88, v111, v88
	ds_bpermute_b32 v89, v100, v88
	v_pk_mul_f32 v[90:91], v[70:71], v[70:71]
	v_pk_mul_f32 v[94:95], v[64:65], v[64:65]
	v_pk_mul_f32 v[96:97], v[60:61], v[60:61]
	v_pk_mul_f32 v[98:99], v[62:63], v[62:63]
	s_waitcnt lgkmcnt(0)
	v_add_f32_e32 v88, v88, v89
	ds_bpermute_b32 v89, v101, v88
	v_pk_mul_f32 v[110:111], v[58:59], v[58:59]
	s_waitcnt lgkmcnt(0)
	v_add_f32_e32 v88, v88, v89
	ds_bpermute_b32 v89, v102, v88
	s_waitcnt lgkmcnt(0)
	v_add_f32_e32 v92, v88, v89
	ds_bpermute_b32 v93, v103, v92
	v_pk_mul_f32 v[88:89], v[68:69], v[68:69]
	s_waitcnt lgkmcnt(0)
	v_add_f32_e32 v108, v92, v93
	ds_bpermute_b32 v109, v104, v108
	v_add_f32_e32 v88, v89, v88
	v_add_f32_e32 v88, v90, v88
	v_pk_mul_f32 v[92:93], v[66:67], v[66:67]
	v_add_f32_e32 v88, v91, v88
	s_waitcnt lgkmcnt(0)
	v_add_f32_e32 v112, v108, v109
	ds_bpermute_b32 v113, v105, v112
	v_add_f32_e32 v88, v92, v88
	v_add_f32_e32 v88, v93, v88
	v_add_f32_e32 v88, v94, v88
	v_add_f32_e32 v88, v95, v88
	s_waitcnt lgkmcnt(0)
	v_add_f32_e32 v89, v112, v113
	v_fmamk_f32 v89, v89, 0x3a800000, v106
	v_mul_f32_e32 v90, 0x4f800000, v89
	v_cmp_gt_f32_e32 vcc, s23, v89
	v_add_f32_e32 v88, v96, v88
	v_add_f32_e32 v88, v97, v88
	v_cndmask_b32_e32 v89, v89, v90, vcc
	v_sqrt_f32_e32 v90, v89
	v_add_f32_e32 v88, v98, v88
	v_pk_mul_f32 v[108:109], v[56:57], v[56:57]
	v_add_f32_e32 v88, v99, v88
	v_add_u32_e32 v91, -1, v90
	v_add_u32_e32 v92, 1, v90
	v_fma_f32 v93, -v91, v90, v89
	v_fma_f32 v112, -v92, v90, v89
	v_cmp_ge_f32_e64 s[0:1], 0, v93
	v_add_f32_e32 v88, v108, v88
	v_add_f32_e32 v88, v109, v88
	v_cndmask_b32_e64 v90, v90, v91, s[0:1]
	v_cmp_lt_f32_e64 s[0:1], 0, v112
	v_add_f32_e32 v88, v110, v88
	v_add_f32_e32 v88, v111, v88
	v_cndmask_b32_e64 v90, v90, v92, s[0:1]
	v_mul_f32_e32 v91, 0x37800000, v90
	v_cndmask_b32_e32 v90, v90, v91, vcc
	v_cmp_class_f32_e32 vcc, v89, v107
	s_nop 1
	v_cndmask_b32_e32 v89, v90, v89, vcc
	v_div_scale_f32 v90, s[0:1], v89, v89, 1.0
	v_rcp_f32_e32 v91, v90
	v_div_scale_f32 v93, vcc, 1.0, v89, 1.0
	s_lshl_b64 s[0:1], s[2:3], 12
	v_fma_f32 v92, -v90, v91, 1.0
	v_fmac_f32_e32 v91, v92, v91
	ds_bpermute_b32 v92, v100, v88
	v_mul_f32_e32 v94, v93, v91
	v_fma_f32 v95, -v90, v94, v93
	v_fmac_f32_e32 v94, v95, v91
	s_waitcnt lgkmcnt(0)
	v_add_f32_e32 v92, v88, v92
	ds_bpermute_b32 v95, v101, v92
	v_fma_f32 v88, -v90, v94, v93
	v_div_fmas_f32 v88, v88, v91, v94
	v_div_fixup_f32 v88, v88, v89, 1.0
	v_lshl_add_u64 v[90:91], v[22:23], 0, s[0:1]
	s_waitcnt lgkmcnt(0)
	v_add_f32_e32 v89, v92, v95
	ds_bpermute_b32 v92, v102, v89
	v_pk_mul_f32 v[84:85], v[84:85], v[88:89] op_sel_hi:[1,0]
	v_pk_mul_f32 v[86:87], v[86:87], v[88:89] op_sel_hi:[1,0]
	v_pk_mul_f32 v[84:85], v[4:5], v[84:85]
	v_pk_mul_f32 v[86:87], v[6:7], v[86:87]
	s_waitcnt lgkmcnt(0)
	v_add_f32_e32 v89, v89, v92
	ds_bpermute_b32 v92, v103, v89
	global_store_dwordx4 v[90:91], v[84:87], off nt
	v_pk_mul_f32 v[80:81], v[80:81], v[88:89] op_sel_hi:[1,0]
	v_pk_mul_f32 v[76:77], v[76:77], v[88:89] op_sel_hi:[1,0]
	v_pk_mul_f32 v[84:85], v[82:83], v[88:89] op_sel_hi:[1,0]
	s_waitcnt lgkmcnt(0)
	v_add_f32_e32 v86, v89, v92
	ds_bpermute_b32 v87, v104, v86
	v_pk_mul_f32 v[82:83], v[2:3], v[80:81]
	v_pk_mul_f32 v[80:81], v[0:1], v[84:85]
	global_store_dwordx4 v[90:91], v[80:83], off offset:16 nt
	v_pk_mul_f32 v[78:79], v[78:79], v[88:89] op_sel_hi:[1,0]
	v_pk_mul_f32 v[76:77], v[12:13], v[76:77]
	s_waitcnt lgkmcnt(0)
	v_add_f32_e32 v80, v86, v87
	ds_bpermute_b32 v81, v105, v80
	v_pk_mul_f32 v[78:79], v[14:15], v[78:79]
	global_store_dwordx4 v[90:91], v[76:79], off offset:2048 nt
	v_pk_mul_f32 v[72:73], v[72:73], v[88:89] op_sel_hi:[1,0]
	v_pk_mul_f32 v[74:75], v[74:75], v[88:89] op_sel_hi:[1,0]
	s_waitcnt lgkmcnt(0)
	v_add_f32_e32 v80, v80, v81
	v_fmamk_f32 v80, v80, 0x3a800000, v106
	v_mul_f32_e32 v81, 0x4f800000, v80
	v_cmp_gt_f32_e32 vcc, s23, v80
	v_pk_mul_f32 v[74:75], v[10:11], v[74:75]
	v_pk_mul_f32 v[72:73], v[8:9], v[72:73]
	v_cndmask_b32_e32 v80, v80, v81, vcc
	v_sqrt_f32_e32 v81, v80
	global_store_dwordx4 v[90:91], v[72:75], off offset:2064 nt
	v_pk_mul_f32 v[82:83], v[46:47], v[46:47]
	v_pk_mul_f32 v[84:85], v[40:41], v[40:41]
	v_add_u32_e32 v76, -1, v81
	v_fma_f32 v77, -v76, v81, v80
	v_cmp_ge_f32_e64 s[0:1], 0, v77
	v_add_u32_e32 v77, 1, v81
	v_fma_f32 v78, -v77, v81, v80
	v_cndmask_b32_e64 v76, v81, v76, s[0:1]
	v_cmp_lt_f32_e64 s[0:1], 0, v78
	v_pk_mul_f32 v[74:75], v[54:55], v[54:55]
	v_pk_mul_f32 v[78:79], v[48:49], v[48:49]
	v_cndmask_b32_e64 v76, v76, v77, s[0:1]
	v_mul_f32_e32 v77, 0x37800000, v76
	v_cndmask_b32_e32 v76, v76, v77, vcc
	v_cmp_class_f32_e32 vcc, v80, v107
	v_pk_mul_f32 v[86:87], v[42:43], v[42:43]
	s_nop 0
	v_cndmask_b32_e32 v88, v76, v80, vcc
	v_div_scale_f32 v89, s[0:1], v88, v88, 1.0
	v_rcp_f32_e32 v92, v89
	v_pk_mul_f32 v[76:77], v[50:51], v[50:51]
	v_pk_mul_f32 v[80:81], v[44:45], v[44:45]
	s_lshl_b64 s[0:1], s[8:9], 12
	v_fma_f32 v72, -v89, v92, 1.0
	v_fmac_f32_e32 v92, v72, v92
	v_pk_mul_f32 v[72:73], v[52:53], v[52:53]
	s_nop 0
	v_add_f32_e32 v72, v73, v72
	v_add_f32_e32 v72, v74, v72
	v_add_f32_e32 v72, v75, v72
	v_add_f32_e32 v72, v76, v72
	v_add_f32_e32 v72, v77, v72
	v_add_f32_e32 v72, v78, v72
	v_add_f32_e32 v72, v79, v72
	v_add_f32_e32 v72, v80, v72
	v_add_f32_e32 v72, v81, v72
	v_add_f32_e32 v72, v82, v72
	v_add_f32_e32 v72, v83, v72
	v_add_f32_e32 v72, v84, v72
	v_add_f32_e32 v72, v85, v72
	v_add_f32_e32 v72, v86, v72
	v_add_f32_e32 v72, v87, v72
	ds_bpermute_b32 v73, v100, v72
	v_div_scale_f32 v74, vcc, 1.0, v88, 1.0
	v_mul_f32_e32 v75, v74, v92
	v_fma_f32 v76, -v89, v75, v74
	s_waitcnt lgkmcnt(0)
	v_add_f32_e32 v73, v72, v73
	v_fmac_f32_e32 v75, v76, v92
	ds_bpermute_b32 v76, v101, v73
	v_fma_f32 v72, -v89, v75, v74
	v_div_fmas_f32 v72, v72, v92, v75
	v_div_fixup_f32 v72, v72, v88, 1.0
	v_lshl_add_u64 v[74:75], v[22:23], 0, s[0:1]
	s_waitcnt lgkmcnt(0)
	v_add_f32_e32 v73, v73, v76
	ds_bpermute_b32 v76, v102, v73
	v_pk_mul_f32 v[68:69], v[68:69], v[72:73] op_sel_hi:[1,0]
	v_pk_mul_f32 v[70:71], v[70:71], v[72:73] op_sel_hi:[1,0]
	v_pk_mul_f32 v[68:69], v[4:5], v[68:69]
	v_pk_mul_f32 v[70:71], v[6:7], v[70:71]
	s_waitcnt lgkmcnt(0)
	v_add_f32_e32 v73, v73, v76
	ds_bpermute_b32 v76, v103, v73
	global_store_dwordx4 v[74:75], v[68:71], off nt
	v_pk_mul_f32 v[64:65], v[64:65], v[72:73] op_sel_hi:[1,0]
	v_pk_mul_f32 v[60:61], v[60:61], v[72:73] op_sel_hi:[1,0]
	v_pk_mul_f32 v[68:69], v[66:67], v[72:73] op_sel_hi:[1,0]
	s_waitcnt lgkmcnt(0)
	v_add_f32_e32 v70, v73, v76
	ds_bpermute_b32 v71, v104, v70
	v_pk_mul_f32 v[66:67], v[2:3], v[64:65]
	v_pk_mul_f32 v[64:65], v[0:1], v[68:69]
	global_store_dwordx4 v[74:75], v[64:67], off offset:16 nt
	v_pk_mul_f32 v[62:63], v[62:63], v[72:73] op_sel_hi:[1,0]
	v_pk_mul_f32 v[60:61], v[12:13], v[60:61]
	s_waitcnt lgkmcnt(0)
	v_add_f32_e32 v64, v70, v71
	ds_bpermute_b32 v65, v105, v64
	v_pk_mul_f32 v[62:63], v[14:15], v[62:63]
	global_store_dwordx4 v[74:75], v[60:63], off offset:2048 nt
	v_pk_mul_f32 v[56:57], v[56:57], v[72:73] op_sel_hi:[1,0]
	v_pk_mul_f32 v[58:59], v[58:59], v[72:73] op_sel_hi:[1,0]
	s_waitcnt lgkmcnt(0)
	v_add_f32_e32 v64, v64, v65
	v_fmamk_f32 v64, v64, 0x3a800000, v106
	v_mul_f32_e32 v65, 0x4f800000, v64
	v_cmp_gt_f32_e32 vcc, s23, v64
	v_pk_mul_f32 v[58:59], v[10:11], v[58:59]
	v_pk_mul_f32 v[56:57], v[8:9], v[56:57]
	v_cndmask_b32_e32 v64, v64, v65, vcc
	v_sqrt_f32_e32 v65, v64
	global_store_dwordx4 v[74:75], v[56:59], off offset:2064 nt
	v_pk_mul_f32 v[66:67], v[30:31], v[30:31]
	v_pk_mul_f32 v[68:69], v[24:25], v[24:25]
	v_add_u32_e32 v60, -1, v65
	v_fma_f32 v61, -v60, v65, v64
	v_cmp_ge_f32_e64 s[0:1], 0, v61
	v_add_u32_e32 v61, 1, v65
	v_fma_f32 v62, -v61, v65, v64
	v_cndmask_b32_e64 v60, v65, v60, s[0:1]
	v_cmp_lt_f32_e64 s[0:1], 0, v62
	v_pk_mul_f32 v[58:59], v[38:39], v[38:39]
	v_pk_mul_f32 v[62:63], v[34:35], v[34:35]
	v_cndmask_b32_e64 v60, v60, v61, s[0:1]
	v_mul_f32_e32 v61, 0x37800000, v60
	v_cndmask_b32_e32 v60, v60, v61, vcc
	v_cmp_class_f32_e32 vcc, v64, v107
	v_pk_mul_f32 v[70:71], v[26:27], v[26:27]
	s_nop 0
	v_cndmask_b32_e32 v72, v60, v64, vcc
	v_div_scale_f32 v73, s[0:1], v72, v72, 1.0
	v_rcp_f32_e32 v76, v73
	v_pk_mul_f32 v[60:61], v[32:33], v[32:33]
	v_pk_mul_f32 v[64:65], v[28:29], v[28:29]
	s_lshl_b64 s[0:1], s[6:7], 12
	v_fma_f32 v56, -v73, v76, 1.0
	v_fmac_f32_e32 v76, v56, v76
	v_pk_mul_f32 v[56:57], v[36:37], v[36:37]
	s_nop 0
	v_add_f32_e32 v56, v56, v57
	v_add_f32_e32 v56, v56, v58
	v_add_f32_e32 v56, v56, v59
	v_add_f32_e32 v56, v56, v60
	v_add_f32_e32 v56, v56, v61
	v_add_f32_e32 v56, v56, v62
	v_add_f32_e32 v56, v56, v63
	v_add_f32_e32 v56, v56, v64
	v_add_f32_e32 v56, v56, v65
	v_add_f32_e32 v56, v56, v66
	v_add_f32_e32 v56, v56, v67
	v_add_f32_e32 v56, v56, v68
	v_add_f32_e32 v56, v56, v69
	v_add_f32_e32 v56, v56, v70
	v_add_f32_e32 v56, v56, v71
	ds_bpermute_b32 v57, v100, v56
	v_div_scale_f32 v58, vcc, 1.0, v72, 1.0
	v_mul_f32_e32 v59, v58, v76
	v_fma_f32 v60, -v73, v59, v58
	s_waitcnt lgkmcnt(0)
	v_add_f32_e32 v57, v56, v57
	v_fmac_f32_e32 v59, v60, v76
	ds_bpermute_b32 v60, v101, v57
	v_fma_f32 v56, -v73, v59, v58
	v_div_fmas_f32 v56, v56, v76, v59
	v_div_fixup_f32 v56, v56, v72, 1.0
	v_lshl_add_u64 v[58:59], v[22:23], 0, s[0:1]
	s_waitcnt lgkmcnt(0)
	v_add_f32_e32 v57, v57, v60
	ds_bpermute_b32 v60, v102, v57
	v_pk_mul_f32 v[52:53], v[52:53], v[56:57] op_sel_hi:[1,0]
	v_pk_mul_f32 v[54:55], v[54:55], v[56:57] op_sel_hi:[1,0]
	v_pk_mul_f32 v[52:53], v[4:5], v[52:53]
	v_pk_mul_f32 v[54:55], v[6:7], v[54:55]
	s_waitcnt lgkmcnt(0)
	v_add_f32_e32 v57, v57, v60
	ds_bpermute_b32 v60, v103, v57
	global_store_dwordx4 v[58:59], v[52:55], off nt
	v_pk_mul_f32 v[48:49], v[48:49], v[56:57] op_sel_hi:[1,0]
	v_pk_mul_f32 v[44:45], v[44:45], v[56:57] op_sel_hi:[1,0]
	v_pk_mul_f32 v[52:53], v[50:51], v[56:57] op_sel_hi:[1,0]
	s_waitcnt lgkmcnt(0)
	v_add_f32_e32 v54, v57, v60
	ds_bpermute_b32 v55, v104, v54
	v_pk_mul_f32 v[50:51], v[2:3], v[48:49]
	v_pk_mul_f32 v[48:49], v[0:1], v[52:53]
	global_store_dwordx4 v[58:59], v[48:51], off offset:16 nt
	v_pk_mul_f32 v[46:47], v[46:47], v[56:57] op_sel_hi:[1,0]
	v_pk_mul_f32 v[44:45], v[12:13], v[44:45]
	s_waitcnt lgkmcnt(0)
	v_add_f32_e32 v48, v54, v55
	ds_bpermute_b32 v49, v105, v48
	v_pk_mul_f32 v[46:47], v[14:15], v[46:47]
	global_store_dwordx4 v[58:59], v[44:47], off offset:2048 nt
	v_pk_mul_f32 v[40:41], v[40:41], v[56:57] op_sel_hi:[1,0]
	v_pk_mul_f32 v[42:43], v[42:43], v[56:57] op_sel_hi:[1,0]
	s_waitcnt lgkmcnt(0)
	v_add_f32_e32 v48, v48, v49
	v_fmamk_f32 v48, v48, 0x3a800000, v106
	v_mul_f32_e32 v49, 0x4f800000, v48
	v_cmp_gt_f32_e32 vcc, s23, v48
	v_pk_mul_f32 v[42:43], v[10:11], v[42:43]
	v_pk_mul_f32 v[40:41], v[8:9], v[40:41]
	v_cndmask_b32_e32 v48, v48, v49, vcc
	v_sqrt_f32_e32 v49, v48
	global_store_dwordx4 v[58:59], v[40:43], off offset:2064 nt
	v_add_u32_e32 v44, -1, v49
	v_fma_f32 v45, -v44, v49, v48
	v_cmp_ge_f32_e64 s[0:1], 0, v45
	v_add_u32_e32 v45, 1, v49
	v_fma_f32 v46, -v45, v49, v48
	v_cndmask_b32_e64 v44, v49, v44, s[0:1]
	v_cmp_lt_f32_e64 s[0:1], 0, v46
	s_nop 1
	v_cndmask_b32_e64 v44, v44, v45, s[0:1]
	v_mul_f32_e32 v45, 0x37800000, v44
	v_cndmask_b32_e32 v44, v44, v45, vcc
	v_cmp_class_f32_e32 vcc, v48, v107
	s_nop 1
	v_cndmask_b32_e32 v44, v44, v48, vcc
	v_div_scale_f32 v45, s[0:1], v44, v44, 1.0
	v_rcp_f32_e32 v46, v45
	s_lshl_b64 s[0:1], s[4:5], 12
	v_fma_f32 v40, -v45, v46, 1.0
	v_fmac_f32_e32 v46, v40, v46
	v_div_scale_f32 v40, vcc, 1.0, v44, 1.0
	v_mul_f32_e32 v41, v40, v46
	v_fma_f32 v42, -v45, v41, v40
	v_fmac_f32_e32 v41, v42, v46
	v_fma_f32 v40, -v45, v41, v40
	v_div_fmas_f32 v40, v40, v46, v41
	v_div_fixup_f32 v40, v40, v44, 1.0
	v_lshl_add_u64 v[42:43], v[22:23], 0, s[0:1]
	v_pk_mul_f32 v[36:37], v[36:37], v[40:41] op_sel_hi:[1,0]
	v_pk_mul_f32 v[38:39], v[38:39], v[40:41] op_sel_hi:[1,0]
	v_pk_mul_f32 v[32:33], v[32:33], v[40:41] op_sel_hi:[1,0]
	v_pk_mul_f32 v[34:35], v[34:35], v[40:41] op_sel_hi:[1,0]
	v_pk_mul_f32 v[28:29], v[28:29], v[40:41] op_sel_hi:[1,0]
	v_pk_mul_f32 v[30:31], v[30:31], v[40:41] op_sel_hi:[1,0]
	v_pk_mul_f32 v[24:25], v[24:25], v[40:41] op_sel_hi:[1,0]
	v_pk_mul_f32 v[26:27], v[26:27], v[40:41] op_sel_hi:[1,0]
	s_add_i32 s0, s2, 0x2000
	v_pk_mul_f32 v[38:39], v[6:7], v[38:39]
	v_pk_mul_f32 v[36:37], v[4:5], v[36:37]
	v_pk_mul_f32 v[34:35], v[2:3], v[34:35]
	v_pk_mul_f32 v[32:33], v[0:1], v[32:33]
	v_pk_mul_f32 v[30:31], v[14:15], v[30:31]
	v_pk_mul_f32 v[28:29], v[12:13], v[28:29]
	v_pk_mul_f32 v[26:27], v[10:11], v[26:27]
	v_pk_mul_f32 v[24:25], v[8:9], v[24:25]
	s_cmp_lt_i32 s2, 0xe000
	s_mov_b32 s2, s0
	global_store_dwordx4 v[42:43], v[36:39], off nt
	global_store_dwordx4 v[42:43], v[32:35], off offset:16 nt
	global_store_dwordx4 v[42:43], v[28:31], off offset:2048 nt
	global_store_dwordx4 v[42:43], v[24:27], off offset:2064 nt
	s_cbranch_scc0 .LBB0_1060
.LBB0_1049:
	s_ashr_i32 s3, s2, 31
	s_add_i32 s8, s2, 0x800
	s_lshl_b64 s[0:1], s[2:3], 11
	s_ashr_i32 s9, s8, 31
	s_add_i32 s6, s2, 0x1000
	v_lshl_add_u64 v[32:33], v[20:21], 0, s[0:1]
	s_lshl_b64 s[0:1], s[8:9], 11
	s_ashr_i32 s7, s6, 31
	s_add_i32 s4, s2, 0x1800
	v_lshl_add_u64 v[40:41], v[20:21], 0, s[0:1]
	s_lshl_b64 s[0:1], s[6:7], 11
	s_ashr_i32 s5, s4, 31
	v_lshl_add_u64 v[44:45], v[20:21], 0, s[0:1]
	s_lshl_b64 s[0:1], s[4:5], 11
	global_load_dwordx4 v[24:27], v[32:33], off nt
	global_load_dwordx4 v[28:31], v[32:33], off offset:1024 nt
	s_nop 0
	global_load_dwordx4 v[32:35], v[40:41], off nt
	global_load_dwordx4 v[36:39], v[40:41], off offset:1024 nt
	s_nop 0
	global_load_dwordx4 v[40:43], v[44:45], off nt
	global_load_dwordx4 v[88:91], v[44:45], off offset:1024 nt
	v_lshl_add_u64 v[44:45], v[20:21], 0, s[0:1]
	s_lshl_b64 s[0:1], s[2:3], 6
	global_load_dwordx4 v[92:95], v[44:45], off nt
	global_load_dwordx4 v[96:99], v[44:45], off offset:1024 nt
	v_lshl_add_u64 v[44:45], v[18:19], 0, s[0:1]
	s_lshl_b64 s[0:1], s[8:9], 6
	s_lshl_b64 s[10:11], s[6:7], 6
	global_load_dword v108, v[44:45], off nt
	v_lshl_add_u64 v[44:45], v[18:19], 0, s[0:1]
	s_lshl_b64 s[14:15], s[4:5], 6
	global_load_dword v109, v[44:45], off nt
	v_lshl_add_u64 v[44:45], v[18:19], 0, s[10:11]
	global_load_dword v110, v[44:45], off nt
	v_lshl_add_u64 v[44:45], v[18:19], 0, s[14:15]
	global_load_dword v111, v[44:45], off nt
	s_waitcnt vmcnt(11)
	v_and_b32_e32 v85, 0xffff0000, v24
	v_lshlrev_b32_e32 v84, 16, v24
	v_and_b32_e32 v87, 0xffff0000, v25
	v_lshlrev_b32_e32 v86, 16, v25
	v_and_b32_e32 v83, 0xffff0000, v26
	v_lshlrev_b32_e32 v82, 16, v26
	v_and_b32_e32 v81, 0xffff0000, v27
	v_lshlrev_b32_e32 v80, 16, v27
	s_waitcnt vmcnt(10)
	v_and_b32_e32 v77, 0xffff0000, v28
	v_lshlrev_b32_e32 v76, 16, v28
	s_waitcnt vmcnt(3)
	v_cmp_lt_i32_e32 vcc, -1, v108
	s_and_b32 s1, vcc_lo, 0xffff
	v_and_b32_e32 v79, 0xffff0000, v29
	s_waitcnt vmcnt(2)
	v_cmp_lt_i32_e32 vcc, -1, v109
	s_and_b32 s24, vcc_lo, 0xffff
	s_waitcnt vmcnt(1)
	v_cmp_lt_i32_e32 vcc, -1, v110
	s_and_b32 s25, vcc_lo, 0xffff
	s_waitcnt vmcnt(0)
	v_cmp_lt_i32_e32 vcc, -1, v111
	s_or_b32 s0, s24, s1
	s_and_b32 s26, vcc_lo, 0xffff
	s_or_b32 s0, s0, s25
	s_or_b32 s0, s0, s26
	v_lshlrev_b32_e32 v78, 16, v29
	v_and_b32_e32 v73, 0xffff0000, v30
	v_lshlrev_b32_e32 v72, 16, v30
	v_and_b32_e32 v75, 0xffff0000, v31
	v_lshlrev_b32_e32 v74, 16, v31
	v_and_b32_e32 v69, 0xffff0000, v32
	v_lshlrev_b32_e32 v68, 16, v32
	v_and_b32_e32 v71, 0xffff0000, v33
	v_lshlrev_b32_e32 v70, 16, v33
	v_and_b32_e32 v67, 0xffff0000, v34
	v_lshlrev_b32_e32 v66, 16, v34
	v_and_b32_e32 v65, 0xffff0000, v35
	v_lshlrev_b32_e32 v64, 16, v35
	v_and_b32_e32 v61, 0xffff0000, v36
	v_lshlrev_b32_e32 v60, 16, v36
	v_and_b32_e32 v63, 0xffff0000, v37
	v_lshlrev_b32_e32 v62, 16, v37
	v_and_b32_e32 v57, 0xffff0000, v38
	v_lshlrev_b32_e32 v56, 16, v38
	v_and_b32_e32 v59, 0xffff0000, v39
	v_lshlrev_b32_e32 v58, 16, v39
	v_and_b32_e32 v53, 0xffff0000, v40
	v_lshlrev_b32_e32 v52, 16, v40
	v_and_b32_e32 v55, 0xffff0000, v41
	v_lshlrev_b32_e32 v54, 16, v41
	v_and_b32_e32 v51, 0xffff0000, v42
	v_lshlrev_b32_e32 v50, 16, v42
	v_and_b32_e32 v49, 0xffff0000, v43
	v_lshlrev_b32_e32 v48, 16, v43
	v_and_b32_e32 v45, 0xffff0000, v88
	v_lshlrev_b32_e32 v44, 16, v88
	v_and_b32_e32 v47, 0xffff0000, v89
	v_lshlrev_b32_e32 v46, 16, v89
	v_and_b32_e32 v41, 0xffff0000, v90
	v_lshlrev_b32_e32 v40, 16, v90
	v_and_b32_e32 v43, 0xffff0000, v91
	v_lshlrev_b32_e32 v42, 16, v91
	v_lshlrev_b32_e32 v36, 16, v92
	v_and_b32_e32 v37, 0xffff0000, v92
	v_lshlrev_b32_e32 v38, 16, v93
	v_and_b32_e32 v39, 0xffff0000, v93
	v_lshlrev_b32_e32 v32, 16, v94
	v_and_b32_e32 v33, 0xffff0000, v94
	v_lshlrev_b32_e32 v34, 16, v95
	v_and_b32_e32 v35, 0xffff0000, v95
	v_lshlrev_b32_e32 v28, 16, v96
	v_and_b32_e32 v29, 0xffff0000, v96
	v_lshlrev_b32_e32 v30, 16, v97
	v_and_b32_e32 v31, 0xffff0000, v97
	v_lshlrev_b32_e32 v24, 16, v98
	v_and_b32_e32 v25, 0xffff0000, v98
	v_lshlrev_b32_e32 v26, 16, v99
	s_cmp_eq_u32 s0, 0
	v_and_b32_e32 v27, 0xffff0000, v99
	s_cbranch_scc1 .LBB0_1048
	s_ashr_i32 s27, s2, 11
	s_ashr_i32 s28, s8, 11
	s_ashr_i32 s29, s6, 11
	s_ashr_i32 s30, s4, 11
	s_branch .LBB0_1052
.LBB0_1051:
	s_add_i32 s15, s25, -1
	s_and_b32 s25, s15, s25
	s_add_i32 s15, s24, -1
	s_and_b32 s24, s15, s24
	s_add_i32 s15, s1, -1
	s_and_b32 s1, s15, s1
	s_lshl_b32 s11, s11, 5
	s_and_b64 s[18:19], exec, s[18:19]
	s_cselect_b32 s11, 0, s11
	s_add_i32 s18, s11, s30
	s_ashr_i32 s19, s18, 31
	s_lshl_b64 s[18:19], s[18:19], 18
	s_add_u32 s11, s13, s18
	s_addc_u32 s15, s22, s19
	s_add_u32 s16, s11, s16
	s_addc_u32 s17, s15, s17
	v_lshl_add_u64 v[112:113], s[16:17], 0, v[16:17]
	global_load_dwordx2 v[114:115], v[112:113], off nt
	global_load_dwordx2 v[116:117], v[112:113], off offset:512 nt
	s_waitcnt vmcnt(7)
	v_cvt_pk_f32_fp8_e32 v[112:113], v92
	v_cvt_pk_f32_fp8_sdwa v[118:119], v92 src0_sel:WORD_1
	v_cvt_pk_f32_fp8_e32 v[120:121], v93
	v_cvt_pk_f32_fp8_sdwa v[92:93], v93 src0_sel:WORD_1
	v_pk_fma_f32 v[84:85], s[12:13], v[112:113], v[84:85] op_sel_hi:[0,1,1]
	v_pk_fma_f32 v[86:87], s[12:13], v[118:119], v[86:87] op_sel_hi:[0,1,1]
	s_waitcnt vmcnt(6)
	v_cvt_pk_f32_fp8_sdwa v[112:113], v88 src0_sel:WORD_1
	v_pk_fma_f32 v[80:81], s[12:13], v[92:93], v[80:81] op_sel_hi:[0,1,1]
	v_cvt_pk_f32_fp8_e32 v[92:93], v88
	v_cvt_pk_f32_fp8_e32 v[118:119], v89
	v_cvt_pk_f32_fp8_sdwa v[88:89], v89 src0_sel:WORD_1
	v_pk_fma_f32 v[78:79], s[12:13], v[112:113], v[78:79] op_sel_hi:[0,1,1]
	v_pk_fma_f32 v[76:77], s[12:13], v[92:93], v[76:77] op_sel_hi:[0,1,1]
	s_waitcnt vmcnt(5)
	v_cvt_pk_f32_fp8_sdwa v[92:93], v96 src0_sel:WORD_1
	v_pk_fma_f32 v[74:75], s[12:13], v[88:89], v[74:75] op_sel_hi:[0,1,1]
	v_cvt_pk_f32_fp8_e32 v[88:89], v96
	v_cvt_pk_f32_fp8_e32 v[112:113], v97
	v_cvt_pk_f32_fp8_sdwa v[96:97], v97 src0_sel:WORD_1
	v_pk_fma_f32 v[70:71], s[0:1], v[92:93], v[70:71] op_sel_hi:[0,1,1]
	v_pk_fma_f32 v[68:69], s[0:1], v[88:89], v[68:69] op_sel_hi:[0,1,1]
	s_waitcnt vmcnt(4)
	v_cvt_pk_f32_fp8_e32 v[88:89], v90
	v_pk_fma_f32 v[64:65], s[0:1], v[96:97], v[64:65] op_sel_hi:[0,1,1]
	v_cvt_pk_f32_fp8_sdwa v[92:93], v90 src0_sel:WORD_1
	v_cvt_pk_f32_fp8_e32 v[96:97], v91
	v_cvt_pk_f32_fp8_sdwa v[90:91], v91 src0_sel:WORD_1
	v_pk_fma_f32 v[60:61], s[0:1], v[88:89], v[60:61] op_sel_hi:[0,1,1]
	v_pk_fma_f32 v[62:63], s[0:1], v[92:93], v[62:63] op_sel_hi:[0,1,1]
	s_waitcnt vmcnt(3)
	v_cvt_pk_f32_fp8_e32 v[88:89], v98
	v_pk_fma_f32 v[58:59], s[0:1], v[90:91], v[58:59] op_sel_hi:[0,1,1]
	v_cvt_pk_f32_fp8_sdwa v[90:91], v98 src0_sel:WORD_1
	v_cvt_pk_f32_fp8_e32 v[92:93], v99
	v_pk_fma_f32 v[52:53], s[14:15], v[88:89], v[52:53] op_sel_hi:[0,1,1]
	s_waitcnt vmcnt(2)
	v_cvt_pk_f32_fp8_e32 v[88:89], v94
	v_pk_fma_f32 v[54:55], s[14:15], v[90:91], v[54:55] op_sel_hi:[0,1,1]
	v_pk_fma_f32 v[50:51], s[14:15], v[92:93], v[50:51] op_sel_hi:[0,1,1]
	v_cvt_pk_f32_fp8_sdwa v[90:91], v94 src0_sel:WORD_1
	v_cvt_pk_f32_fp8_e32 v[92:93], v95
	v_cvt_pk_f32_fp8_sdwa v[94:95], v95 src0_sel:WORD_1
	v_pk_fma_f32 v[44:45], s[14:15], v[88:89], v[44:45] op_sel_hi:[0,1,1]
	v_pk_fma_f32 v[46:47], s[14:15], v[90:91], v[46:47] op_sel_hi:[0,1,1]
	v_pk_fma_f32 v[40:41], s[14:15], v[92:93], v[40:41] op_sel_hi:[0,1,1]
	v_pk_fma_f32 v[42:43], s[14:15], v[94:95], v[42:43] op_sel_hi:[0,1,1]
	s_add_i32 s11, s26, -1
	s_and_b32 s26, s11, s26
	v_pk_fma_f32 v[56:57], s[0:1], v[96:97], v[56:57] op_sel_hi:[0,1,1]
	v_cvt_pk_f32_fp8_sdwa v[96:97], v99 src0_sel:WORD_1
	v_pk_fma_f32 v[66:67], s[0:1], v[112:113], v[66:67] op_sel_hi:[0,1,1]
	s_or_b32 s0, s25, s26
	s_or_b32 s0, s0, s24
	s_or_b32 s0, s0, s1
	v_pk_fma_f32 v[82:83], s[12:13], v[120:121], v[82:83] op_sel_hi:[0,1,1]
	v_pk_fma_f32 v[72:73], s[12:13], v[118:119], v[72:73] op_sel_hi:[0,1,1]
	v_pk_fma_f32 v[48:49], s[14:15], v[96:97], v[48:49] op_sel_hi:[0,1,1]
	s_cmp_lg_u32 s0, 0
	s_waitcnt vmcnt(1)
	v_cvt_pk_f32_fp8_e32 v[88:89], v114
	v_cvt_pk_f32_fp8_sdwa v[90:91], v114 src0_sel:WORD_1
	v_cvt_pk_f32_fp8_e32 v[92:93], v115
	v_cvt_pk_f32_fp8_sdwa v[94:95], v115 src0_sel:WORD_1
	v_pk_fma_f32 v[36:37], s[10:11], v[88:89], v[36:37] op_sel_hi:[0,1,1]
	v_pk_fma_f32 v[38:39], s[10:11], v[90:91], v[38:39] op_sel_hi:[0,1,1]
	v_pk_fma_f32 v[32:33], s[10:11], v[92:93], v[32:33] op_sel_hi:[0,1,1]
	v_pk_fma_f32 v[34:35], s[10:11], v[94:95], v[34:35] op_sel_hi:[0,1,1]
	s_waitcnt vmcnt(0)
	v_cvt_pk_f32_fp8_e32 v[88:89], v116
	v_cvt_pk_f32_fp8_sdwa v[90:91], v116 src0_sel:WORD_1
	v_cvt_pk_f32_fp8_e32 v[92:93], v117
	v_cvt_pk_f32_fp8_sdwa v[94:95], v117 src0_sel:WORD_1
	v_pk_fma_f32 v[28:29], s[10:11], v[88:89], v[28:29] op_sel_hi:[0,1,1]
	v_pk_fma_f32 v[30:31], s[10:11], v[90:91], v[30:31] op_sel_hi:[0,1,1]
	v_pk_fma_f32 v[24:25], s[10:11], v[92:93], v[24:25] op_sel_hi:[0,1,1]
	v_pk_fma_f32 v[26:27], s[10:11], v[94:95], v[26:27] op_sel_hi:[0,1,1]
	s_cbranch_scc0 .LBB0_1048

.LBB0_1054:
	s_lshl_b32 s18, s18, 5
	s_and_b64 s[14:15], exec, s[14:15]
	s_cselect_b32 s14, 0, s18
	s_add_i32 s14, s14, s27
	s_ashr_i32 s15, s14, 31
	s_lshl_b64 s[14:15], s[14:15], 18
	s_add_u32 s14, s13, s14
	s_addc_u32 s15, s22, s15
	s_add_u32 s14, s14, s16
	s_addc_u32 s15, s15, s17
	v_lshl_add_u64 v[90:91], s[14:15], 0, v[16:17]
	global_load_dwordx2 v[92:93], v[90:91], off nt
	global_load_dwordx2 v[88:89], v[90:91], off offset:512 nt
	s_cmp_eq_u32 s24, 0
	s_cselect_b64 s[14:15], -1, 0
	s_ff1_i32_b32 s16, s24
	s_and_b64 vcc, exec, s[14:15]
	s_cbranch_vccnz .LBB0_1056
	v_readlane_b32 s10, v109, s16
	s_ashr_i32 s11, s10, 31
	s_lshl_b64 s[10:11], s[10:11], 10
	s_brev_b32 s0, 60
.LBB0_1056:
	s_lshl_b32 s16, s16, 5
	s_and_b64 s[14:15], exec, s[14:15]
	s_cselect_b32 s14, 0, s16
	s_add_i32 s14, s14, s28
	s_ashr_i32 s15, s14, 31
	s_lshl_b64 s[14:15], s[14:15], 18
	s_add_u32 s14, s13, s14
	s_addc_u32 s15, s22, s15
	s_add_u32 s10, s14, s10
	s_addc_u32 s11, s15, s11
	v_lshl_add_u64 v[94:95], s[10:11], 0, v[16:17]
	global_load_dwordx2 v[96:97], v[94:95], off nt
	global_load_dwordx2 v[90:91], v[94:95], off offset:512 nt
	s_cmp_eq_u32 s25, 0
	s_cselect_b64 s[18:19], -1, 0
	s_ff1_i32_b32 s11, s25
	s_mov_b64 s[16:17], 0
	s_mov_b32 s10, 0
	s_and_b64 vcc, exec, s[18:19]
	s_mov_b32 s14, 0
	s_mov_b64 s[20:21], 0
	s_cbranch_vccnz .LBB0_1058
	v_readlane_b32 s14, v110, s11
	s_ashr_i32 s15, s14, 31
	s_lshl_b64 s[20:21], s[14:15], 10
	s_brev_b32 s14, 60
.LBB0_1058:
	s_lshl_b32 s11, s11, 5
	s_and_b64 s[18:19], exec, s[18:19]
	s_cselect_b32 s11, 0, s11
	s_add_i32 s18, s11, s29
	s_ashr_i32 s19, s18, 31
	s_lshl_b64 s[18:19], s[18:19], 18
	s_add_u32 s11, s13, s18
	s_addc_u32 s15, s22, s19
	s_add_u32 s18, s11, s20
	s_addc_u32 s19, s15, s21
	v_lshl_add_u64 v[112:113], s[18:19], 0, v[16:17]
	global_load_dwordx2 v[98:99], v[112:113], off nt
	global_load_dwordx2 v[94:95], v[112:113], off offset:512 nt
	s_cmp_eq_u32 s26, 0
	s_cselect_b64 s[18:19], -1, 0
	s_ff1_i32_b32 s11, s26
	s_and_b64 vcc, exec, s[18:19]
	s_cbranch_vccnz .LBB0_1051
	v_readlane_b32 s16, v111, s11
	s_ashr_i32 s17, s16, 31
	s_lshl_b64 s[16:17], s[16:17], 10
	s_brev_b32 s10, 60
	s_branch .LBB0_1051
